# P12 combine: expert-row loads rolling across trips (next trip's item requested as soon as the item's registers are free)
# baseline (speedup 1.0000x reference)
; __global__ void __launch_bounds__(512, 2) fwd_kernel(Params p) {
;     ...
;         moe_tables(ctl + CW_CNT, ts, tid);
;         constexpr int NI = T * (DM / 16), UN = 4;
;         for (int it0 = GT(); it0 < NI; it0 += UN * NGT) {
;             int mm[UN], cc[UN], ee[UN][4], rk[UN][4]; u32x4 xa[UN], xb[UN], y[UN][4];
; #pragma unroll
;             for (int u = 0; u < UN; ++u) { const int it = it0 + u * NGT < NI ? it0 + u * NGT : it0; mm[u] = it >> 7; cc[u] = (it & 127) * 16;
;                 const i32x4 e4 = *(const i32x4*)(tok_e + mm[u] * 4), r4 = *(const i32x4*)(tok_rank + mm[u] * 4);
; #pragma unroll
;                 for (int k = 0; k < 4; ++k) { ee[u][k] = e4[k]; rk[u][k] = r4[k]; }
;                 const bf16_t* xp = X1 + (size_t)mm[u] * DM + cc[u]; xa[u] = *(const u32x4*)xp; xb[u] = *(const u32x4*)(xp + 8); }
; #pragma unroll
;             for (int u = 0; u < UN; ++u)
; #pragma unroll
;                 for (int k = 0; k < 4; ++k) { const int pos = ts[ee[u][k]] * 256 + rk[u][k]; y[u][k] = *(const u32x4*)(Yb + (size_t)pos * DM + cc[u]); }
.LBB0_1194:
	s_or_b64 exec, exec, s[2:3]
	s_waitcnt lgkmcnt(0)
	s_barrier
	v_mbcnt_lo_u32_b32 v0, -1, 0
	v_mbcnt_hi_u32_b32 v0, -1, v0
	v_readlane_b32 s0, v252, 3
	s_nop 1
	v_add_u32_e32 v0, s0, v0
	v_readlane_b32 s0, v252, 7
	s_mov_b32 s11, 0x200000
	s_waitcnt vmcnt(9) lgkmcnt(0)
	v_add_u32_e32 v88, s0, v0
	v_cmp_gt_i32_e32 vcc, s11, v88
	s_barrier
	s_and_saveexec_b64 s[0:1], vcc
	s_cbranch_execz .LBB0_1207
	s_cmpk_lg_i32 s33, 0x100
	s_cbranch_scc1 .Lp12n_orig
	s_load_dwordx2 s[4:5], s[88:89], 0xb0
	s_mov_b32 s10, 0x3d800000
	s_mov_b32 s11, 0x3d800000
	s_add_i32 s23, 0, 0x25100
	v_and_b32_e32 v1, 63, v0
	v_bfe_u32 v2, v88, 6, 1
	v_lshrrev_b32_e32 v3, 7, v88
	v_lshlrev_b32_e32 v4, 2, v1
	v_lshl_or_b32 v4, v2, 10, v4
	v_lshlrev_b32_e32 v5, 3, v1
	v_lshl_or_b32 v5, v2, 11, v5
	v_lshlrev_b32_e32 v6, 4, v1
	v_lshl_or_b32 v6, v2, 12, v6
	v_mov_b32_e32 v192, v3
	v_lshlrev_b32_e32 v196, 4, v192
	v_lshl_add_u32 v156, v192, 13, v6
	v_add_u32_e32 v193, 0x400, v3
	v_lshlrev_b32_e32 v197, 4, v193
	v_lshl_add_u32 v157, v193, 13, v6
	v_add_u32_e32 v194, 0x800, v3
	v_lshlrev_b32_e32 v198, 4, v194
	v_lshl_add_u32 v158, v194, 13, v6
	v_add_u32_e32 v195, 0xc00, v3
	v_lshlrev_b32_e32 v199, 4, v195
	v_lshl_add_u32 v159, v195, 13, v6
	global_load_dwordx4 v[8:11], v196, s[16:17]
	global_load_dwordx4 v[12:15], v197, s[16:17]
	global_load_dwordx4 v[16:19], v198, s[16:17]
	global_load_dwordx4 v[20:23], v199, s[16:17]
	global_load_dwordx4 v[24:27], v196, s[18:19]
	global_load_dwordx4 v[28:31], v197, s[18:19]
	global_load_dwordx4 v[32:35], v198, s[18:19]
	global_load_dwordx4 v[36:39], v199, s[18:19]
	v_lshl_add_u32 v196, v192, 12, v5
	global_load_dwordx2 v[40:41], v196, s[14:15]
	global_load_dwordx2 v[42:43], v196, s[14:15] offset:512
	global_load_dwordx2 v[44:45], v196, s[14:15] offset:1024
	global_load_dwordx2 v[46:47], v196, s[14:15] offset:1536
	v_lshl_add_u32 v197, v193, 12, v5
	global_load_dwordx2 v[48:49], v197, s[14:15]
	global_load_dwordx2 v[50:51], v197, s[14:15] offset:512
	global_load_dwordx2 v[52:53], v197, s[14:15] offset:1024
	global_load_dwordx2 v[54:55], v197, s[14:15] offset:1536
	v_lshl_add_u32 v198, v194, 12, v5
	global_load_dwordx2 v[56:57], v198, s[14:15]
	global_load_dwordx2 v[58:59], v198, s[14:15] offset:512
	global_load_dwordx2 v[60:61], v198, s[14:15] offset:1024
	global_load_dwordx2 v[62:63], v198, s[14:15] offset:1536
	v_lshl_add_u32 v199, v195, 12, v5
	global_load_dwordx2 v[64:65], v199, s[14:15]
	global_load_dwordx2 v[66:67], v199, s[14:15] offset:512
	global_load_dwordx2 v[68:69], v199, s[14:15] offset:1024
	global_load_dwordx2 v[70:71], v199, s[14:15] offset:1536
	s_waitcnt lgkmcnt(0)
	s_waitcnt vmcnt(16)
	v_lshl_add_u32 v200, v8, 2, s23
	v_lshl_add_u32 v201, v9, 2, s23
	v_lshl_add_u32 v202, v10, 2, s23
	v_lshl_add_u32 v203, v11, 2, s23
	ds_read_b32 v136, v200
	ds_read_b32 v137, v201
	ds_read_b32 v138, v202
	ds_read_b32 v139, v203
	s_waitcnt lgkmcnt(0)
	v_lshl_add_u32 v136, v136, 8, v24
	v_lshl_add_u32 v137, v137, 8, v25
	v_lshl_add_u32 v138, v138, 8, v26
	v_lshl_add_u32 v139, v139, 8, v27
	v_lshl_add_u32 v136, v136, 11, v4
	v_lshl_add_u32 v137, v137, 11, v4
	v_lshl_add_u32 v138, v138, 11, v4
	v_lshl_add_u32 v139, v139, 11, v4
	global_load_dword v72, v136, s[6:7]
	global_load_dword v73, v136, s[6:7] offset:256
	global_load_dword v74, v136, s[6:7] offset:512
	global_load_dword v75, v136, s[6:7] offset:768
	global_load_dword v76, v137, s[6:7]
	global_load_dword v77, v137, s[6:7] offset:256
	global_load_dword v78, v137, s[6:7] offset:512
	global_load_dword v79, v137, s[6:7] offset:768
	global_load_dword v80, v138, s[6:7]
	global_load_dword v81, v138, s[6:7] offset:256
	global_load_dword v82, v138, s[6:7] offset:512
	global_load_dword v83, v138, s[6:7] offset:768
	global_load_dword v84, v139, s[6:7]
	global_load_dword v85, v139, s[6:7] offset:256
	global_load_dword v86, v139, s[6:7] offset:512
	global_load_dword v87, v139, s[6:7] offset:768
	v_lshl_add_u32 v200, v12, 2, s23
	v_lshl_add_u32 v201, v13, 2, s23
	v_lshl_add_u32 v202, v14, 2, s23
	v_lshl_add_u32 v203, v15, 2, s23
	ds_read_b32 v140, v200
	ds_read_b32 v141, v201
	ds_read_b32 v142, v202
	ds_read_b32 v143, v203
	s_waitcnt lgkmcnt(0)
	v_lshl_add_u32 v140, v140, 8, v28
	v_lshl_add_u32 v141, v141, 8, v29
	v_lshl_add_u32 v142, v142, 8, v30
	v_lshl_add_u32 v143, v143, 8, v31
	v_lshl_add_u32 v140, v140, 11, v4
	v_lshl_add_u32 v141, v141, 11, v4
	v_lshl_add_u32 v142, v142, 11, v4
	v_lshl_add_u32 v143, v143, 11, v4
	global_load_dword v88, v140, s[6:7]
	global_load_dword v89, v140, s[6:7] offset:256
	global_load_dword v90, v140, s[6:7] offset:512
	global_load_dword v91, v140, s[6:7] offset:768
	global_load_dword v92, v141, s[6:7]
	global_load_dword v93, v141, s[6:7] offset:256
	global_load_dword v94, v141, s[6:7] offset:512
	global_load_dword v95, v141, s[6:7] offset:768
	global_load_dword v96, v142, s[6:7]
	global_load_dword v97, v142, s[6:7] offset:256
	global_load_dword v98, v142, s[6:7] offset:512
	global_load_dword v99, v142, s[6:7] offset:768
	global_load_dword v100, v143, s[6:7]
	global_load_dword v101, v143, s[6:7] offset:256
	global_load_dword v102, v143, s[6:7] offset:512
	global_load_dword v103, v143, s[6:7] offset:768
	v_lshl_add_u32 v200, v16, 2, s23
	v_lshl_add_u32 v201, v17, 2, s23
	v_lshl_add_u32 v202, v18, 2, s23
	v_lshl_add_u32 v203, v19, 2, s23
	ds_read_b32 v144, v200
	ds_read_b32 v145, v201
	ds_read_b32 v146, v202
	ds_read_b32 v147, v203
	s_waitcnt lgkmcnt(0)
; __device__ __forceinline__ float bf_lo(unsigned w) { return __uint_as_float(w << 16); }
; __device__ __forceinline__ float bf_hi(unsigned w) { return __uint_as_float(w & 0xffff0000u); }
; __global__ void __launch_bounds__(512, 2) fwd_kernel(Params p) {
;     ...
;             for (int u = 0; u < UN; ++u) { const int it = it0 + u * NGT < NI ? it0 + u * NGT : it0; mm[u] = it >> 7; cc[u] = (it & 127) * 16;
;                 const i32x4 e4 = *(const i32x4*)(tok_e + mm[u] * 4), r4 = *(const i32x4*)(tok_rank + mm[u] * 4);
; #pragma unroll
;                 for (int k = 0; k < 4; ++k) { ee[u][k] = e4[k]; rk[u][k] = r4[k]; }
;                 const bf16_t* xp = X1 + (size_t)mm[u] * DM + cc[u]; xa[u] = *(const u32x4*)xp; xb[u] = *(const u32x4*)(xp + 8); }
; #pragma unroll
;             for (int u = 0; u < UN; ++u)
; #pragma unroll
;                 for (int k = 0; k < 4; ++k) { const int pos = ts[ee[u][k]] * 256 + rk[u][k]; y[u][k] = *(const u32x4*)(Yb + (size_t)pos * DM + cc[u]); }
; #pragma unroll
;             for (int u = 0; u < UN; ++u) {
;                 f32x4 a[4];
;                 a[0] = (f32x4){bf_lo(xa[u].x), bf_hi(xa[u].x), bf_lo(xa[u].y), bf_hi(xa[u].y)}; a[1] = (f32x4){bf_lo(xa[u].z), bf_hi(xa[u].z), bf_lo(xa[u].w), bf_hi(xa[u].w)};
;                 a[2] = (f32x4){bf_lo(xb[u].x), bf_hi(xb[u].x), bf_lo(xb[u].y), bf_hi(xb[u].y)}; a[3] = (f32x4){bf_lo(xb[u].z), bf_hi(xb[u].z), bf_lo(xb[u].w), bf_hi(xb[u].w)};
; #pragma unroll
;                 for (int k = 0; k < 4; ++k)
; #pragma unroll
;                     for (int q = 0; q < 4; ++q) { const f32x2 lo = __builtin_amdgcn_cvt_pk_f32_fp8((int)y[u][k][q], false), hi = __builtin_amdgcn_cvt_pk_f32_fp8((int)y[u][k][q], true);
;                         a[q].x += lo.x * (1.0f / Y8_SCALE); a[q].y += lo.y * (1.0f / Y8_SCALE); a[q].z += hi.x * (1.0f / Y8_SCALE); a[q].w += hi.y * (1.0f / Y8_SCALE); }
;                 if (it0 + u * NGT < NI) { float* op = p.out + (size_t)mm[u] * DM + cc[u];
; #pragma unroll
;                     for (int q = 0; q < 4; ++q) *(f32x4*)(op + 4 * q) = a[q]; }
	v_lshl_add_u32 v144, v144, 8, v32
	v_lshl_add_u32 v145, v145, 8, v33
	v_lshl_add_u32 v146, v146, 8, v34
	v_lshl_add_u32 v147, v147, 8, v35
	v_lshl_add_u32 v144, v144, 11, v4
	v_lshl_add_u32 v145, v145, 11, v4
	v_lshl_add_u32 v146, v146, 11, v4
	v_lshl_add_u32 v147, v147, 11, v4
	global_load_dword v104, v144, s[6:7]
	global_load_dword v105, v144, s[6:7] offset:256
	global_load_dword v106, v144, s[6:7] offset:512
	global_load_dword v107, v144, s[6:7] offset:768
	global_load_dword v108, v145, s[6:7]
	global_load_dword v109, v145, s[6:7] offset:256
	global_load_dword v110, v145, s[6:7] offset:512
	global_load_dword v111, v145, s[6:7] offset:768
	global_load_dword v112, v146, s[6:7]
	global_load_dword v113, v146, s[6:7] offset:256
	global_load_dword v114, v146, s[6:7] offset:512
	global_load_dword v115, v146, s[6:7] offset:768
	global_load_dword v116, v147, s[6:7]
	global_load_dword v117, v147, s[6:7] offset:256
	global_load_dword v118, v147, s[6:7] offset:512
	global_load_dword v119, v147, s[6:7] offset:768
	v_lshl_add_u32 v200, v20, 2, s23
	v_lshl_add_u32 v201, v21, 2, s23
	v_lshl_add_u32 v202, v22, 2, s23
	v_lshl_add_u32 v203, v23, 2, s23
	ds_read_b32 v148, v200
	ds_read_b32 v149, v201
	ds_read_b32 v150, v202
	ds_read_b32 v151, v203
	s_waitcnt lgkmcnt(0)
	v_lshl_add_u32 v148, v148, 8, v36
	v_lshl_add_u32 v149, v149, 8, v37
	v_lshl_add_u32 v150, v150, 8, v38
	v_lshl_add_u32 v151, v151, 8, v39
	v_lshl_add_u32 v148, v148, 11, v4
	v_lshl_add_u32 v149, v149, 11, v4
	v_lshl_add_u32 v150, v150, 11, v4
	v_lshl_add_u32 v151, v151, 11, v4
	global_load_dword v120, v148, s[6:7]
	global_load_dword v121, v148, s[6:7] offset:256
	global_load_dword v122, v148, s[6:7] offset:512
	global_load_dword v123, v148, s[6:7] offset:768
	global_load_dword v124, v149, s[6:7]
	global_load_dword v125, v149, s[6:7] offset:256
	global_load_dword v126, v149, s[6:7] offset:512
	global_load_dword v127, v149, s[6:7] offset:768
	global_load_dword v128, v150, s[6:7]
	global_load_dword v129, v150, s[6:7] offset:256
	global_load_dword v130, v150, s[6:7] offset:512
	global_load_dword v131, v150, s[6:7] offset:768
	global_load_dword v132, v151, s[6:7]
	global_load_dword v133, v151, s[6:7] offset:256
	global_load_dword v134, v151, s[6:7] offset:512
	global_load_dword v135, v151, s[6:7] offset:768
	v_add_u32_e32 v192, 0x1000, v3
	v_lshlrev_b32_e32 v196, 4, v192
	v_lshl_add_u32 v248, v192, 13, v6
	v_add_u32_e32 v193, 0x1400, v3
	v_lshlrev_b32_e32 v197, 4, v193
	v_lshl_add_u32 v249, v193, 13, v6
	v_add_u32_e32 v194, 0x1800, v3
	v_lshlrev_b32_e32 v198, 4, v194
	v_lshl_add_u32 v250, v194, 13, v6
	v_add_u32_e32 v195, 0x1c00, v3
	v_lshlrev_b32_e32 v199, 4, v195
	v_lshl_add_u32 v251, v195, 13, v6
	global_load_dwordx4 v[8:11], v196, s[16:17]
	global_load_dwordx4 v[12:15], v197, s[16:17]
	global_load_dwordx4 v[16:19], v198, s[16:17]
	global_load_dwordx4 v[20:23], v199, s[16:17]
	global_load_dwordx4 v[24:27], v196, s[18:19]
	global_load_dwordx4 v[28:31], v197, s[18:19]
	global_load_dwordx4 v[32:35], v198, s[18:19]
	global_load_dwordx4 v[36:39], v199, s[18:19]
	v_lshl_add_u32 v196, v192, 12, v5
	global_load_dwordx2 v[216:217], v196, s[14:15]
	global_load_dwordx2 v[218:219], v196, s[14:15] offset:512
	global_load_dwordx2 v[220:221], v196, s[14:15] offset:1024
	global_load_dwordx2 v[222:223], v196, s[14:15] offset:1536
	v_lshl_add_u32 v197, v193, 12, v5
	global_load_dwordx2 v[224:225], v197, s[14:15]
	global_load_dwordx2 v[226:227], v197, s[14:15] offset:512
	global_load_dwordx2 v[228:229], v197, s[14:15] offset:1024
	global_load_dwordx2 v[230:231], v197, s[14:15] offset:1536
	v_lshl_add_u32 v198, v194, 12, v5
	global_load_dwordx2 v[232:233], v198, s[14:15]
	global_load_dwordx2 v[234:235], v198, s[14:15] offset:512
	global_load_dwordx2 v[236:237], v198, s[14:15] offset:1024
	global_load_dwordx2 v[238:239], v198, s[14:15] offset:1536
	v_lshl_add_u32 v199, v195, 12, v5
	global_load_dwordx2 v[240:241], v199, s[14:15]
	global_load_dwordx2 v[242:243], v199, s[14:15] offset:512
	global_load_dwordx2 v[244:245], v199, s[14:15] offset:1024
	global_load_dwordx2 v[246:247], v199, s[14:15] offset:1536
	s_waitcnt vmcnt(63)
	v_lshlrev_b32_e32 v176, 16, v40
	v_and_b32_e32 v177, 0xffff0000, v40
	v_lshlrev_b32_e32 v178, 16, v41
	v_and_b32_e32 v179, 0xffff0000, v41
	v_cvt_pk_f32_fp8_e32 v[160:161], v72
	v_cvt_pk_f32_fp8_sdwa v[162:163], v72 src0_sel:WORD_1
	v_pk_fma_f32 v[176:177], v[160:161], s[10:11], v[176:177] op_sel_hi:[1,0,1]
	v_pk_fma_f32 v[178:179], v[162:163], s[10:11], v[178:179] op_sel_hi:[1,0,1]
	v_cvt_pk_f32_fp8_e32 v[164:165], v76
	v_cvt_pk_f32_fp8_sdwa v[166:167], v76 src0_sel:WORD_1
	v_pk_fma_f32 v[176:177], v[164:165], s[10:11], v[176:177] op_sel_hi:[1,0,1]
	v_pk_fma_f32 v[178:179], v[166:167], s[10:11], v[178:179] op_sel_hi:[1,0,1]
	v_cvt_pk_f32_fp8_e32 v[168:169], v80
	v_cvt_pk_f32_fp8_sdwa v[170:171], v80 src0_sel:WORD_1
	v_pk_fma_f32 v[176:177], v[168:169], s[10:11], v[176:177] op_sel_hi:[1,0,1]
	v_pk_fma_f32 v[178:179], v[170:171], s[10:11], v[178:179] op_sel_hi:[1,0,1]
	v_cvt_pk_f32_fp8_e32 v[172:173], v84
	v_cvt_pk_f32_fp8_sdwa v[174:175], v84 src0_sel:WORD_1
	v_pk_fma_f32 v[176:177], v[172:173], s[10:11], v[176:177] op_sel_hi:[1,0,1]
	v_pk_fma_f32 v[178:179], v[174:175], s[10:11], v[178:179] op_sel_hi:[1,0,1]
	global_store_dwordx4 v156, v[176:179], s[4:5]
	v_lshlrev_b32_e32 v180, 16, v42
	v_and_b32_e32 v181, 0xffff0000, v42
	v_lshlrev_b32_e32 v182, 16, v43
	v_and_b32_e32 v183, 0xffff0000, v43
	v_cvt_pk_f32_fp8_e32 v[160:161], v73
	v_cvt_pk_f32_fp8_sdwa v[162:163], v73 src0_sel:WORD_1
	v_pk_fma_f32 v[180:181], v[160:161], s[10:11], v[180:181] op_sel_hi:[1,0,1]
; __device__ __forceinline__ float bf_lo(unsigned w) { return __uint_as_float(w << 16); }
; __device__ __forceinline__ float bf_hi(unsigned w) { return __uint_as_float(w & 0xffff0000u); }
; __global__ void __launch_bounds__(512, 2) fwd_kernel(Params p) {
;     ...
;             for (int u = 0; u < UN; ++u) { const int it = it0 + u * NGT < NI ? it0 + u * NGT : it0; mm[u] = it >> 7; cc[u] = (it & 127) * 16;
;                 const i32x4 e4 = *(const i32x4*)(tok_e + mm[u] * 4), r4 = *(const i32x4*)(tok_rank + mm[u] * 4);
; #pragma unroll
;                 for (int k = 0; k < 4; ++k) { ee[u][k] = e4[k]; rk[u][k] = r4[k]; }
;                 const bf16_t* xp = X1 + (size_t)mm[u] * DM + cc[u]; xa[u] = *(const u32x4*)xp; xb[u] = *(const u32x4*)(xp + 8); }
; #pragma unroll
;             for (int u = 0; u < UN; ++u)
; #pragma unroll
;                 for (int k = 0; k < 4; ++k) { const int pos = ts[ee[u][k]] * 256 + rk[u][k]; y[u][k] = *(const u32x4*)(Yb + (size_t)pos * DM + cc[u]); }
; #pragma unroll
;             for (int u = 0; u < UN; ++u) {
;                 f32x4 a[4];
;                 a[0] = (f32x4){bf_lo(xa[u].x), bf_hi(xa[u].x), bf_lo(xa[u].y), bf_hi(xa[u].y)}; a[1] = (f32x4){bf_lo(xa[u].z), bf_hi(xa[u].z), bf_lo(xa[u].w), bf_hi(xa[u].w)};
;                 a[2] = (f32x4){bf_lo(xb[u].x), bf_hi(xb[u].x), bf_lo(xb[u].y), bf_hi(xb[u].y)}; a[3] = (f32x4){bf_lo(xb[u].z), bf_hi(xb[u].z), bf_lo(xb[u].w), bf_hi(xb[u].w)};
; #pragma unroll
;                 for (int k = 0; k < 4; ++k)
; #pragma unroll
;                     for (int q = 0; q < 4; ++q) { const f32x2 lo = __builtin_amdgcn_cvt_pk_f32_fp8((int)y[u][k][q], false), hi = __builtin_amdgcn_cvt_pk_f32_fp8((int)y[u][k][q], true);
;                         a[q].x += lo.x * (1.0f / Y8_SCALE); a[q].y += lo.y * (1.0f / Y8_SCALE); a[q].z += hi.x * (1.0f / Y8_SCALE); a[q].w += hi.y * (1.0f / Y8_SCALE); }
;                 if (it0 + u * NGT < NI) { float* op = p.out + (size_t)mm[u] * DM + cc[u];
; #pragma unroll
;                     for (int q = 0; q < 4; ++q) *(f32x4*)(op + 4 * q) = a[q]; }
	v_pk_fma_f32 v[182:183], v[162:163], s[10:11], v[182:183] op_sel_hi:[1,0,1]
	v_cvt_pk_f32_fp8_e32 v[164:165], v77
	v_cvt_pk_f32_fp8_sdwa v[166:167], v77 src0_sel:WORD_1
	v_pk_fma_f32 v[180:181], v[164:165], s[10:11], v[180:181] op_sel_hi:[1,0,1]
	v_pk_fma_f32 v[182:183], v[166:167], s[10:11], v[182:183] op_sel_hi:[1,0,1]
	v_cvt_pk_f32_fp8_e32 v[168:169], v81
	v_cvt_pk_f32_fp8_sdwa v[170:171], v81 src0_sel:WORD_1
	v_pk_fma_f32 v[180:181], v[168:169], s[10:11], v[180:181] op_sel_hi:[1,0,1]
	v_pk_fma_f32 v[182:183], v[170:171], s[10:11], v[182:183] op_sel_hi:[1,0,1]
	v_cvt_pk_f32_fp8_e32 v[172:173], v85
	v_cvt_pk_f32_fp8_sdwa v[174:175], v85 src0_sel:WORD_1
	v_pk_fma_f32 v[180:181], v[172:173], s[10:11], v[180:181] op_sel_hi:[1,0,1]
	v_pk_fma_f32 v[182:183], v[174:175], s[10:11], v[182:183] op_sel_hi:[1,0,1]
	global_store_dwordx4 v156, v[180:183], s[4:5] offset:1024
	v_lshlrev_b32_e32 v184, 16, v44
	v_and_b32_e32 v185, 0xffff0000, v44
	v_lshlrev_b32_e32 v186, 16, v45
	v_and_b32_e32 v187, 0xffff0000, v45
	v_cvt_pk_f32_fp8_e32 v[160:161], v74
	v_cvt_pk_f32_fp8_sdwa v[162:163], v74 src0_sel:WORD_1
	v_pk_fma_f32 v[184:185], v[160:161], s[10:11], v[184:185] op_sel_hi:[1,0,1]
	v_pk_fma_f32 v[186:187], v[162:163], s[10:11], v[186:187] op_sel_hi:[1,0,1]
	v_cvt_pk_f32_fp8_e32 v[164:165], v78
	v_cvt_pk_f32_fp8_sdwa v[166:167], v78 src0_sel:WORD_1
	v_pk_fma_f32 v[184:185], v[164:165], s[10:11], v[184:185] op_sel_hi:[1,0,1]
	v_pk_fma_f32 v[186:187], v[166:167], s[10:11], v[186:187] op_sel_hi:[1,0,1]
	v_cvt_pk_f32_fp8_e32 v[168:169], v82
	v_cvt_pk_f32_fp8_sdwa v[170:171], v82 src0_sel:WORD_1
	v_pk_fma_f32 v[184:185], v[168:169], s[10:11], v[184:185] op_sel_hi:[1,0,1]
	v_pk_fma_f32 v[186:187], v[170:171], s[10:11], v[186:187] op_sel_hi:[1,0,1]
	v_cvt_pk_f32_fp8_e32 v[172:173], v86
	v_cvt_pk_f32_fp8_sdwa v[174:175], v86 src0_sel:WORD_1
	v_pk_fma_f32 v[184:185], v[172:173], s[10:11], v[184:185] op_sel_hi:[1,0,1]
	v_pk_fma_f32 v[186:187], v[174:175], s[10:11], v[186:187] op_sel_hi:[1,0,1]
	global_store_dwordx4 v156, v[184:187], s[4:5] offset:2048
	v_lshlrev_b32_e32 v188, 16, v46
	v_and_b32_e32 v189, 0xffff0000, v46
	v_lshlrev_b32_e32 v190, 16, v47
	v_and_b32_e32 v191, 0xffff0000, v47
	v_cvt_pk_f32_fp8_e32 v[160:161], v75
	v_cvt_pk_f32_fp8_sdwa v[162:163], v75 src0_sel:WORD_1
	v_pk_fma_f32 v[188:189], v[160:161], s[10:11], v[188:189] op_sel_hi:[1,0,1]
	v_pk_fma_f32 v[190:191], v[162:163], s[10:11], v[190:191] op_sel_hi:[1,0,1]
	v_cvt_pk_f32_fp8_e32 v[164:165], v79
	v_cvt_pk_f32_fp8_sdwa v[166:167], v79 src0_sel:WORD_1
	v_pk_fma_f32 v[188:189], v[164:165], s[10:11], v[188:189] op_sel_hi:[1,0,1]
	v_pk_fma_f32 v[190:191], v[166:167], s[10:11], v[190:191] op_sel_hi:[1,0,1]
	v_cvt_pk_f32_fp8_e32 v[168:169], v83
	v_cvt_pk_f32_fp8_sdwa v[170:171], v83 src0_sel:WORD_1
	v_pk_fma_f32 v[188:189], v[168:169], s[10:11], v[188:189] op_sel_hi:[1,0,1]
	v_pk_fma_f32 v[190:191], v[170:171], s[10:11], v[190:191] op_sel_hi:[1,0,1]
	v_cvt_pk_f32_fp8_e32 v[172:173], v87
	v_cvt_pk_f32_fp8_sdwa v[174:175], v87 src0_sel:WORD_1
	v_pk_fma_f32 v[188:189], v[172:173], s[10:11], v[188:189] op_sel_hi:[1,0,1]
	v_pk_fma_f32 v[190:191], v[174:175], s[10:11], v[190:191] op_sel_hi:[1,0,1]
	global_store_dwordx4 v156, v[188:191], s[4:5] offset:3072
	s_waitcnt vmcnt(20)
	v_lshl_add_u32 v200, v8, 2, s23
	v_lshl_add_u32 v201, v9, 2, s23
	v_lshl_add_u32 v202, v10, 2, s23
	v_lshl_add_u32 v203, v11, 2, s23
	ds_read_b32 v136, v200
	ds_read_b32 v137, v201
	ds_read_b32 v138, v202
	ds_read_b32 v139, v203
	s_waitcnt lgkmcnt(0)
	v_lshl_add_u32 v136, v136, 8, v24
	v_lshl_add_u32 v137, v137, 8, v25
	v_lshl_add_u32 v138, v138, 8, v26
	v_lshl_add_u32 v139, v139, 8, v27
	v_lshl_add_u32 v136, v136, 11, v4
	v_lshl_add_u32 v137, v137, 11, v4
	v_lshl_add_u32 v138, v138, 11, v4
	v_lshl_add_u32 v139, v139, 11, v4
	global_load_dword v72, v136, s[6:7]
	global_load_dword v73, v136, s[6:7] offset:256
	global_load_dword v74, v136, s[6:7] offset:512
	global_load_dword v75, v136, s[6:7] offset:768
	global_load_dword v76, v137, s[6:7]
	global_load_dword v77, v137, s[6:7] offset:256
	global_load_dword v78, v137, s[6:7] offset:512
	global_load_dword v79, v137, s[6:7] offset:768
	global_load_dword v80, v138, s[6:7]
	global_load_dword v81, v138, s[6:7] offset:256
	global_load_dword v82, v138, s[6:7] offset:512
	global_load_dword v83, v138, s[6:7] offset:768
	global_load_dword v84, v139, s[6:7]
	global_load_dword v85, v139, s[6:7] offset:256
	global_load_dword v86, v139, s[6:7] offset:512
	global_load_dword v87, v139, s[6:7] offset:768
	s_waitcnt vmcnt(63)
; __device__ __forceinline__ float bf_lo(unsigned w) { return __uint_as_float(w << 16); }
; __device__ __forceinline__ float bf_hi(unsigned w) { return __uint_as_float(w & 0xffff0000u); }
; __global__ void __launch_bounds__(512, 2) fwd_kernel(Params p) {
;     ...
;             for (int u = 0; u < UN; ++u) { const int it = it0 + u * NGT < NI ? it0 + u * NGT : it0; mm[u] = it >> 7; cc[u] = (it & 127) * 16;
;                 const i32x4 e4 = *(const i32x4*)(tok_e + mm[u] * 4), r4 = *(const i32x4*)(tok_rank + mm[u] * 4);
; #pragma unroll
;                 for (int k = 0; k < 4; ++k) { ee[u][k] = e4[k]; rk[u][k] = r4[k]; }
;                 const bf16_t* xp = X1 + (size_t)mm[u] * DM + cc[u]; xa[u] = *(const u32x4*)xp; xb[u] = *(const u32x4*)(xp + 8); }
; #pragma unroll
;             for (int u = 0; u < UN; ++u)
; #pragma unroll
;                 for (int k = 0; k < 4; ++k) { const int pos = ts[ee[u][k]] * 256 + rk[u][k]; y[u][k] = *(const u32x4*)(Yb + (size_t)pos * DM + cc[u]); }
;     ...
;             for (int u = 0; u < UN; ++u) {
;                 f32x4 a[4];
;                 a[0] = (f32x4){bf_lo(xa[u].x), bf_hi(xa[u].x), bf_lo(xa[u].y), bf_hi(xa[u].y)}; a[1] = (f32x4){bf_lo(xa[u].z), bf_hi(xa[u].z), bf_lo(xa[u].w), bf_hi(xa[u].w)};
;                 a[2] = (f32x4){bf_lo(xb[u].x), bf_hi(xb[u].x), bf_lo(xb[u].y), bf_hi(xb[u].y)}; a[3] = (f32x4){bf_lo(xb[u].z), bf_hi(xb[u].z), bf_lo(xb[u].w), bf_hi(xb[u].w)};
; #pragma unroll
;                 for (int k = 0; k < 4; ++k)
; #pragma unroll
;                     for (int q = 0; q < 4; ++q) { const f32x2 lo = __builtin_amdgcn_cvt_pk_f32_fp8((int)y[u][k][q], false), hi = __builtin_amdgcn_cvt_pk_f32_fp8((int)y[u][k][q], true);
;                         a[q].x += lo.x * (1.0f / Y8_SCALE); a[q].y += lo.y * (1.0f / Y8_SCALE); a[q].z += hi.x * (1.0f / Y8_SCALE); a[q].w += hi.y * (1.0f / Y8_SCALE); }
;                 if (it0 + u * NGT < NI) { float* op = p.out + (size_t)mm[u] * DM + cc[u];
; #pragma unroll
;                     for (int q = 0; q < 4; ++q) *(f32x4*)(op + 4 * q) = a[q]; }
	v_lshlrev_b32_e32 v176, 16, v48
	v_and_b32_e32 v177, 0xffff0000, v48
	v_lshlrev_b32_e32 v178, 16, v49
	v_and_b32_e32 v179, 0xffff0000, v49
	v_cvt_pk_f32_fp8_e32 v[160:161], v88
	v_cvt_pk_f32_fp8_sdwa v[162:163], v88 src0_sel:WORD_1
	v_pk_fma_f32 v[176:177], v[160:161], s[10:11], v[176:177] op_sel_hi:[1,0,1]
	v_pk_fma_f32 v[178:179], v[162:163], s[10:11], v[178:179] op_sel_hi:[1,0,1]
	v_cvt_pk_f32_fp8_e32 v[164:165], v92
	v_cvt_pk_f32_fp8_sdwa v[166:167], v92 src0_sel:WORD_1
	v_pk_fma_f32 v[176:177], v[164:165], s[10:11], v[176:177] op_sel_hi:[1,0,1]
	v_pk_fma_f32 v[178:179], v[166:167], s[10:11], v[178:179] op_sel_hi:[1,0,1]
	v_cvt_pk_f32_fp8_e32 v[168:169], v96
	v_cvt_pk_f32_fp8_sdwa v[170:171], v96 src0_sel:WORD_1
	v_pk_fma_f32 v[176:177], v[168:169], s[10:11], v[176:177] op_sel_hi:[1,0,1]
	v_pk_fma_f32 v[178:179], v[170:171], s[10:11], v[178:179] op_sel_hi:[1,0,1]
	v_cvt_pk_f32_fp8_e32 v[172:173], v100
	v_cvt_pk_f32_fp8_sdwa v[174:175], v100 src0_sel:WORD_1
	v_pk_fma_f32 v[176:177], v[172:173], s[10:11], v[176:177] op_sel_hi:[1,0,1]
	v_pk_fma_f32 v[178:179], v[174:175], s[10:11], v[178:179] op_sel_hi:[1,0,1]
	global_store_dwordx4 v157, v[176:179], s[4:5]
	v_lshlrev_b32_e32 v180, 16, v50
	v_and_b32_e32 v181, 0xffff0000, v50
	v_lshlrev_b32_e32 v182, 16, v51
	v_and_b32_e32 v183, 0xffff0000, v51
	v_cvt_pk_f32_fp8_e32 v[160:161], v89
	v_cvt_pk_f32_fp8_sdwa v[162:163], v89 src0_sel:WORD_1
	v_pk_fma_f32 v[180:181], v[160:161], s[10:11], v[180:181] op_sel_hi:[1,0,1]
	v_pk_fma_f32 v[182:183], v[162:163], s[10:11], v[182:183] op_sel_hi:[1,0,1]
	v_cvt_pk_f32_fp8_e32 v[164:165], v93
	v_cvt_pk_f32_fp8_sdwa v[166:167], v93 src0_sel:WORD_1
	v_pk_fma_f32 v[180:181], v[164:165], s[10:11], v[180:181] op_sel_hi:[1,0,1]
	v_pk_fma_f32 v[182:183], v[166:167], s[10:11], v[182:183] op_sel_hi:[1,0,1]
	v_cvt_pk_f32_fp8_e32 v[168:169], v97
	v_cvt_pk_f32_fp8_sdwa v[170:171], v97 src0_sel:WORD_1
	v_pk_fma_f32 v[180:181], v[168:169], s[10:11], v[180:181] op_sel_hi:[1,0,1]
	v_pk_fma_f32 v[182:183], v[170:171], s[10:11], v[182:183] op_sel_hi:[1,0,1]
	v_cvt_pk_f32_fp8_e32 v[172:173], v101
	v_cvt_pk_f32_fp8_sdwa v[174:175], v101 src0_sel:WORD_1
	v_pk_fma_f32 v[180:181], v[172:173], s[10:11], v[180:181] op_sel_hi:[1,0,1]
	v_pk_fma_f32 v[182:183], v[174:175], s[10:11], v[182:183] op_sel_hi:[1,0,1]
	global_store_dwordx4 v157, v[180:183], s[4:5] offset:1024
	v_lshlrev_b32_e32 v184, 16, v52
	v_and_b32_e32 v185, 0xffff0000, v52
	v_lshlrev_b32_e32 v186, 16, v53
	v_and_b32_e32 v187, 0xffff0000, v53
	v_cvt_pk_f32_fp8_e32 v[160:161], v90
	v_cvt_pk_f32_fp8_sdwa v[162:163], v90 src0_sel:WORD_1
	v_pk_fma_f32 v[184:185], v[160:161], s[10:11], v[184:185] op_sel_hi:[1,0,1]
	v_pk_fma_f32 v[186:187], v[162:163], s[10:11], v[186:187] op_sel_hi:[1,0,1]
	v_cvt_pk_f32_fp8_e32 v[164:165], v94
	v_cvt_pk_f32_fp8_sdwa v[166:167], v94 src0_sel:WORD_1
	v_pk_fma_f32 v[184:185], v[164:165], s[10:11], v[184:185] op_sel_hi:[1,0,1]
	v_pk_fma_f32 v[186:187], v[166:167], s[10:11], v[186:187] op_sel_hi:[1,0,1]
	v_cvt_pk_f32_fp8_e32 v[168:169], v98
	v_cvt_pk_f32_fp8_sdwa v[170:171], v98 src0_sel:WORD_1
	v_pk_fma_f32 v[184:185], v[168:169], s[10:11], v[184:185] op_sel_hi:[1,0,1]
	v_pk_fma_f32 v[186:187], v[170:171], s[10:11], v[186:187] op_sel_hi:[1,0,1]
	v_cvt_pk_f32_fp8_e32 v[172:173], v102
	v_cvt_pk_f32_fp8_sdwa v[174:175], v102 src0_sel:WORD_1
	v_pk_fma_f32 v[184:185], v[172:173], s[10:11], v[184:185] op_sel_hi:[1,0,1]
	v_pk_fma_f32 v[186:187], v[174:175], s[10:11], v[186:187] op_sel_hi:[1,0,1]
	global_store_dwordx4 v157, v[184:187], s[4:5] offset:2048
	v_lshlrev_b32_e32 v188, 16, v54
	v_and_b32_e32 v189, 0xffff0000, v54
	v_lshlrev_b32_e32 v190, 16, v55
	v_and_b32_e32 v191, 0xffff0000, v55
	v_cvt_pk_f32_fp8_e32 v[160:161], v91
	v_cvt_pk_f32_fp8_sdwa v[162:163], v91 src0_sel:WORD_1
	v_pk_fma_f32 v[188:189], v[160:161], s[10:11], v[188:189] op_sel_hi:[1,0,1]
	v_pk_fma_f32 v[190:191], v[162:163], s[10:11], v[190:191] op_sel_hi:[1,0,1]
	v_cvt_pk_f32_fp8_e32 v[164:165], v95
	v_cvt_pk_f32_fp8_sdwa v[166:167], v95 src0_sel:WORD_1
	v_pk_fma_f32 v[188:189], v[164:165], s[10:11], v[188:189] op_sel_hi:[1,0,1]
	v_pk_fma_f32 v[190:191], v[166:167], s[10:11], v[190:191] op_sel_hi:[1,0,1]
	v_cvt_pk_f32_fp8_e32 v[168:169], v99
	v_cvt_pk_f32_fp8_sdwa v[170:171], v99 src0_sel:WORD_1
	v_pk_fma_f32 v[188:189], v[168:169], s[10:11], v[188:189] op_sel_hi:[1,0,1]
	v_pk_fma_f32 v[190:191], v[170:171], s[10:11], v[190:191] op_sel_hi:[1,0,1]
	v_cvt_pk_f32_fp8_e32 v[172:173], v103
	v_cvt_pk_f32_fp8_sdwa v[174:175], v103 src0_sel:WORD_1
	v_pk_fma_f32 v[188:189], v[172:173], s[10:11], v[188:189] op_sel_hi:[1,0,1]
	v_pk_fma_f32 v[190:191], v[174:175], s[10:11], v[190:191] op_sel_hi:[1,0,1]
	global_store_dwordx4 v157, v[188:191], s[4:5] offset:3072
	v_lshl_add_u32 v200, v12, 2, s23
	v_lshl_add_u32 v201, v13, 2, s23
	v_lshl_add_u32 v202, v14, 2, s23
	v_lshl_add_u32 v203, v15, 2, s23
	ds_read_b32 v140, v200
	ds_read_b32 v141, v201
	ds_read_b32 v142, v202
	ds_read_b32 v143, v203
	s_waitcnt lgkmcnt(0)
	v_lshl_add_u32 v140, v140, 8, v28
	v_lshl_add_u32 v141, v141, 8, v29
	v_lshl_add_u32 v142, v142, 8, v30
	v_lshl_add_u32 v143, v143, 8, v31
	v_lshl_add_u32 v140, v140, 11, v4
	v_lshl_add_u32 v141, v141, 11, v4
	v_lshl_add_u32 v142, v142, 11, v4
	v_lshl_add_u32 v143, v143, 11, v4
	global_load_dword v88, v140, s[6:7]
	global_load_dword v89, v140, s[6:7] offset:256
	global_load_dword v90, v140, s[6:7] offset:512
	global_load_dword v91, v140, s[6:7] offset:768
	global_load_dword v92, v141, s[6:7]
	global_load_dword v93, v141, s[6:7] offset:256
	global_load_dword v94, v141, s[6:7] offset:512
	global_load_dword v95, v141, s[6:7] offset:768
	global_load_dword v96, v142, s[6:7]
	global_load_dword v97, v142, s[6:7] offset:256
	global_load_dword v98, v142, s[6:7] offset:512
	global_load_dword v99, v142, s[6:7] offset:768
	global_load_dword v100, v143, s[6:7]
	global_load_dword v101, v143, s[6:7] offset:256
	global_load_dword v102, v143, s[6:7] offset:512
	global_load_dword v103, v143, s[6:7] offset:768
	s_waitcnt vmcnt(63)
; __device__ __forceinline__ float bf_lo(unsigned w) { return __uint_as_float(w << 16); }
; __device__ __forceinline__ float bf_hi(unsigned w) { return __uint_as_float(w & 0xffff0000u); }
; __global__ void __launch_bounds__(512, 2) fwd_kernel(Params p) {
;     ...
;             for (int u = 0; u < UN; ++u) { const int it = it0 + u * NGT < NI ? it0 + u * NGT : it0; mm[u] = it >> 7; cc[u] = (it & 127) * 16;
;                 const i32x4 e4 = *(const i32x4*)(tok_e + mm[u] * 4), r4 = *(const i32x4*)(tok_rank + mm[u] * 4);
; #pragma unroll
;                 for (int k = 0; k < 4; ++k) { ee[u][k] = e4[k]; rk[u][k] = r4[k]; }
;                 const bf16_t* xp = X1 + (size_t)mm[u] * DM + cc[u]; xa[u] = *(const u32x4*)xp; xb[u] = *(const u32x4*)(xp + 8); }
; #pragma unroll
;             for (int u = 0; u < UN; ++u)
; #pragma unroll
;                 for (int k = 0; k < 4; ++k) { const int pos = ts[ee[u][k]] * 256 + rk[u][k]; y[u][k] = *(const u32x4*)(Yb + (size_t)pos * DM + cc[u]); }
;     ...
;             for (int u = 0; u < UN; ++u) {
;                 f32x4 a[4];
;                 a[0] = (f32x4){bf_lo(xa[u].x), bf_hi(xa[u].x), bf_lo(xa[u].y), bf_hi(xa[u].y)}; a[1] = (f32x4){bf_lo(xa[u].z), bf_hi(xa[u].z), bf_lo(xa[u].w), bf_hi(xa[u].w)};
;                 a[2] = (f32x4){bf_lo(xb[u].x), bf_hi(xb[u].x), bf_lo(xb[u].y), bf_hi(xb[u].y)}; a[3] = (f32x4){bf_lo(xb[u].z), bf_hi(xb[u].z), bf_lo(xb[u].w), bf_hi(xb[u].w)};
; #pragma unroll
;                 for (int k = 0; k < 4; ++k)
; #pragma unroll
;                     for (int q = 0; q < 4; ++q) { const f32x2 lo = __builtin_amdgcn_cvt_pk_f32_fp8((int)y[u][k][q], false), hi = __builtin_amdgcn_cvt_pk_f32_fp8((int)y[u][k][q], true);
;                         a[q].x += lo.x * (1.0f / Y8_SCALE); a[q].y += lo.y * (1.0f / Y8_SCALE); a[q].z += hi.x * (1.0f / Y8_SCALE); a[q].w += hi.y * (1.0f / Y8_SCALE); }
;                 if (it0 + u * NGT < NI) { float* op = p.out + (size_t)mm[u] * DM + cc[u];
; #pragma unroll
;                     for (int q = 0; q < 4; ++q) *(f32x4*)(op + 4 * q) = a[q]; }
	v_lshlrev_b32_e32 v176, 16, v56
	v_and_b32_e32 v177, 0xffff0000, v56
	v_lshlrev_b32_e32 v178, 16, v57
	v_and_b32_e32 v179, 0xffff0000, v57
	v_cvt_pk_f32_fp8_e32 v[160:161], v104
	v_cvt_pk_f32_fp8_sdwa v[162:163], v104 src0_sel:WORD_1
	v_pk_fma_f32 v[176:177], v[160:161], s[10:11], v[176:177] op_sel_hi:[1,0,1]
	v_pk_fma_f32 v[178:179], v[162:163], s[10:11], v[178:179] op_sel_hi:[1,0,1]
	v_cvt_pk_f32_fp8_e32 v[164:165], v108
	v_cvt_pk_f32_fp8_sdwa v[166:167], v108 src0_sel:WORD_1
	v_pk_fma_f32 v[176:177], v[164:165], s[10:11], v[176:177] op_sel_hi:[1,0,1]
	v_pk_fma_f32 v[178:179], v[166:167], s[10:11], v[178:179] op_sel_hi:[1,0,1]
	v_cvt_pk_f32_fp8_e32 v[168:169], v112
	v_cvt_pk_f32_fp8_sdwa v[170:171], v112 src0_sel:WORD_1
	v_pk_fma_f32 v[176:177], v[168:169], s[10:11], v[176:177] op_sel_hi:[1,0,1]
	v_pk_fma_f32 v[178:179], v[170:171], s[10:11], v[178:179] op_sel_hi:[1,0,1]
	v_cvt_pk_f32_fp8_e32 v[172:173], v116
	v_cvt_pk_f32_fp8_sdwa v[174:175], v116 src0_sel:WORD_1
	v_pk_fma_f32 v[176:177], v[172:173], s[10:11], v[176:177] op_sel_hi:[1,0,1]
	v_pk_fma_f32 v[178:179], v[174:175], s[10:11], v[178:179] op_sel_hi:[1,0,1]
	global_store_dwordx4 v158, v[176:179], s[4:5]
	v_lshlrev_b32_e32 v180, 16, v58
	v_and_b32_e32 v181, 0xffff0000, v58
	v_lshlrev_b32_e32 v182, 16, v59
	v_and_b32_e32 v183, 0xffff0000, v59
	v_cvt_pk_f32_fp8_e32 v[160:161], v105
	v_cvt_pk_f32_fp8_sdwa v[162:163], v105 src0_sel:WORD_1
	v_pk_fma_f32 v[180:181], v[160:161], s[10:11], v[180:181] op_sel_hi:[1,0,1]
	v_pk_fma_f32 v[182:183], v[162:163], s[10:11], v[182:183] op_sel_hi:[1,0,1]
	v_cvt_pk_f32_fp8_e32 v[164:165], v109
	v_cvt_pk_f32_fp8_sdwa v[166:167], v109 src0_sel:WORD_1
	v_pk_fma_f32 v[180:181], v[164:165], s[10:11], v[180:181] op_sel_hi:[1,0,1]
	v_pk_fma_f32 v[182:183], v[166:167], s[10:11], v[182:183] op_sel_hi:[1,0,1]
	v_cvt_pk_f32_fp8_e32 v[168:169], v113
	v_cvt_pk_f32_fp8_sdwa v[170:171], v113 src0_sel:WORD_1
	v_pk_fma_f32 v[180:181], v[168:169], s[10:11], v[180:181] op_sel_hi:[1,0,1]
	v_pk_fma_f32 v[182:183], v[170:171], s[10:11], v[182:183] op_sel_hi:[1,0,1]
	v_cvt_pk_f32_fp8_e32 v[172:173], v117
	v_cvt_pk_f32_fp8_sdwa v[174:175], v117 src0_sel:WORD_1
	v_pk_fma_f32 v[180:181], v[172:173], s[10:11], v[180:181] op_sel_hi:[1,0,1]
	v_pk_fma_f32 v[182:183], v[174:175], s[10:11], v[182:183] op_sel_hi:[1,0,1]
	global_store_dwordx4 v158, v[180:183], s[4:5] offset:1024
	v_lshlrev_b32_e32 v184, 16, v60
	v_and_b32_e32 v185, 0xffff0000, v60
	v_lshlrev_b32_e32 v186, 16, v61
	v_and_b32_e32 v187, 0xffff0000, v61
	v_cvt_pk_f32_fp8_e32 v[160:161], v106
	v_cvt_pk_f32_fp8_sdwa v[162:163], v106 src0_sel:WORD_1
	v_pk_fma_f32 v[184:185], v[160:161], s[10:11], v[184:185] op_sel_hi:[1,0,1]
	v_pk_fma_f32 v[186:187], v[162:163], s[10:11], v[186:187] op_sel_hi:[1,0,1]
	v_cvt_pk_f32_fp8_e32 v[164:165], v110
	v_cvt_pk_f32_fp8_sdwa v[166:167], v110 src0_sel:WORD_1
	v_pk_fma_f32 v[184:185], v[164:165], s[10:11], v[184:185] op_sel_hi:[1,0,1]
	v_pk_fma_f32 v[186:187], v[166:167], s[10:11], v[186:187] op_sel_hi:[1,0,1]
	v_cvt_pk_f32_fp8_e32 v[168:169], v114
	v_cvt_pk_f32_fp8_sdwa v[170:171], v114 src0_sel:WORD_1
	v_pk_fma_f32 v[184:185], v[168:169], s[10:11], v[184:185] op_sel_hi:[1,0,1]
	v_pk_fma_f32 v[186:187], v[170:171], s[10:11], v[186:187] op_sel_hi:[1,0,1]
	v_cvt_pk_f32_fp8_e32 v[172:173], v118
	v_cvt_pk_f32_fp8_sdwa v[174:175], v118 src0_sel:WORD_1
	v_pk_fma_f32 v[184:185], v[172:173], s[10:11], v[184:185] op_sel_hi:[1,0,1]
	v_pk_fma_f32 v[186:187], v[174:175], s[10:11], v[186:187] op_sel_hi:[1,0,1]
	global_store_dwordx4 v158, v[184:187], s[4:5] offset:2048
	v_lshlrev_b32_e32 v188, 16, v62
	v_and_b32_e32 v189, 0xffff0000, v62
	v_lshlrev_b32_e32 v190, 16, v63
	v_and_b32_e32 v191, 0xffff0000, v63
	v_cvt_pk_f32_fp8_e32 v[160:161], v107
	v_cvt_pk_f32_fp8_sdwa v[162:163], v107 src0_sel:WORD_1
	v_pk_fma_f32 v[188:189], v[160:161], s[10:11], v[188:189] op_sel_hi:[1,0,1]
	v_pk_fma_f32 v[190:191], v[162:163], s[10:11], v[190:191] op_sel_hi:[1,0,1]
	v_cvt_pk_f32_fp8_e32 v[164:165], v111
	v_cvt_pk_f32_fp8_sdwa v[166:167], v111 src0_sel:WORD_1
	v_pk_fma_f32 v[188:189], v[164:165], s[10:11], v[188:189] op_sel_hi:[1,0,1]
	v_pk_fma_f32 v[190:191], v[166:167], s[10:11], v[190:191] op_sel_hi:[1,0,1]
	v_cvt_pk_f32_fp8_e32 v[168:169], v115
	v_cvt_pk_f32_fp8_sdwa v[170:171], v115 src0_sel:WORD_1
	v_pk_fma_f32 v[188:189], v[168:169], s[10:11], v[188:189] op_sel_hi:[1,0,1]
	v_pk_fma_f32 v[190:191], v[170:171], s[10:11], v[190:191] op_sel_hi:[1,0,1]
	v_cvt_pk_f32_fp8_e32 v[172:173], v119
	v_cvt_pk_f32_fp8_sdwa v[174:175], v119 src0_sel:WORD_1
	v_pk_fma_f32 v[188:189], v[172:173], s[10:11], v[188:189] op_sel_hi:[1,0,1]
	v_pk_fma_f32 v[190:191], v[174:175], s[10:11], v[190:191] op_sel_hi:[1,0,1]
	global_store_dwordx4 v158, v[188:191], s[4:5] offset:3072
	v_lshl_add_u32 v200, v16, 2, s23
	v_lshl_add_u32 v201, v17, 2, s23
	v_lshl_add_u32 v202, v18, 2, s23
	v_lshl_add_u32 v203, v19, 2, s23
	ds_read_b32 v144, v200
	ds_read_b32 v145, v201
	ds_read_b32 v146, v202
	ds_read_b32 v147, v203
	s_waitcnt lgkmcnt(0)
	v_lshl_add_u32 v144, v144, 8, v32
	v_lshl_add_u32 v145, v145, 8, v33
	v_lshl_add_u32 v146, v146, 8, v34
	v_lshl_add_u32 v147, v147, 8, v35
	v_lshl_add_u32 v144, v144, 11, v4
	v_lshl_add_u32 v145, v145, 11, v4
	v_lshl_add_u32 v146, v146, 11, v4
	v_lshl_add_u32 v147, v147, 11, v4
	global_load_dword v104, v144, s[6:7]
	global_load_dword v105, v144, s[6:7] offset:256
	global_load_dword v106, v144, s[6:7] offset:512
	global_load_dword v107, v144, s[6:7] offset:768
	global_load_dword v108, v145, s[6:7]
	global_load_dword v109, v145, s[6:7] offset:256
	global_load_dword v110, v145, s[6:7] offset:512
	global_load_dword v111, v145, s[6:7] offset:768
	global_load_dword v112, v146, s[6:7]
	global_load_dword v113, v146, s[6:7] offset:256
	global_load_dword v114, v146, s[6:7] offset:512
	global_load_dword v115, v146, s[6:7] offset:768
	global_load_dword v116, v147, s[6:7]
	global_load_dword v117, v147, s[6:7] offset:256
	global_load_dword v118, v147, s[6:7] offset:512
	global_load_dword v119, v147, s[6:7] offset:768
	s_waitcnt vmcnt(63)
; __device__ __forceinline__ float bf_lo(unsigned w) { return __uint_as_float(w << 16); }
; __device__ __forceinline__ float bf_hi(unsigned w) { return __uint_as_float(w & 0xffff0000u); }
; __global__ void __launch_bounds__(512, 2) fwd_kernel(Params p) {
;     ...
;             for (int u = 0; u < UN; ++u) { const int it = it0 + u * NGT < NI ? it0 + u * NGT : it0; mm[u] = it >> 7; cc[u] = (it & 127) * 16;
;                 const i32x4 e4 = *(const i32x4*)(tok_e + mm[u] * 4), r4 = *(const i32x4*)(tok_rank + mm[u] * 4);
; #pragma unroll
;                 for (int k = 0; k < 4; ++k) { ee[u][k] = e4[k]; rk[u][k] = r4[k]; }
;                 const bf16_t* xp = X1 + (size_t)mm[u] * DM + cc[u]; xa[u] = *(const u32x4*)xp; xb[u] = *(const u32x4*)(xp + 8); }
; #pragma unroll
;             for (int u = 0; u < UN; ++u)
; #pragma unroll
;                 for (int k = 0; k < 4; ++k) { const int pos = ts[ee[u][k]] * 256 + rk[u][k]; y[u][k] = *(const u32x4*)(Yb + (size_t)pos * DM + cc[u]); }
;     ...
;             for (int u = 0; u < UN; ++u) {
;                 f32x4 a[4];
;                 a[0] = (f32x4){bf_lo(xa[u].x), bf_hi(xa[u].x), bf_lo(xa[u].y), bf_hi(xa[u].y)}; a[1] = (f32x4){bf_lo(xa[u].z), bf_hi(xa[u].z), bf_lo(xa[u].w), bf_hi(xa[u].w)};
;                 a[2] = (f32x4){bf_lo(xb[u].x), bf_hi(xb[u].x), bf_lo(xb[u].y), bf_hi(xb[u].y)}; a[3] = (f32x4){bf_lo(xb[u].z), bf_hi(xb[u].z), bf_lo(xb[u].w), bf_hi(xb[u].w)};
; #pragma unroll
;                 for (int k = 0; k < 4; ++k)
; #pragma unroll
;                     for (int q = 0; q < 4; ++q) { const f32x2 lo = __builtin_amdgcn_cvt_pk_f32_fp8((int)y[u][k][q], false), hi = __builtin_amdgcn_cvt_pk_f32_fp8((int)y[u][k][q], true);
;                         a[q].x += lo.x * (1.0f / Y8_SCALE); a[q].y += lo.y * (1.0f / Y8_SCALE); a[q].z += hi.x * (1.0f / Y8_SCALE); a[q].w += hi.y * (1.0f / Y8_SCALE); }
;                 if (it0 + u * NGT < NI) { float* op = p.out + (size_t)mm[u] * DM + cc[u];
; #pragma unroll
;                     for (int q = 0; q < 4; ++q) *(f32x4*)(op + 4 * q) = a[q]; }
	v_lshlrev_b32_e32 v176, 16, v64
	v_and_b32_e32 v177, 0xffff0000, v64
	v_lshlrev_b32_e32 v178, 16, v65
	v_and_b32_e32 v179, 0xffff0000, v65
	v_cvt_pk_f32_fp8_e32 v[160:161], v120
	v_cvt_pk_f32_fp8_sdwa v[162:163], v120 src0_sel:WORD_1
	v_pk_fma_f32 v[176:177], v[160:161], s[10:11], v[176:177] op_sel_hi:[1,0,1]
	v_pk_fma_f32 v[178:179], v[162:163], s[10:11], v[178:179] op_sel_hi:[1,0,1]
	v_cvt_pk_f32_fp8_e32 v[164:165], v124
	v_cvt_pk_f32_fp8_sdwa v[166:167], v124 src0_sel:WORD_1
	v_pk_fma_f32 v[176:177], v[164:165], s[10:11], v[176:177] op_sel_hi:[1,0,1]
	v_pk_fma_f32 v[178:179], v[166:167], s[10:11], v[178:179] op_sel_hi:[1,0,1]
	v_cvt_pk_f32_fp8_e32 v[168:169], v128
	v_cvt_pk_f32_fp8_sdwa v[170:171], v128 src0_sel:WORD_1
	v_pk_fma_f32 v[176:177], v[168:169], s[10:11], v[176:177] op_sel_hi:[1,0,1]
	v_pk_fma_f32 v[178:179], v[170:171], s[10:11], v[178:179] op_sel_hi:[1,0,1]
	v_cvt_pk_f32_fp8_e32 v[172:173], v132
	v_cvt_pk_f32_fp8_sdwa v[174:175], v132 src0_sel:WORD_1
	v_pk_fma_f32 v[176:177], v[172:173], s[10:11], v[176:177] op_sel_hi:[1,0,1]
	v_pk_fma_f32 v[178:179], v[174:175], s[10:11], v[178:179] op_sel_hi:[1,0,1]
	global_store_dwordx4 v159, v[176:179], s[4:5]
	v_lshlrev_b32_e32 v180, 16, v66
	v_and_b32_e32 v181, 0xffff0000, v66
	v_lshlrev_b32_e32 v182, 16, v67
	v_and_b32_e32 v183, 0xffff0000, v67
	v_cvt_pk_f32_fp8_e32 v[160:161], v121
	v_cvt_pk_f32_fp8_sdwa v[162:163], v121 src0_sel:WORD_1
	v_pk_fma_f32 v[180:181], v[160:161], s[10:11], v[180:181] op_sel_hi:[1,0,1]
	v_pk_fma_f32 v[182:183], v[162:163], s[10:11], v[182:183] op_sel_hi:[1,0,1]
	v_cvt_pk_f32_fp8_e32 v[164:165], v125
	v_cvt_pk_f32_fp8_sdwa v[166:167], v125 src0_sel:WORD_1
	v_pk_fma_f32 v[180:181], v[164:165], s[10:11], v[180:181] op_sel_hi:[1,0,1]
	v_pk_fma_f32 v[182:183], v[166:167], s[10:11], v[182:183] op_sel_hi:[1,0,1]
	v_cvt_pk_f32_fp8_e32 v[168:169], v129
	v_cvt_pk_f32_fp8_sdwa v[170:171], v129 src0_sel:WORD_1
	v_pk_fma_f32 v[180:181], v[168:169], s[10:11], v[180:181] op_sel_hi:[1,0,1]
	v_pk_fma_f32 v[182:183], v[170:171], s[10:11], v[182:183] op_sel_hi:[1,0,1]
	v_cvt_pk_f32_fp8_e32 v[172:173], v133
	v_cvt_pk_f32_fp8_sdwa v[174:175], v133 src0_sel:WORD_1
	v_pk_fma_f32 v[180:181], v[172:173], s[10:11], v[180:181] op_sel_hi:[1,0,1]
	v_pk_fma_f32 v[182:183], v[174:175], s[10:11], v[182:183] op_sel_hi:[1,0,1]
	global_store_dwordx4 v159, v[180:183], s[4:5] offset:1024
	v_lshlrev_b32_e32 v184, 16, v68
	v_and_b32_e32 v185, 0xffff0000, v68
	v_lshlrev_b32_e32 v186, 16, v69
	v_and_b32_e32 v187, 0xffff0000, v69
	v_cvt_pk_f32_fp8_e32 v[160:161], v122
	v_cvt_pk_f32_fp8_sdwa v[162:163], v122 src0_sel:WORD_1
	v_pk_fma_f32 v[184:185], v[160:161], s[10:11], v[184:185] op_sel_hi:[1,0,1]
	v_pk_fma_f32 v[186:187], v[162:163], s[10:11], v[186:187] op_sel_hi:[1,0,1]
	v_cvt_pk_f32_fp8_e32 v[164:165], v126
	v_cvt_pk_f32_fp8_sdwa v[166:167], v126 src0_sel:WORD_1
	v_pk_fma_f32 v[184:185], v[164:165], s[10:11], v[184:185] op_sel_hi:[1,0,1]
	v_pk_fma_f32 v[186:187], v[166:167], s[10:11], v[186:187] op_sel_hi:[1,0,1]
	v_cvt_pk_f32_fp8_e32 v[168:169], v130
	v_cvt_pk_f32_fp8_sdwa v[170:171], v130 src0_sel:WORD_1
	v_pk_fma_f32 v[184:185], v[168:169], s[10:11], v[184:185] op_sel_hi:[1,0,1]
	v_pk_fma_f32 v[186:187], v[170:171], s[10:11], v[186:187] op_sel_hi:[1,0,1]
	v_cvt_pk_f32_fp8_e32 v[172:173], v134
	v_cvt_pk_f32_fp8_sdwa v[174:175], v134 src0_sel:WORD_1
	v_pk_fma_f32 v[184:185], v[172:173], s[10:11], v[184:185] op_sel_hi:[1,0,1]
	v_pk_fma_f32 v[186:187], v[174:175], s[10:11], v[186:187] op_sel_hi:[1,0,1]
	global_store_dwordx4 v159, v[184:187], s[4:5] offset:2048
	v_lshlrev_b32_e32 v188, 16, v70
	v_and_b32_e32 v189, 0xffff0000, v70
	v_lshlrev_b32_e32 v190, 16, v71
	v_and_b32_e32 v191, 0xffff0000, v71
	v_cvt_pk_f32_fp8_e32 v[160:161], v123
	v_cvt_pk_f32_fp8_sdwa v[162:163], v123 src0_sel:WORD_1
	v_pk_fma_f32 v[188:189], v[160:161], s[10:11], v[188:189] op_sel_hi:[1,0,1]
	v_pk_fma_f32 v[190:191], v[162:163], s[10:11], v[190:191] op_sel_hi:[1,0,1]
	v_cvt_pk_f32_fp8_e32 v[164:165], v127
	v_cvt_pk_f32_fp8_sdwa v[166:167], v127 src0_sel:WORD_1
	v_pk_fma_f32 v[188:189], v[164:165], s[10:11], v[188:189] op_sel_hi:[1,0,1]
	v_pk_fma_f32 v[190:191], v[166:167], s[10:11], v[190:191] op_sel_hi:[1,0,1]
	v_cvt_pk_f32_fp8_e32 v[168:169], v131
	v_cvt_pk_f32_fp8_sdwa v[170:171], v131 src0_sel:WORD_1
	v_pk_fma_f32 v[188:189], v[168:169], s[10:11], v[188:189] op_sel_hi:[1,0,1]
	v_pk_fma_f32 v[190:191], v[170:171], s[10:11], v[190:191] op_sel_hi:[1,0,1]
	v_cvt_pk_f32_fp8_e32 v[172:173], v135
	v_cvt_pk_f32_fp8_sdwa v[174:175], v135 src0_sel:WORD_1
	v_pk_fma_f32 v[188:189], v[172:173], s[10:11], v[188:189] op_sel_hi:[1,0,1]
	v_pk_fma_f32 v[190:191], v[174:175], s[10:11], v[190:191] op_sel_hi:[1,0,1]
	global_store_dwordx4 v159, v[188:191], s[4:5] offset:3072
	v_lshl_add_u32 v200, v20, 2, s23
	v_lshl_add_u32 v201, v21, 2, s23
	v_lshl_add_u32 v202, v22, 2, s23
	v_lshl_add_u32 v203, v23, 2, s23
	ds_read_b32 v148, v200
	ds_read_b32 v149, v201
	ds_read_b32 v150, v202
	ds_read_b32 v151, v203
	s_waitcnt lgkmcnt(0)
; __device__ __forceinline__ float bf_lo(unsigned w) { return __uint_as_float(w << 16); }
; __device__ __forceinline__ float bf_hi(unsigned w) { return __uint_as_float(w & 0xffff0000u); }
; __global__ void __launch_bounds__(512, 2) fwd_kernel(Params p) {
;     ...
;             for (int u = 0; u < UN; ++u) { const int it = it0 + u * NGT < NI ? it0 + u * NGT : it0; mm[u] = it >> 7; cc[u] = (it & 127) * 16;
;                 const i32x4 e4 = *(const i32x4*)(tok_e + mm[u] * 4), r4 = *(const i32x4*)(tok_rank + mm[u] * 4);
; #pragma unroll
;                 for (int k = 0; k < 4; ++k) { ee[u][k] = e4[k]; rk[u][k] = r4[k]; }
;                 const bf16_t* xp = X1 + (size_t)mm[u] * DM + cc[u]; xa[u] = *(const u32x4*)xp; xb[u] = *(const u32x4*)(xp + 8); }
; #pragma unroll
;             for (int u = 0; u < UN; ++u)
; #pragma unroll
;                 for (int k = 0; k < 4; ++k) { const int pos = ts[ee[u][k]] * 256 + rk[u][k]; y[u][k] = *(const u32x4*)(Yb + (size_t)pos * DM + cc[u]); }
;     ...
;             for (int u = 0; u < UN; ++u) {
;                 f32x4 a[4];
;                 a[0] = (f32x4){bf_lo(xa[u].x), bf_hi(xa[u].x), bf_lo(xa[u].y), bf_hi(xa[u].y)}; a[1] = (f32x4){bf_lo(xa[u].z), bf_hi(xa[u].z), bf_lo(xa[u].w), bf_hi(xa[u].w)};
;                 a[2] = (f32x4){bf_lo(xb[u].x), bf_hi(xb[u].x), bf_lo(xb[u].y), bf_hi(xb[u].y)}; a[3] = (f32x4){bf_lo(xb[u].z), bf_hi(xb[u].z), bf_lo(xb[u].w), bf_hi(xb[u].w)};
; #pragma unroll
;                 for (int k = 0; k < 4; ++k)
; #pragma unroll
;                     for (int q = 0; q < 4; ++q) { const f32x2 lo = __builtin_amdgcn_cvt_pk_f32_fp8((int)y[u][k][q], false), hi = __builtin_amdgcn_cvt_pk_f32_fp8((int)y[u][k][q], true);
;                         a[q].x += lo.x * (1.0f / Y8_SCALE); a[q].y += lo.y * (1.0f / Y8_SCALE); a[q].z += hi.x * (1.0f / Y8_SCALE); a[q].w += hi.y * (1.0f / Y8_SCALE); }
;                 if (it0 + u * NGT < NI) { float* op = p.out + (size_t)mm[u] * DM + cc[u];
; #pragma unroll
;                     for (int q = 0; q < 4; ++q) *(f32x4*)(op + 4 * q) = a[q]; }
	v_lshl_add_u32 v148, v148, 8, v36
	v_lshl_add_u32 v149, v149, 8, v37
	v_lshl_add_u32 v150, v150, 8, v38
	v_lshl_add_u32 v151, v151, 8, v39
	v_lshl_add_u32 v148, v148, 11, v4
	v_lshl_add_u32 v149, v149, 11, v4
	v_lshl_add_u32 v150, v150, 11, v4
	v_lshl_add_u32 v151, v151, 11, v4
	global_load_dword v120, v148, s[6:7]
	global_load_dword v121, v148, s[6:7] offset:256
	global_load_dword v122, v148, s[6:7] offset:512
	global_load_dword v123, v148, s[6:7] offset:768
	global_load_dword v124, v149, s[6:7]
	global_load_dword v125, v149, s[6:7] offset:256
	global_load_dword v126, v149, s[6:7] offset:512
	global_load_dword v127, v149, s[6:7] offset:768
	global_load_dword v128, v150, s[6:7]
	global_load_dword v129, v150, s[6:7] offset:256
	global_load_dword v130, v150, s[6:7] offset:512
	global_load_dword v131, v150, s[6:7] offset:768
	global_load_dword v132, v151, s[6:7]
	global_load_dword v133, v151, s[6:7] offset:256
	global_load_dword v134, v151, s[6:7] offset:512
	global_load_dword v135, v151, s[6:7] offset:768
	v_add_u32_e32 v192, 0x2000, v3
	v_lshlrev_b32_e32 v196, 4, v192
	v_lshl_add_u32 v156, v192, 13, v6
	v_add_u32_e32 v193, 0x2400, v3
	v_lshlrev_b32_e32 v197, 4, v193
	v_lshl_add_u32 v157, v193, 13, v6
	v_add_u32_e32 v194, 0x2800, v3
	v_lshlrev_b32_e32 v198, 4, v194
	v_lshl_add_u32 v158, v194, 13, v6
	v_add_u32_e32 v195, 0x2c00, v3
	v_lshlrev_b32_e32 v199, 4, v195
	v_lshl_add_u32 v159, v195, 13, v6
	global_load_dwordx4 v[8:11], v196, s[16:17]
	global_load_dwordx4 v[12:15], v197, s[16:17]
	global_load_dwordx4 v[16:19], v198, s[16:17]
	global_load_dwordx4 v[20:23], v199, s[16:17]
	global_load_dwordx4 v[24:27], v196, s[18:19]
	global_load_dwordx4 v[28:31], v197, s[18:19]
	global_load_dwordx4 v[32:35], v198, s[18:19]
	global_load_dwordx4 v[36:39], v199, s[18:19]
	v_lshl_add_u32 v196, v192, 12, v5
	global_load_dwordx2 v[40:41], v196, s[14:15]
	global_load_dwordx2 v[42:43], v196, s[14:15] offset:512
	global_load_dwordx2 v[44:45], v196, s[14:15] offset:1024
	global_load_dwordx2 v[46:47], v196, s[14:15] offset:1536
	v_lshl_add_u32 v197, v193, 12, v5
	global_load_dwordx2 v[48:49], v197, s[14:15]
	global_load_dwordx2 v[50:51], v197, s[14:15] offset:512
	global_load_dwordx2 v[52:53], v197, s[14:15] offset:1024
	global_load_dwordx2 v[54:55], v197, s[14:15] offset:1536
	v_lshl_add_u32 v198, v194, 12, v5
	global_load_dwordx2 v[56:57], v198, s[14:15]
	global_load_dwordx2 v[58:59], v198, s[14:15] offset:512
	global_load_dwordx2 v[60:61], v198, s[14:15] offset:1024
	global_load_dwordx2 v[62:63], v198, s[14:15] offset:1536
	v_lshl_add_u32 v199, v195, 12, v5
	global_load_dwordx2 v[64:65], v199, s[14:15]
	global_load_dwordx2 v[66:67], v199, s[14:15] offset:512
	global_load_dwordx2 v[68:69], v199, s[14:15] offset:1024
	global_load_dwordx2 v[70:71], v199, s[14:15] offset:1536
	s_waitcnt vmcnt(63)
	v_lshlrev_b32_e32 v176, 16, v216
	v_and_b32_e32 v177, 0xffff0000, v216
	v_lshlrev_b32_e32 v178, 16, v217
	v_and_b32_e32 v179, 0xffff0000, v217
	v_cvt_pk_f32_fp8_e32 v[160:161], v72
	v_cvt_pk_f32_fp8_sdwa v[162:163], v72 src0_sel:WORD_1
	v_pk_fma_f32 v[176:177], v[160:161], s[10:11], v[176:177] op_sel_hi:[1,0,1]
	v_pk_fma_f32 v[178:179], v[162:163], s[10:11], v[178:179] op_sel_hi:[1,0,1]
	v_cvt_pk_f32_fp8_e32 v[164:165], v76
	v_cvt_pk_f32_fp8_sdwa v[166:167], v76 src0_sel:WORD_1
	v_pk_fma_f32 v[176:177], v[164:165], s[10:11], v[176:177] op_sel_hi:[1,0,1]
	v_pk_fma_f32 v[178:179], v[166:167], s[10:11], v[178:179] op_sel_hi:[1,0,1]
	v_cvt_pk_f32_fp8_e32 v[168:169], v80
	v_cvt_pk_f32_fp8_sdwa v[170:171], v80 src0_sel:WORD_1
	v_pk_fma_f32 v[176:177], v[168:169], s[10:11], v[176:177] op_sel_hi:[1,0,1]
	v_pk_fma_f32 v[178:179], v[170:171], s[10:11], v[178:179] op_sel_hi:[1,0,1]
	v_cvt_pk_f32_fp8_e32 v[172:173], v84
	v_cvt_pk_f32_fp8_sdwa v[174:175], v84 src0_sel:WORD_1
	v_pk_fma_f32 v[176:177], v[172:173], s[10:11], v[176:177] op_sel_hi:[1,0,1]
	v_pk_fma_f32 v[178:179], v[174:175], s[10:11], v[178:179] op_sel_hi:[1,0,1]
	global_store_dwordx4 v248, v[176:179], s[4:5]
	v_lshlrev_b32_e32 v180, 16, v218
	v_and_b32_e32 v181, 0xffff0000, v218
	v_lshlrev_b32_e32 v182, 16, v219
	v_and_b32_e32 v183, 0xffff0000, v219
	v_cvt_pk_f32_fp8_e32 v[160:161], v73
	v_cvt_pk_f32_fp8_sdwa v[162:163], v73 src0_sel:WORD_1
	v_pk_fma_f32 v[180:181], v[160:161], s[10:11], v[180:181] op_sel_hi:[1,0,1]
	v_pk_fma_f32 v[182:183], v[162:163], s[10:11], v[182:183] op_sel_hi:[1,0,1]
	v_cvt_pk_f32_fp8_e32 v[164:165], v77
	v_cvt_pk_f32_fp8_sdwa v[166:167], v77 src0_sel:WORD_1
	v_pk_fma_f32 v[180:181], v[164:165], s[10:11], v[180:181] op_sel_hi:[1,0,1]
	v_pk_fma_f32 v[182:183], v[166:167], s[10:11], v[182:183] op_sel_hi:[1,0,1]
	v_cvt_pk_f32_fp8_e32 v[168:169], v81
	v_cvt_pk_f32_fp8_sdwa v[170:171], v81 src0_sel:WORD_1
	v_pk_fma_f32 v[180:181], v[168:169], s[10:11], v[180:181] op_sel_hi:[1,0,1]
	v_pk_fma_f32 v[182:183], v[170:171], s[10:11], v[182:183] op_sel_hi:[1,0,1]
	v_cvt_pk_f32_fp8_e32 v[172:173], v85
	v_cvt_pk_f32_fp8_sdwa v[174:175], v85 src0_sel:WORD_1
	v_pk_fma_f32 v[180:181], v[172:173], s[10:11], v[180:181] op_sel_hi:[1,0,1]
	v_pk_fma_f32 v[182:183], v[174:175], s[10:11], v[182:183] op_sel_hi:[1,0,1]
	global_store_dwordx4 v248, v[180:183], s[4:5] offset:1024
	v_lshlrev_b32_e32 v184, 16, v220
	v_and_b32_e32 v185, 0xffff0000, v220
	v_lshlrev_b32_e32 v186, 16, v221
	v_and_b32_e32 v187, 0xffff0000, v221
	v_cvt_pk_f32_fp8_e32 v[160:161], v74
	v_cvt_pk_f32_fp8_sdwa v[162:163], v74 src0_sel:WORD_1
	v_pk_fma_f32 v[184:185], v[160:161], s[10:11], v[184:185] op_sel_hi:[1,0,1]
	v_pk_fma_f32 v[186:187], v[162:163], s[10:11], v[186:187] op_sel_hi:[1,0,1]
	v_cvt_pk_f32_fp8_e32 v[164:165], v78
; __device__ __forceinline__ float bf_lo(unsigned w) { return __uint_as_float(w << 16); }
; __device__ __forceinline__ float bf_hi(unsigned w) { return __uint_as_float(w & 0xffff0000u); }
; __global__ void __launch_bounds__(512, 2) fwd_kernel(Params p) {
;     ...
;             for (int u = 0; u < UN; ++u) { const int it = it0 + u * NGT < NI ? it0 + u * NGT : it0; mm[u] = it >> 7; cc[u] = (it & 127) * 16;
;                 const i32x4 e4 = *(const i32x4*)(tok_e + mm[u] * 4), r4 = *(const i32x4*)(tok_rank + mm[u] * 4);
; #pragma unroll
;                 for (int k = 0; k < 4; ++k) { ee[u][k] = e4[k]; rk[u][k] = r4[k]; }
;                 const bf16_t* xp = X1 + (size_t)mm[u] * DM + cc[u]; xa[u] = *(const u32x4*)xp; xb[u] = *(const u32x4*)(xp + 8); }
; #pragma unroll
;             for (int u = 0; u < UN; ++u)
; #pragma unroll
;                 for (int k = 0; k < 4; ++k) { const int pos = ts[ee[u][k]] * 256 + rk[u][k]; y[u][k] = *(const u32x4*)(Yb + (size_t)pos * DM + cc[u]); }
; #pragma unroll
;             for (int u = 0; u < UN; ++u) {
;                 f32x4 a[4];
;                 a[0] = (f32x4){bf_lo(xa[u].x), bf_hi(xa[u].x), bf_lo(xa[u].y), bf_hi(xa[u].y)}; a[1] = (f32x4){bf_lo(xa[u].z), bf_hi(xa[u].z), bf_lo(xa[u].w), bf_hi(xa[u].w)};
;                 a[2] = (f32x4){bf_lo(xb[u].x), bf_hi(xb[u].x), bf_lo(xb[u].y), bf_hi(xb[u].y)}; a[3] = (f32x4){bf_lo(xb[u].z), bf_hi(xb[u].z), bf_lo(xb[u].w), bf_hi(xb[u].w)};
; #pragma unroll
;                 for (int k = 0; k < 4; ++k)
; #pragma unroll
;                     for (int q = 0; q < 4; ++q) { const f32x2 lo = __builtin_amdgcn_cvt_pk_f32_fp8((int)y[u][k][q], false), hi = __builtin_amdgcn_cvt_pk_f32_fp8((int)y[u][k][q], true);
;                         a[q].x += lo.x * (1.0f / Y8_SCALE); a[q].y += lo.y * (1.0f / Y8_SCALE); a[q].z += hi.x * (1.0f / Y8_SCALE); a[q].w += hi.y * (1.0f / Y8_SCALE); }
;                 if (it0 + u * NGT < NI) { float* op = p.out + (size_t)mm[u] * DM + cc[u];
; #pragma unroll
;                     for (int q = 0; q < 4; ++q) *(f32x4*)(op + 4 * q) = a[q]; }
	v_cvt_pk_f32_fp8_sdwa v[166:167], v78 src0_sel:WORD_1
	v_pk_fma_f32 v[184:185], v[164:165], s[10:11], v[184:185] op_sel_hi:[1,0,1]
	v_pk_fma_f32 v[186:187], v[166:167], s[10:11], v[186:187] op_sel_hi:[1,0,1]
	v_cvt_pk_f32_fp8_e32 v[168:169], v82
	v_cvt_pk_f32_fp8_sdwa v[170:171], v82 src0_sel:WORD_1
	v_pk_fma_f32 v[184:185], v[168:169], s[10:11], v[184:185] op_sel_hi:[1,0,1]
	v_pk_fma_f32 v[186:187], v[170:171], s[10:11], v[186:187] op_sel_hi:[1,0,1]
	v_cvt_pk_f32_fp8_e32 v[172:173], v86
	v_cvt_pk_f32_fp8_sdwa v[174:175], v86 src0_sel:WORD_1
	v_pk_fma_f32 v[184:185], v[172:173], s[10:11], v[184:185] op_sel_hi:[1,0,1]
	v_pk_fma_f32 v[186:187], v[174:175], s[10:11], v[186:187] op_sel_hi:[1,0,1]
	global_store_dwordx4 v248, v[184:187], s[4:5] offset:2048
	v_lshlrev_b32_e32 v188, 16, v222
	v_and_b32_e32 v189, 0xffff0000, v222
	v_lshlrev_b32_e32 v190, 16, v223
	v_and_b32_e32 v191, 0xffff0000, v223
	v_cvt_pk_f32_fp8_e32 v[160:161], v75
	v_cvt_pk_f32_fp8_sdwa v[162:163], v75 src0_sel:WORD_1
	v_pk_fma_f32 v[188:189], v[160:161], s[10:11], v[188:189] op_sel_hi:[1,0,1]
	v_pk_fma_f32 v[190:191], v[162:163], s[10:11], v[190:191] op_sel_hi:[1,0,1]
	v_cvt_pk_f32_fp8_e32 v[164:165], v79
	v_cvt_pk_f32_fp8_sdwa v[166:167], v79 src0_sel:WORD_1
	v_pk_fma_f32 v[188:189], v[164:165], s[10:11], v[188:189] op_sel_hi:[1,0,1]
	v_pk_fma_f32 v[190:191], v[166:167], s[10:11], v[190:191] op_sel_hi:[1,0,1]
	v_cvt_pk_f32_fp8_e32 v[168:169], v83
	v_cvt_pk_f32_fp8_sdwa v[170:171], v83 src0_sel:WORD_1
	v_pk_fma_f32 v[188:189], v[168:169], s[10:11], v[188:189] op_sel_hi:[1,0,1]
	v_pk_fma_f32 v[190:191], v[170:171], s[10:11], v[190:191] op_sel_hi:[1,0,1]
	v_cvt_pk_f32_fp8_e32 v[172:173], v87
	v_cvt_pk_f32_fp8_sdwa v[174:175], v87 src0_sel:WORD_1
	v_pk_fma_f32 v[188:189], v[172:173], s[10:11], v[188:189] op_sel_hi:[1,0,1]
	v_pk_fma_f32 v[190:191], v[174:175], s[10:11], v[190:191] op_sel_hi:[1,0,1]
	global_store_dwordx4 v248, v[188:191], s[4:5] offset:3072
	s_waitcnt vmcnt(20)
	v_lshl_add_u32 v200, v8, 2, s23
	v_lshl_add_u32 v201, v9, 2, s23
	v_lshl_add_u32 v202, v10, 2, s23
	v_lshl_add_u32 v203, v11, 2, s23
	ds_read_b32 v136, v200
	ds_read_b32 v137, v201
	ds_read_b32 v138, v202
	ds_read_b32 v139, v203
	s_waitcnt lgkmcnt(0)
	v_lshl_add_u32 v136, v136, 8, v24
	v_lshl_add_u32 v137, v137, 8, v25
	v_lshl_add_u32 v138, v138, 8, v26
	v_lshl_add_u32 v139, v139, 8, v27
	v_lshl_add_u32 v136, v136, 11, v4
	v_lshl_add_u32 v137, v137, 11, v4
	v_lshl_add_u32 v138, v138, 11, v4
	v_lshl_add_u32 v139, v139, 11, v4
	global_load_dword v72, v136, s[6:7]
	global_load_dword v73, v136, s[6:7] offset:256
	global_load_dword v74, v136, s[6:7] offset:512
	global_load_dword v75, v136, s[6:7] offset:768
	global_load_dword v76, v137, s[6:7]
	global_load_dword v77, v137, s[6:7] offset:256
	global_load_dword v78, v137, s[6:7] offset:512
	global_load_dword v79, v137, s[6:7] offset:768
	global_load_dword v80, v138, s[6:7]
	global_load_dword v81, v138, s[6:7] offset:256
	global_load_dword v82, v138, s[6:7] offset:512
	global_load_dword v83, v138, s[6:7] offset:768
	global_load_dword v84, v139, s[6:7]
	global_load_dword v85, v139, s[6:7] offset:256
	global_load_dword v86, v139, s[6:7] offset:512
	global_load_dword v87, v139, s[6:7] offset:768
	s_waitcnt vmcnt(63)
	v_lshlrev_b32_e32 v176, 16, v224
	v_and_b32_e32 v177, 0xffff0000, v224
	v_lshlrev_b32_e32 v178, 16, v225
	v_and_b32_e32 v179, 0xffff0000, v225
	v_cvt_pk_f32_fp8_e32 v[160:161], v88
	v_cvt_pk_f32_fp8_sdwa v[162:163], v88 src0_sel:WORD_1
	v_pk_fma_f32 v[176:177], v[160:161], s[10:11], v[176:177] op_sel_hi:[1,0,1]
	v_pk_fma_f32 v[178:179], v[162:163], s[10:11], v[178:179] op_sel_hi:[1,0,1]
	v_cvt_pk_f32_fp8_e32 v[164:165], v92
	v_cvt_pk_f32_fp8_sdwa v[166:167], v92 src0_sel:WORD_1
	v_pk_fma_f32 v[176:177], v[164:165], s[10:11], v[176:177] op_sel_hi:[1,0,1]
	v_pk_fma_f32 v[178:179], v[166:167], s[10:11], v[178:179] op_sel_hi:[1,0,1]
	v_cvt_pk_f32_fp8_e32 v[168:169], v96
	v_cvt_pk_f32_fp8_sdwa v[170:171], v96 src0_sel:WORD_1
	v_pk_fma_f32 v[176:177], v[168:169], s[10:11], v[176:177] op_sel_hi:[1,0,1]
	v_pk_fma_f32 v[178:179], v[170:171], s[10:11], v[178:179] op_sel_hi:[1,0,1]
	v_cvt_pk_f32_fp8_e32 v[172:173], v100
	v_cvt_pk_f32_fp8_sdwa v[174:175], v100 src0_sel:WORD_1
	v_pk_fma_f32 v[176:177], v[172:173], s[10:11], v[176:177] op_sel_hi:[1,0,1]
	v_pk_fma_f32 v[178:179], v[174:175], s[10:11], v[178:179] op_sel_hi:[1,0,1]
	global_store_dwordx4 v249, v[176:179], s[4:5]
	v_lshlrev_b32_e32 v180, 16, v226
	v_and_b32_e32 v181, 0xffff0000, v226
	v_lshlrev_b32_e32 v182, 16, v227
	v_and_b32_e32 v183, 0xffff0000, v227
	v_cvt_pk_f32_fp8_e32 v[160:161], v89
	v_cvt_pk_f32_fp8_sdwa v[162:163], v89 src0_sel:WORD_1
	v_pk_fma_f32 v[180:181], v[160:161], s[10:11], v[180:181] op_sel_hi:[1,0,1]
	v_pk_fma_f32 v[182:183], v[162:163], s[10:11], v[182:183] op_sel_hi:[1,0,1]
	v_cvt_pk_f32_fp8_e32 v[164:165], v93
	v_cvt_pk_f32_fp8_sdwa v[166:167], v93 src0_sel:WORD_1
	v_pk_fma_f32 v[180:181], v[164:165], s[10:11], v[180:181] op_sel_hi:[1,0,1]
	v_pk_fma_f32 v[182:183], v[166:167], s[10:11], v[182:183] op_sel_hi:[1,0,1]
	v_cvt_pk_f32_fp8_e32 v[168:169], v97
	v_cvt_pk_f32_fp8_sdwa v[170:171], v97 src0_sel:WORD_1
	v_pk_fma_f32 v[180:181], v[168:169], s[10:11], v[180:181] op_sel_hi:[1,0,1]
	v_pk_fma_f32 v[182:183], v[170:171], s[10:11], v[182:183] op_sel_hi:[1,0,1]
	v_cvt_pk_f32_fp8_e32 v[172:173], v101
	v_cvt_pk_f32_fp8_sdwa v[174:175], v101 src0_sel:WORD_1
	v_pk_fma_f32 v[180:181], v[172:173], s[10:11], v[180:181] op_sel_hi:[1,0,1]
	v_pk_fma_f32 v[182:183], v[174:175], s[10:11], v[182:183] op_sel_hi:[1,0,1]
	global_store_dwordx4 v249, v[180:183], s[4:5] offset:1024
; __device__ __forceinline__ float bf_lo(unsigned w) { return __uint_as_float(w << 16); }
; __device__ __forceinline__ float bf_hi(unsigned w) { return __uint_as_float(w & 0xffff0000u); }
; __global__ void __launch_bounds__(512, 2) fwd_kernel(Params p) {
;     ...
;             for (int u = 0; u < UN; ++u) { const int it = it0 + u * NGT < NI ? it0 + u * NGT : it0; mm[u] = it >> 7; cc[u] = (it & 127) * 16;
;                 const i32x4 e4 = *(const i32x4*)(tok_e + mm[u] * 4), r4 = *(const i32x4*)(tok_rank + mm[u] * 4);
; #pragma unroll
;                 for (int k = 0; k < 4; ++k) { ee[u][k] = e4[k]; rk[u][k] = r4[k]; }
;                 const bf16_t* xp = X1 + (size_t)mm[u] * DM + cc[u]; xa[u] = *(const u32x4*)xp; xb[u] = *(const u32x4*)(xp + 8); }
; #pragma unroll
;             for (int u = 0; u < UN; ++u)
; #pragma unroll
;                 for (int k = 0; k < 4; ++k) { const int pos = ts[ee[u][k]] * 256 + rk[u][k]; y[u][k] = *(const u32x4*)(Yb + (size_t)pos * DM + cc[u]); }
; #pragma unroll
;             for (int u = 0; u < UN; ++u) {
;                 f32x4 a[4];
;                 a[0] = (f32x4){bf_lo(xa[u].x), bf_hi(xa[u].x), bf_lo(xa[u].y), bf_hi(xa[u].y)}; a[1] = (f32x4){bf_lo(xa[u].z), bf_hi(xa[u].z), bf_lo(xa[u].w), bf_hi(xa[u].w)};
;                 a[2] = (f32x4){bf_lo(xb[u].x), bf_hi(xb[u].x), bf_lo(xb[u].y), bf_hi(xb[u].y)}; a[3] = (f32x4){bf_lo(xb[u].z), bf_hi(xb[u].z), bf_lo(xb[u].w), bf_hi(xb[u].w)};
; #pragma unroll
;                 for (int k = 0; k < 4; ++k)
; #pragma unroll
;                     for (int q = 0; q < 4; ++q) { const f32x2 lo = __builtin_amdgcn_cvt_pk_f32_fp8((int)y[u][k][q], false), hi = __builtin_amdgcn_cvt_pk_f32_fp8((int)y[u][k][q], true);
;                         a[q].x += lo.x * (1.0f / Y8_SCALE); a[q].y += lo.y * (1.0f / Y8_SCALE); a[q].z += hi.x * (1.0f / Y8_SCALE); a[q].w += hi.y * (1.0f / Y8_SCALE); }
;                 if (it0 + u * NGT < NI) { float* op = p.out + (size_t)mm[u] * DM + cc[u];
; #pragma unroll
;                     for (int q = 0; q < 4; ++q) *(f32x4*)(op + 4 * q) = a[q]; }
	v_lshlrev_b32_e32 v184, 16, v228
	v_and_b32_e32 v185, 0xffff0000, v228
	v_lshlrev_b32_e32 v186, 16, v229
	v_and_b32_e32 v187, 0xffff0000, v229
	v_cvt_pk_f32_fp8_e32 v[160:161], v90
	v_cvt_pk_f32_fp8_sdwa v[162:163], v90 src0_sel:WORD_1
	v_pk_fma_f32 v[184:185], v[160:161], s[10:11], v[184:185] op_sel_hi:[1,0,1]
	v_pk_fma_f32 v[186:187], v[162:163], s[10:11], v[186:187] op_sel_hi:[1,0,1]
	v_cvt_pk_f32_fp8_e32 v[164:165], v94
	v_cvt_pk_f32_fp8_sdwa v[166:167], v94 src0_sel:WORD_1
	v_pk_fma_f32 v[184:185], v[164:165], s[10:11], v[184:185] op_sel_hi:[1,0,1]
	v_pk_fma_f32 v[186:187], v[166:167], s[10:11], v[186:187] op_sel_hi:[1,0,1]
	v_cvt_pk_f32_fp8_e32 v[168:169], v98
	v_cvt_pk_f32_fp8_sdwa v[170:171], v98 src0_sel:WORD_1
	v_pk_fma_f32 v[184:185], v[168:169], s[10:11], v[184:185] op_sel_hi:[1,0,1]
	v_pk_fma_f32 v[186:187], v[170:171], s[10:11], v[186:187] op_sel_hi:[1,0,1]
	v_cvt_pk_f32_fp8_e32 v[172:173], v102
	v_cvt_pk_f32_fp8_sdwa v[174:175], v102 src0_sel:WORD_1
	v_pk_fma_f32 v[184:185], v[172:173], s[10:11], v[184:185] op_sel_hi:[1,0,1]
	v_pk_fma_f32 v[186:187], v[174:175], s[10:11], v[186:187] op_sel_hi:[1,0,1]
	global_store_dwordx4 v249, v[184:187], s[4:5] offset:2048
	v_lshlrev_b32_e32 v188, 16, v230
	v_and_b32_e32 v189, 0xffff0000, v230
	v_lshlrev_b32_e32 v190, 16, v231
	v_and_b32_e32 v191, 0xffff0000, v231
	v_cvt_pk_f32_fp8_e32 v[160:161], v91
	v_cvt_pk_f32_fp8_sdwa v[162:163], v91 src0_sel:WORD_1
	v_pk_fma_f32 v[188:189], v[160:161], s[10:11], v[188:189] op_sel_hi:[1,0,1]
	v_pk_fma_f32 v[190:191], v[162:163], s[10:11], v[190:191] op_sel_hi:[1,0,1]
	v_cvt_pk_f32_fp8_e32 v[164:165], v95
	v_cvt_pk_f32_fp8_sdwa v[166:167], v95 src0_sel:WORD_1
	v_pk_fma_f32 v[188:189], v[164:165], s[10:11], v[188:189] op_sel_hi:[1,0,1]
	v_pk_fma_f32 v[190:191], v[166:167], s[10:11], v[190:191] op_sel_hi:[1,0,1]
	v_cvt_pk_f32_fp8_e32 v[168:169], v99
	v_cvt_pk_f32_fp8_sdwa v[170:171], v99 src0_sel:WORD_1
	v_pk_fma_f32 v[188:189], v[168:169], s[10:11], v[188:189] op_sel_hi:[1,0,1]
	v_pk_fma_f32 v[190:191], v[170:171], s[10:11], v[190:191] op_sel_hi:[1,0,1]
	v_cvt_pk_f32_fp8_e32 v[172:173], v103
	v_cvt_pk_f32_fp8_sdwa v[174:175], v103 src0_sel:WORD_1
	v_pk_fma_f32 v[188:189], v[172:173], s[10:11], v[188:189] op_sel_hi:[1,0,1]
	v_pk_fma_f32 v[190:191], v[174:175], s[10:11], v[190:191] op_sel_hi:[1,0,1]
	global_store_dwordx4 v249, v[188:191], s[4:5] offset:3072
	v_lshl_add_u32 v200, v12, 2, s23
	v_lshl_add_u32 v201, v13, 2, s23
	v_lshl_add_u32 v202, v14, 2, s23
	v_lshl_add_u32 v203, v15, 2, s23
	ds_read_b32 v140, v200
	ds_read_b32 v141, v201
	ds_read_b32 v142, v202
	ds_read_b32 v143, v203
	s_waitcnt lgkmcnt(0)
	v_lshl_add_u32 v140, v140, 8, v28
	v_lshl_add_u32 v141, v141, 8, v29
	v_lshl_add_u32 v142, v142, 8, v30
	v_lshl_add_u32 v143, v143, 8, v31
	v_lshl_add_u32 v140, v140, 11, v4
	v_lshl_add_u32 v141, v141, 11, v4
	v_lshl_add_u32 v142, v142, 11, v4
	v_lshl_add_u32 v143, v143, 11, v4
	global_load_dword v88, v140, s[6:7]
	global_load_dword v89, v140, s[6:7] offset:256
	global_load_dword v90, v140, s[6:7] offset:512
	global_load_dword v91, v140, s[6:7] offset:768
	global_load_dword v92, v141, s[6:7]
	global_load_dword v93, v141, s[6:7] offset:256
	global_load_dword v94, v141, s[6:7] offset:512
	global_load_dword v95, v141, s[6:7] offset:768
	global_load_dword v96, v142, s[6:7]
	global_load_dword v97, v142, s[6:7] offset:256
	global_load_dword v98, v142, s[6:7] offset:512
	global_load_dword v99, v142, s[6:7] offset:768
	global_load_dword v100, v143, s[6:7]
	global_load_dword v101, v143, s[6:7] offset:256
	global_load_dword v102, v143, s[6:7] offset:512
	global_load_dword v103, v143, s[6:7] offset:768
	s_waitcnt vmcnt(63)
	v_lshlrev_b32_e32 v176, 16, v232
	v_and_b32_e32 v177, 0xffff0000, v232
	v_lshlrev_b32_e32 v178, 16, v233
	v_and_b32_e32 v179, 0xffff0000, v233
	v_cvt_pk_f32_fp8_e32 v[160:161], v104
	v_cvt_pk_f32_fp8_sdwa v[162:163], v104 src0_sel:WORD_1
	v_pk_fma_f32 v[176:177], v[160:161], s[10:11], v[176:177] op_sel_hi:[1,0,1]
	v_pk_fma_f32 v[178:179], v[162:163], s[10:11], v[178:179] op_sel_hi:[1,0,1]
	v_cvt_pk_f32_fp8_e32 v[164:165], v108
	v_cvt_pk_f32_fp8_sdwa v[166:167], v108 src0_sel:WORD_1
	v_pk_fma_f32 v[176:177], v[164:165], s[10:11], v[176:177] op_sel_hi:[1,0,1]
	v_pk_fma_f32 v[178:179], v[166:167], s[10:11], v[178:179] op_sel_hi:[1,0,1]
	v_cvt_pk_f32_fp8_e32 v[168:169], v112
	v_cvt_pk_f32_fp8_sdwa v[170:171], v112 src0_sel:WORD_1
	v_pk_fma_f32 v[176:177], v[168:169], s[10:11], v[176:177] op_sel_hi:[1,0,1]
	v_pk_fma_f32 v[178:179], v[170:171], s[10:11], v[178:179] op_sel_hi:[1,0,1]
	v_cvt_pk_f32_fp8_e32 v[172:173], v116
	v_cvt_pk_f32_fp8_sdwa v[174:175], v116 src0_sel:WORD_1
	v_pk_fma_f32 v[176:177], v[172:173], s[10:11], v[176:177] op_sel_hi:[1,0,1]
	v_pk_fma_f32 v[178:179], v[174:175], s[10:11], v[178:179] op_sel_hi:[1,0,1]
	global_store_dwordx4 v250, v[176:179], s[4:5]
	v_lshlrev_b32_e32 v180, 16, v234
	v_and_b32_e32 v181, 0xffff0000, v234
	v_lshlrev_b32_e32 v182, 16, v235
	v_and_b32_e32 v183, 0xffff0000, v235
	v_cvt_pk_f32_fp8_e32 v[160:161], v105
	v_cvt_pk_f32_fp8_sdwa v[162:163], v105 src0_sel:WORD_1
	v_pk_fma_f32 v[180:181], v[160:161], s[10:11], v[180:181] op_sel_hi:[1,0,1]
	v_pk_fma_f32 v[182:183], v[162:163], s[10:11], v[182:183] op_sel_hi:[1,0,1]
	v_cvt_pk_f32_fp8_e32 v[164:165], v109
	v_cvt_pk_f32_fp8_sdwa v[166:167], v109 src0_sel:WORD_1
	v_pk_fma_f32 v[180:181], v[164:165], s[10:11], v[180:181] op_sel_hi:[1,0,1]
	v_pk_fma_f32 v[182:183], v[166:167], s[10:11], v[182:183] op_sel_hi:[1,0,1]
	v_cvt_pk_f32_fp8_e32 v[168:169], v113
	v_cvt_pk_f32_fp8_sdwa v[170:171], v113 src0_sel:WORD_1
	v_pk_fma_f32 v[180:181], v[168:169], s[10:11], v[180:181] op_sel_hi:[1,0,1]
; __device__ __forceinline__ float bf_lo(unsigned w) { return __uint_as_float(w << 16); }
; __device__ __forceinline__ float bf_hi(unsigned w) { return __uint_as_float(w & 0xffff0000u); }
; __global__ void __launch_bounds__(512, 2) fwd_kernel(Params p) {
;     ...
;             for (int u = 0; u < UN; ++u) { const int it = it0 + u * NGT < NI ? it0 + u * NGT : it0; mm[u] = it >> 7; cc[u] = (it & 127) * 16;
;                 const i32x4 e4 = *(const i32x4*)(tok_e + mm[u] * 4), r4 = *(const i32x4*)(tok_rank + mm[u] * 4);
; #pragma unroll
;                 for (int k = 0; k < 4; ++k) { ee[u][k] = e4[k]; rk[u][k] = r4[k]; }
;                 const bf16_t* xp = X1 + (size_t)mm[u] * DM + cc[u]; xa[u] = *(const u32x4*)xp; xb[u] = *(const u32x4*)(xp + 8); }
; #pragma unroll
;             for (int u = 0; u < UN; ++u)
; #pragma unroll
;                 for (int k = 0; k < 4; ++k) { const int pos = ts[ee[u][k]] * 256 + rk[u][k]; y[u][k] = *(const u32x4*)(Yb + (size_t)pos * DM + cc[u]); }
; #pragma unroll
;             for (int u = 0; u < UN; ++u) {
;                 f32x4 a[4];
;                 a[0] = (f32x4){bf_lo(xa[u].x), bf_hi(xa[u].x), bf_lo(xa[u].y), bf_hi(xa[u].y)}; a[1] = (f32x4){bf_lo(xa[u].z), bf_hi(xa[u].z), bf_lo(xa[u].w), bf_hi(xa[u].w)};
;                 a[2] = (f32x4){bf_lo(xb[u].x), bf_hi(xb[u].x), bf_lo(xb[u].y), bf_hi(xb[u].y)}; a[3] = (f32x4){bf_lo(xb[u].z), bf_hi(xb[u].z), bf_lo(xb[u].w), bf_hi(xb[u].w)};
; #pragma unroll
;                 for (int k = 0; k < 4; ++k)
; #pragma unroll
;                     for (int q = 0; q < 4; ++q) { const f32x2 lo = __builtin_amdgcn_cvt_pk_f32_fp8((int)y[u][k][q], false), hi = __builtin_amdgcn_cvt_pk_f32_fp8((int)y[u][k][q], true);
;                         a[q].x += lo.x * (1.0f / Y8_SCALE); a[q].y += lo.y * (1.0f / Y8_SCALE); a[q].z += hi.x * (1.0f / Y8_SCALE); a[q].w += hi.y * (1.0f / Y8_SCALE); }
;                 if (it0 + u * NGT < NI) { float* op = p.out + (size_t)mm[u] * DM + cc[u];
; #pragma unroll
;                     for (int q = 0; q < 4; ++q) *(f32x4*)(op + 4 * q) = a[q]; }
	v_pk_fma_f32 v[182:183], v[170:171], s[10:11], v[182:183] op_sel_hi:[1,0,1]
	v_cvt_pk_f32_fp8_e32 v[172:173], v117
	v_cvt_pk_f32_fp8_sdwa v[174:175], v117 src0_sel:WORD_1
	v_pk_fma_f32 v[180:181], v[172:173], s[10:11], v[180:181] op_sel_hi:[1,0,1]
	v_pk_fma_f32 v[182:183], v[174:175], s[10:11], v[182:183] op_sel_hi:[1,0,1]
	global_store_dwordx4 v250, v[180:183], s[4:5] offset:1024
	v_lshlrev_b32_e32 v184, 16, v236
	v_and_b32_e32 v185, 0xffff0000, v236
	v_lshlrev_b32_e32 v186, 16, v237
	v_and_b32_e32 v187, 0xffff0000, v237
	v_cvt_pk_f32_fp8_e32 v[160:161], v106
	v_cvt_pk_f32_fp8_sdwa v[162:163], v106 src0_sel:WORD_1
	v_pk_fma_f32 v[184:185], v[160:161], s[10:11], v[184:185] op_sel_hi:[1,0,1]
	v_pk_fma_f32 v[186:187], v[162:163], s[10:11], v[186:187] op_sel_hi:[1,0,1]
	v_cvt_pk_f32_fp8_e32 v[164:165], v110
	v_cvt_pk_f32_fp8_sdwa v[166:167], v110 src0_sel:WORD_1
	v_pk_fma_f32 v[184:185], v[164:165], s[10:11], v[184:185] op_sel_hi:[1,0,1]
	v_pk_fma_f32 v[186:187], v[166:167], s[10:11], v[186:187] op_sel_hi:[1,0,1]
	v_cvt_pk_f32_fp8_e32 v[168:169], v114
	v_cvt_pk_f32_fp8_sdwa v[170:171], v114 src0_sel:WORD_1
	v_pk_fma_f32 v[184:185], v[168:169], s[10:11], v[184:185] op_sel_hi:[1,0,1]
	v_pk_fma_f32 v[186:187], v[170:171], s[10:11], v[186:187] op_sel_hi:[1,0,1]
	v_cvt_pk_f32_fp8_e32 v[172:173], v118
	v_cvt_pk_f32_fp8_sdwa v[174:175], v118 src0_sel:WORD_1
	v_pk_fma_f32 v[184:185], v[172:173], s[10:11], v[184:185] op_sel_hi:[1,0,1]
	v_pk_fma_f32 v[186:187], v[174:175], s[10:11], v[186:187] op_sel_hi:[1,0,1]
	global_store_dwordx4 v250, v[184:187], s[4:5] offset:2048
	v_lshlrev_b32_e32 v188, 16, v238
	v_and_b32_e32 v189, 0xffff0000, v238
	v_lshlrev_b32_e32 v190, 16, v239
	v_and_b32_e32 v191, 0xffff0000, v239
	v_cvt_pk_f32_fp8_e32 v[160:161], v107
	v_cvt_pk_f32_fp8_sdwa v[162:163], v107 src0_sel:WORD_1
	v_pk_fma_f32 v[188:189], v[160:161], s[10:11], v[188:189] op_sel_hi:[1,0,1]
	v_pk_fma_f32 v[190:191], v[162:163], s[10:11], v[190:191] op_sel_hi:[1,0,1]
	v_cvt_pk_f32_fp8_e32 v[164:165], v111
	v_cvt_pk_f32_fp8_sdwa v[166:167], v111 src0_sel:WORD_1
	v_pk_fma_f32 v[188:189], v[164:165], s[10:11], v[188:189] op_sel_hi:[1,0,1]
	v_pk_fma_f32 v[190:191], v[166:167], s[10:11], v[190:191] op_sel_hi:[1,0,1]
	v_cvt_pk_f32_fp8_e32 v[168:169], v115
	v_cvt_pk_f32_fp8_sdwa v[170:171], v115 src0_sel:WORD_1
	v_pk_fma_f32 v[188:189], v[168:169], s[10:11], v[188:189] op_sel_hi:[1,0,1]
	v_pk_fma_f32 v[190:191], v[170:171], s[10:11], v[190:191] op_sel_hi:[1,0,1]
	v_cvt_pk_f32_fp8_e32 v[172:173], v119
	v_cvt_pk_f32_fp8_sdwa v[174:175], v119 src0_sel:WORD_1
	v_pk_fma_f32 v[188:189], v[172:173], s[10:11], v[188:189] op_sel_hi:[1,0,1]
	v_pk_fma_f32 v[190:191], v[174:175], s[10:11], v[190:191] op_sel_hi:[1,0,1]
	global_store_dwordx4 v250, v[188:191], s[4:5] offset:3072
	v_lshl_add_u32 v200, v16, 2, s23
	v_lshl_add_u32 v201, v17, 2, s23
	v_lshl_add_u32 v202, v18, 2, s23
	v_lshl_add_u32 v203, v19, 2, s23
	ds_read_b32 v144, v200
	ds_read_b32 v145, v201
	ds_read_b32 v146, v202
	ds_read_b32 v147, v203
	s_waitcnt lgkmcnt(0)
	v_lshl_add_u32 v144, v144, 8, v32
	v_lshl_add_u32 v145, v145, 8, v33
	v_lshl_add_u32 v146, v146, 8, v34
	v_lshl_add_u32 v147, v147, 8, v35
	v_lshl_add_u32 v144, v144, 11, v4
	v_lshl_add_u32 v145, v145, 11, v4
	v_lshl_add_u32 v146, v146, 11, v4
	v_lshl_add_u32 v147, v147, 11, v4
	global_load_dword v104, v144, s[6:7]
	global_load_dword v105, v144, s[6:7] offset:256
	global_load_dword v106, v144, s[6:7] offset:512
	global_load_dword v107, v144, s[6:7] offset:768
	global_load_dword v108, v145, s[6:7]
	global_load_dword v109, v145, s[6:7] offset:256
	global_load_dword v110, v145, s[6:7] offset:512
	global_load_dword v111, v145, s[6:7] offset:768
	global_load_dword v112, v146, s[6:7]
	global_load_dword v113, v146, s[6:7] offset:256
	global_load_dword v114, v146, s[6:7] offset:512
	global_load_dword v115, v146, s[6:7] offset:768
	global_load_dword v116, v147, s[6:7]
	global_load_dword v117, v147, s[6:7] offset:256
	global_load_dword v118, v147, s[6:7] offset:512
	global_load_dword v119, v147, s[6:7] offset:768
	s_waitcnt vmcnt(63)
	v_lshlrev_b32_e32 v176, 16, v240
	v_and_b32_e32 v177, 0xffff0000, v240
	v_lshlrev_b32_e32 v178, 16, v241
	v_and_b32_e32 v179, 0xffff0000, v241
	v_cvt_pk_f32_fp8_e32 v[160:161], v120
	v_cvt_pk_f32_fp8_sdwa v[162:163], v120 src0_sel:WORD_1
	v_pk_fma_f32 v[176:177], v[160:161], s[10:11], v[176:177] op_sel_hi:[1,0,1]
	v_pk_fma_f32 v[178:179], v[162:163], s[10:11], v[178:179] op_sel_hi:[1,0,1]
	v_cvt_pk_f32_fp8_e32 v[164:165], v124
	v_cvt_pk_f32_fp8_sdwa v[166:167], v124 src0_sel:WORD_1
	v_pk_fma_f32 v[176:177], v[164:165], s[10:11], v[176:177] op_sel_hi:[1,0,1]
	v_pk_fma_f32 v[178:179], v[166:167], s[10:11], v[178:179] op_sel_hi:[1,0,1]
	v_cvt_pk_f32_fp8_e32 v[168:169], v128
	v_cvt_pk_f32_fp8_sdwa v[170:171], v128 src0_sel:WORD_1
	v_pk_fma_f32 v[176:177], v[168:169], s[10:11], v[176:177] op_sel_hi:[1,0,1]
	v_pk_fma_f32 v[178:179], v[170:171], s[10:11], v[178:179] op_sel_hi:[1,0,1]
	v_cvt_pk_f32_fp8_e32 v[172:173], v132
	v_cvt_pk_f32_fp8_sdwa v[174:175], v132 src0_sel:WORD_1
	v_pk_fma_f32 v[176:177], v[172:173], s[10:11], v[176:177] op_sel_hi:[1,0,1]
	v_pk_fma_f32 v[178:179], v[174:175], s[10:11], v[178:179] op_sel_hi:[1,0,1]
	global_store_dwordx4 v251, v[176:179], s[4:5]
	v_lshlrev_b32_e32 v180, 16, v242
	v_and_b32_e32 v181, 0xffff0000, v242
	v_lshlrev_b32_e32 v182, 16, v243
	v_and_b32_e32 v183, 0xffff0000, v243
	v_cvt_pk_f32_fp8_e32 v[160:161], v121
	v_cvt_pk_f32_fp8_sdwa v[162:163], v121 src0_sel:WORD_1
	v_pk_fma_f32 v[180:181], v[160:161], s[10:11], v[180:181] op_sel_hi:[1,0,1]
	v_pk_fma_f32 v[182:183], v[162:163], s[10:11], v[182:183] op_sel_hi:[1,0,1]
; __device__ __forceinline__ float bf_lo(unsigned w) { return __uint_as_float(w << 16); }
; __device__ __forceinline__ float bf_hi(unsigned w) { return __uint_as_float(w & 0xffff0000u); }
; __global__ void __launch_bounds__(512, 2) fwd_kernel(Params p) {
;     ...
;             for (int u = 0; u < UN; ++u) { const int it = it0 + u * NGT < NI ? it0 + u * NGT : it0; mm[u] = it >> 7; cc[u] = (it & 127) * 16;
;                 const i32x4 e4 = *(const i32x4*)(tok_e + mm[u] * 4), r4 = *(const i32x4*)(tok_rank + mm[u] * 4);
; #pragma unroll
;                 for (int k = 0; k < 4; ++k) { ee[u][k] = e4[k]; rk[u][k] = r4[k]; }
;                 const bf16_t* xp = X1 + (size_t)mm[u] * DM + cc[u]; xa[u] = *(const u32x4*)xp; xb[u] = *(const u32x4*)(xp + 8); }
; #pragma unroll
;             for (int u = 0; u < UN; ++u)
; #pragma unroll
;                 for (int k = 0; k < 4; ++k) { const int pos = ts[ee[u][k]] * 256 + rk[u][k]; y[u][k] = *(const u32x4*)(Yb + (size_t)pos * DM + cc[u]); }
; #pragma unroll
;             for (int u = 0; u < UN; ++u) {
;                 f32x4 a[4];
;                 a[0] = (f32x4){bf_lo(xa[u].x), bf_hi(xa[u].x), bf_lo(xa[u].y), bf_hi(xa[u].y)}; a[1] = (f32x4){bf_lo(xa[u].z), bf_hi(xa[u].z), bf_lo(xa[u].w), bf_hi(xa[u].w)};
;                 a[2] = (f32x4){bf_lo(xb[u].x), bf_hi(xb[u].x), bf_lo(xb[u].y), bf_hi(xb[u].y)}; a[3] = (f32x4){bf_lo(xb[u].z), bf_hi(xb[u].z), bf_lo(xb[u].w), bf_hi(xb[u].w)};
; #pragma unroll
;                 for (int k = 0; k < 4; ++k)
; #pragma unroll
;                     for (int q = 0; q < 4; ++q) { const f32x2 lo = __builtin_amdgcn_cvt_pk_f32_fp8((int)y[u][k][q], false), hi = __builtin_amdgcn_cvt_pk_f32_fp8((int)y[u][k][q], true);
;                         a[q].x += lo.x * (1.0f / Y8_SCALE); a[q].y += lo.y * (1.0f / Y8_SCALE); a[q].z += hi.x * (1.0f / Y8_SCALE); a[q].w += hi.y * (1.0f / Y8_SCALE); }
;                 if (it0 + u * NGT < NI) { float* op = p.out + (size_t)mm[u] * DM + cc[u];
; #pragma unroll
;                     for (int q = 0; q < 4; ++q) *(f32x4*)(op + 4 * q) = a[q]; }
	v_cvt_pk_f32_fp8_e32 v[164:165], v125
	v_cvt_pk_f32_fp8_sdwa v[166:167], v125 src0_sel:WORD_1
	v_pk_fma_f32 v[180:181], v[164:165], s[10:11], v[180:181] op_sel_hi:[1,0,1]
	v_pk_fma_f32 v[182:183], v[166:167], s[10:11], v[182:183] op_sel_hi:[1,0,1]
	v_cvt_pk_f32_fp8_e32 v[168:169], v129
	v_cvt_pk_f32_fp8_sdwa v[170:171], v129 src0_sel:WORD_1
	v_pk_fma_f32 v[180:181], v[168:169], s[10:11], v[180:181] op_sel_hi:[1,0,1]
	v_pk_fma_f32 v[182:183], v[170:171], s[10:11], v[182:183] op_sel_hi:[1,0,1]
	v_cvt_pk_f32_fp8_e32 v[172:173], v133
	v_cvt_pk_f32_fp8_sdwa v[174:175], v133 src0_sel:WORD_1
	v_pk_fma_f32 v[180:181], v[172:173], s[10:11], v[180:181] op_sel_hi:[1,0,1]
	v_pk_fma_f32 v[182:183], v[174:175], s[10:11], v[182:183] op_sel_hi:[1,0,1]
	global_store_dwordx4 v251, v[180:183], s[4:5] offset:1024
	v_lshlrev_b32_e32 v184, 16, v244
	v_and_b32_e32 v185, 0xffff0000, v244
	v_lshlrev_b32_e32 v186, 16, v245
	v_and_b32_e32 v187, 0xffff0000, v245
	v_cvt_pk_f32_fp8_e32 v[160:161], v122
	v_cvt_pk_f32_fp8_sdwa v[162:163], v122 src0_sel:WORD_1
	v_pk_fma_f32 v[184:185], v[160:161], s[10:11], v[184:185] op_sel_hi:[1,0,1]
	v_pk_fma_f32 v[186:187], v[162:163], s[10:11], v[186:187] op_sel_hi:[1,0,1]
	v_cvt_pk_f32_fp8_e32 v[164:165], v126
	v_cvt_pk_f32_fp8_sdwa v[166:167], v126 src0_sel:WORD_1
	v_pk_fma_f32 v[184:185], v[164:165], s[10:11], v[184:185] op_sel_hi:[1,0,1]
	v_pk_fma_f32 v[186:187], v[166:167], s[10:11], v[186:187] op_sel_hi:[1,0,1]
	v_cvt_pk_f32_fp8_e32 v[168:169], v130
	v_cvt_pk_f32_fp8_sdwa v[170:171], v130 src0_sel:WORD_1
	v_pk_fma_f32 v[184:185], v[168:169], s[10:11], v[184:185] op_sel_hi:[1,0,1]
	v_pk_fma_f32 v[186:187], v[170:171], s[10:11], v[186:187] op_sel_hi:[1,0,1]
	v_cvt_pk_f32_fp8_e32 v[172:173], v134
	v_cvt_pk_f32_fp8_sdwa v[174:175], v134 src0_sel:WORD_1
	v_pk_fma_f32 v[184:185], v[172:173], s[10:11], v[184:185] op_sel_hi:[1,0,1]
	v_pk_fma_f32 v[186:187], v[174:175], s[10:11], v[186:187] op_sel_hi:[1,0,1]
	global_store_dwordx4 v251, v[184:187], s[4:5] offset:2048
	v_lshlrev_b32_e32 v188, 16, v246
	v_and_b32_e32 v189, 0xffff0000, v246
	v_lshlrev_b32_e32 v190, 16, v247
	v_and_b32_e32 v191, 0xffff0000, v247
	v_cvt_pk_f32_fp8_e32 v[160:161], v123
	v_cvt_pk_f32_fp8_sdwa v[162:163], v123 src0_sel:WORD_1
	v_pk_fma_f32 v[188:189], v[160:161], s[10:11], v[188:189] op_sel_hi:[1,0,1]
	v_pk_fma_f32 v[190:191], v[162:163], s[10:11], v[190:191] op_sel_hi:[1,0,1]
	v_cvt_pk_f32_fp8_e32 v[164:165], v127
	v_cvt_pk_f32_fp8_sdwa v[166:167], v127 src0_sel:WORD_1
	v_pk_fma_f32 v[188:189], v[164:165], s[10:11], v[188:189] op_sel_hi:[1,0,1]
	v_pk_fma_f32 v[190:191], v[166:167], s[10:11], v[190:191] op_sel_hi:[1,0,1]
	v_cvt_pk_f32_fp8_e32 v[168:169], v131
	v_cvt_pk_f32_fp8_sdwa v[170:171], v131 src0_sel:WORD_1
	v_pk_fma_f32 v[188:189], v[168:169], s[10:11], v[188:189] op_sel_hi:[1,0,1]
	v_pk_fma_f32 v[190:191], v[170:171], s[10:11], v[190:191] op_sel_hi:[1,0,1]
	v_cvt_pk_f32_fp8_e32 v[172:173], v135
	v_cvt_pk_f32_fp8_sdwa v[174:175], v135 src0_sel:WORD_1
	v_pk_fma_f32 v[188:189], v[172:173], s[10:11], v[188:189] op_sel_hi:[1,0,1]
	v_pk_fma_f32 v[190:191], v[174:175], s[10:11], v[190:191] op_sel_hi:[1,0,1]
	global_store_dwordx4 v251, v[188:191], s[4:5] offset:3072
	v_lshl_add_u32 v200, v20, 2, s23
	v_lshl_add_u32 v201, v21, 2, s23
	v_lshl_add_u32 v202, v22, 2, s23
	v_lshl_add_u32 v203, v23, 2, s23
	ds_read_b32 v148, v200
	ds_read_b32 v149, v201
	ds_read_b32 v150, v202
	ds_read_b32 v151, v203
	s_waitcnt lgkmcnt(0)
	v_lshl_add_u32 v148, v148, 8, v36
	v_lshl_add_u32 v149, v149, 8, v37
	v_lshl_add_u32 v150, v150, 8, v38
	v_lshl_add_u32 v151, v151, 8, v39
	v_lshl_add_u32 v148, v148, 11, v4
	v_lshl_add_u32 v149, v149, 11, v4
	v_lshl_add_u32 v150, v150, 11, v4
	v_lshl_add_u32 v151, v151, 11, v4
	global_load_dword v120, v148, s[6:7]
	global_load_dword v121, v148, s[6:7] offset:256
	global_load_dword v122, v148, s[6:7] offset:512
	global_load_dword v123, v148, s[6:7] offset:768
	global_load_dword v124, v149, s[6:7]
	global_load_dword v125, v149, s[6:7] offset:256
	global_load_dword v126, v149, s[6:7] offset:512
	global_load_dword v127, v149, s[6:7] offset:768
	global_load_dword v128, v150, s[6:7]
	global_load_dword v129, v150, s[6:7] offset:256
	global_load_dword v130, v150, s[6:7] offset:512
	global_load_dword v131, v150, s[6:7] offset:768
	global_load_dword v132, v151, s[6:7]
	global_load_dword v133, v151, s[6:7] offset:256
	global_load_dword v134, v151, s[6:7] offset:512
	global_load_dword v135, v151, s[6:7] offset:768
	v_add_u32_e32 v192, 0x3000, v3
	v_lshlrev_b32_e32 v196, 4, v192
	v_lshl_add_u32 v248, v192, 13, v6
	v_add_u32_e32 v193, 0x3400, v3
	v_lshlrev_b32_e32 v197, 4, v193
	v_lshl_add_u32 v249, v193, 13, v6
	v_add_u32_e32 v194, 0x3800, v3
	v_lshlrev_b32_e32 v198, 4, v194
	v_lshl_add_u32 v250, v194, 13, v6
	v_add_u32_e32 v195, 0x3c00, v3
	v_lshlrev_b32_e32 v199, 4, v195
	v_lshl_add_u32 v251, v195, 13, v6
	global_load_dwordx4 v[8:11], v196, s[16:17]
	global_load_dwordx4 v[12:15], v197, s[16:17]
	global_load_dwordx4 v[16:19], v198, s[16:17]
	global_load_dwordx4 v[20:23], v199, s[16:17]
	global_load_dwordx4 v[24:27], v196, s[18:19]
	global_load_dwordx4 v[28:31], v197, s[18:19]
	global_load_dwordx4 v[32:35], v198, s[18:19]
	global_load_dwordx4 v[36:39], v199, s[18:19]
	v_lshl_add_u32 v196, v192, 12, v5
	global_load_dwordx2 v[216:217], v196, s[14:15]
	global_load_dwordx2 v[218:219], v196, s[14:15] offset:512
	global_load_dwordx2 v[220:221], v196, s[14:15] offset:1024
	global_load_dwordx2 v[222:223], v196, s[14:15] offset:1536
	v_lshl_add_u32 v197, v193, 12, v5
	global_load_dwordx2 v[224:225], v197, s[14:15]
	global_load_dwordx2 v[226:227], v197, s[14:15] offset:512
	global_load_dwordx2 v[228:229], v197, s[14:15] offset:1024
	global_load_dwordx2 v[230:231], v197, s[14:15] offset:1536
	v_lshl_add_u32 v198, v194, 12, v5
	global_load_dwordx2 v[232:233], v198, s[14:15]
	global_load_dwordx2 v[234:235], v198, s[14:15] offset:512
	global_load_dwordx2 v[236:237], v198, s[14:15] offset:1024
	global_load_dwordx2 v[238:239], v198, s[14:15] offset:1536
	v_lshl_add_u32 v199, v195, 12, v5
	global_load_dwordx2 v[240:241], v199, s[14:15]
	global_load_dwordx2 v[242:243], v199, s[14:15] offset:512
	global_load_dwordx2 v[244:245], v199, s[14:15] offset:1024
	global_load_dwordx2 v[246:247], v199, s[14:15] offset:1536
	s_waitcnt vmcnt(63)
; __device__ __forceinline__ float bf_lo(unsigned w) { return __uint_as_float(w << 16); }
; __device__ __forceinline__ float bf_hi(unsigned w) { return __uint_as_float(w & 0xffff0000u); }
; __global__ void __launch_bounds__(512, 2) fwd_kernel(Params p) {
;     ...
;             for (int u = 0; u < UN; ++u) { const int it = it0 + u * NGT < NI ? it0 + u * NGT : it0; mm[u] = it >> 7; cc[u] = (it & 127) * 16;
;                 const i32x4 e4 = *(const i32x4*)(tok_e + mm[u] * 4), r4 = *(const i32x4*)(tok_rank + mm[u] * 4);
; #pragma unroll
;                 for (int k = 0; k < 4; ++k) { ee[u][k] = e4[k]; rk[u][k] = r4[k]; }
;                 const bf16_t* xp = X1 + (size_t)mm[u] * DM + cc[u]; xa[u] = *(const u32x4*)xp; xb[u] = *(const u32x4*)(xp + 8); }
; #pragma unroll
;             for (int u = 0; u < UN; ++u)
; #pragma unroll
;                 for (int k = 0; k < 4; ++k) { const int pos = ts[ee[u][k]] * 256 + rk[u][k]; y[u][k] = *(const u32x4*)(Yb + (size_t)pos * DM + cc[u]); }
; #pragma unroll
;             for (int u = 0; u < UN; ++u) {
;                 f32x4 a[4];
;                 a[0] = (f32x4){bf_lo(xa[u].x), bf_hi(xa[u].x), bf_lo(xa[u].y), bf_hi(xa[u].y)}; a[1] = (f32x4){bf_lo(xa[u].z), bf_hi(xa[u].z), bf_lo(xa[u].w), bf_hi(xa[u].w)};
;                 a[2] = (f32x4){bf_lo(xb[u].x), bf_hi(xb[u].x), bf_lo(xb[u].y), bf_hi(xb[u].y)}; a[3] = (f32x4){bf_lo(xb[u].z), bf_hi(xb[u].z), bf_lo(xb[u].w), bf_hi(xb[u].w)};
; #pragma unroll
;                 for (int k = 0; k < 4; ++k)
; #pragma unroll
;                     for (int q = 0; q < 4; ++q) { const f32x2 lo = __builtin_amdgcn_cvt_pk_f32_fp8((int)y[u][k][q], false), hi = __builtin_amdgcn_cvt_pk_f32_fp8((int)y[u][k][q], true);
;                         a[q].x += lo.x * (1.0f / Y8_SCALE); a[q].y += lo.y * (1.0f / Y8_SCALE); a[q].z += hi.x * (1.0f / Y8_SCALE); a[q].w += hi.y * (1.0f / Y8_SCALE); }
;                 if (it0 + u * NGT < NI) { float* op = p.out + (size_t)mm[u] * DM + cc[u];
; #pragma unroll
;                     for (int q = 0; q < 4; ++q) *(f32x4*)(op + 4 * q) = a[q]; }
	v_lshlrev_b32_e32 v176, 16, v40
	v_and_b32_e32 v177, 0xffff0000, v40
	v_lshlrev_b32_e32 v178, 16, v41
	v_and_b32_e32 v179, 0xffff0000, v41
	v_cvt_pk_f32_fp8_e32 v[160:161], v72
	v_cvt_pk_f32_fp8_sdwa v[162:163], v72 src0_sel:WORD_1
	v_pk_fma_f32 v[176:177], v[160:161], s[10:11], v[176:177] op_sel_hi:[1,0,1]
	v_pk_fma_f32 v[178:179], v[162:163], s[10:11], v[178:179] op_sel_hi:[1,0,1]
	v_cvt_pk_f32_fp8_e32 v[164:165], v76
	v_cvt_pk_f32_fp8_sdwa v[166:167], v76 src0_sel:WORD_1
	v_pk_fma_f32 v[176:177], v[164:165], s[10:11], v[176:177] op_sel_hi:[1,0,1]
	v_pk_fma_f32 v[178:179], v[166:167], s[10:11], v[178:179] op_sel_hi:[1,0,1]
	v_cvt_pk_f32_fp8_e32 v[168:169], v80
	v_cvt_pk_f32_fp8_sdwa v[170:171], v80 src0_sel:WORD_1
	v_pk_fma_f32 v[176:177], v[168:169], s[10:11], v[176:177] op_sel_hi:[1,0,1]
	v_pk_fma_f32 v[178:179], v[170:171], s[10:11], v[178:179] op_sel_hi:[1,0,1]
	v_cvt_pk_f32_fp8_e32 v[172:173], v84
	v_cvt_pk_f32_fp8_sdwa v[174:175], v84 src0_sel:WORD_1
	v_pk_fma_f32 v[176:177], v[172:173], s[10:11], v[176:177] op_sel_hi:[1,0,1]
	v_pk_fma_f32 v[178:179], v[174:175], s[10:11], v[178:179] op_sel_hi:[1,0,1]
	global_store_dwordx4 v156, v[176:179], s[4:5]
	v_lshlrev_b32_e32 v180, 16, v42
	v_and_b32_e32 v181, 0xffff0000, v42
	v_lshlrev_b32_e32 v182, 16, v43
	v_and_b32_e32 v183, 0xffff0000, v43
	v_cvt_pk_f32_fp8_e32 v[160:161], v73
	v_cvt_pk_f32_fp8_sdwa v[162:163], v73 src0_sel:WORD_1
	v_pk_fma_f32 v[180:181], v[160:161], s[10:11], v[180:181] op_sel_hi:[1,0,1]
	v_pk_fma_f32 v[182:183], v[162:163], s[10:11], v[182:183] op_sel_hi:[1,0,1]
	v_cvt_pk_f32_fp8_e32 v[164:165], v77
	v_cvt_pk_f32_fp8_sdwa v[166:167], v77 src0_sel:WORD_1
	v_pk_fma_f32 v[180:181], v[164:165], s[10:11], v[180:181] op_sel_hi:[1,0,1]
	v_pk_fma_f32 v[182:183], v[166:167], s[10:11], v[182:183] op_sel_hi:[1,0,1]
	v_cvt_pk_f32_fp8_e32 v[168:169], v81
	v_cvt_pk_f32_fp8_sdwa v[170:171], v81 src0_sel:WORD_1
	v_pk_fma_f32 v[180:181], v[168:169], s[10:11], v[180:181] op_sel_hi:[1,0,1]
	v_pk_fma_f32 v[182:183], v[170:171], s[10:11], v[182:183] op_sel_hi:[1,0,1]
	v_cvt_pk_f32_fp8_e32 v[172:173], v85
	v_cvt_pk_f32_fp8_sdwa v[174:175], v85 src0_sel:WORD_1
	v_pk_fma_f32 v[180:181], v[172:173], s[10:11], v[180:181] op_sel_hi:[1,0,1]
	v_pk_fma_f32 v[182:183], v[174:175], s[10:11], v[182:183] op_sel_hi:[1,0,1]
	global_store_dwordx4 v156, v[180:183], s[4:5] offset:1024
	v_lshlrev_b32_e32 v184, 16, v44
	v_and_b32_e32 v185, 0xffff0000, v44
	v_lshlrev_b32_e32 v186, 16, v45
	v_and_b32_e32 v187, 0xffff0000, v45
	v_cvt_pk_f32_fp8_e32 v[160:161], v74
	v_cvt_pk_f32_fp8_sdwa v[162:163], v74 src0_sel:WORD_1
	v_pk_fma_f32 v[184:185], v[160:161], s[10:11], v[184:185] op_sel_hi:[1,0,1]
	v_pk_fma_f32 v[186:187], v[162:163], s[10:11], v[186:187] op_sel_hi:[1,0,1]
	v_cvt_pk_f32_fp8_e32 v[164:165], v78
	v_cvt_pk_f32_fp8_sdwa v[166:167], v78 src0_sel:WORD_1
	v_pk_fma_f32 v[184:185], v[164:165], s[10:11], v[184:185] op_sel_hi:[1,0,1]
	v_pk_fma_f32 v[186:187], v[166:167], s[10:11], v[186:187] op_sel_hi:[1,0,1]
	v_cvt_pk_f32_fp8_e32 v[168:169], v82
	v_cvt_pk_f32_fp8_sdwa v[170:171], v82 src0_sel:WORD_1
	v_pk_fma_f32 v[184:185], v[168:169], s[10:11], v[184:185] op_sel_hi:[1,0,1]
	v_pk_fma_f32 v[186:187], v[170:171], s[10:11], v[186:187] op_sel_hi:[1,0,1]
	v_cvt_pk_f32_fp8_e32 v[172:173], v86
	v_cvt_pk_f32_fp8_sdwa v[174:175], v86 src0_sel:WORD_1
	v_pk_fma_f32 v[184:185], v[172:173], s[10:11], v[184:185] op_sel_hi:[1,0,1]
	v_pk_fma_f32 v[186:187], v[174:175], s[10:11], v[186:187] op_sel_hi:[1,0,1]
	global_store_dwordx4 v156, v[184:187], s[4:5] offset:2048
	v_lshlrev_b32_e32 v188, 16, v46
	v_and_b32_e32 v189, 0xffff0000, v46
	v_lshlrev_b32_e32 v190, 16, v47
	v_and_b32_e32 v191, 0xffff0000, v47
	v_cvt_pk_f32_fp8_e32 v[160:161], v75
	v_cvt_pk_f32_fp8_sdwa v[162:163], v75 src0_sel:WORD_1
	v_pk_fma_f32 v[188:189], v[160:161], s[10:11], v[188:189] op_sel_hi:[1,0,1]
	v_pk_fma_f32 v[190:191], v[162:163], s[10:11], v[190:191] op_sel_hi:[1,0,1]
	v_cvt_pk_f32_fp8_e32 v[164:165], v79
	v_cvt_pk_f32_fp8_sdwa v[166:167], v79 src0_sel:WORD_1
	v_pk_fma_f32 v[188:189], v[164:165], s[10:11], v[188:189] op_sel_hi:[1,0,1]
	v_pk_fma_f32 v[190:191], v[166:167], s[10:11], v[190:191] op_sel_hi:[1,0,1]
	v_cvt_pk_f32_fp8_e32 v[168:169], v83
	v_cvt_pk_f32_fp8_sdwa v[170:171], v83 src0_sel:WORD_1
	v_pk_fma_f32 v[188:189], v[168:169], s[10:11], v[188:189] op_sel_hi:[1,0,1]
	v_pk_fma_f32 v[190:191], v[170:171], s[10:11], v[190:191] op_sel_hi:[1,0,1]
	v_cvt_pk_f32_fp8_e32 v[172:173], v87
	v_cvt_pk_f32_fp8_sdwa v[174:175], v87 src0_sel:WORD_1
	v_pk_fma_f32 v[188:189], v[172:173], s[10:11], v[188:189] op_sel_hi:[1,0,1]
	v_pk_fma_f32 v[190:191], v[174:175], s[10:11], v[190:191] op_sel_hi:[1,0,1]
	global_store_dwordx4 v156, v[188:191], s[4:5] offset:3072
	s_waitcnt vmcnt(20)
	v_lshl_add_u32 v200, v8, 2, s23
	v_lshl_add_u32 v201, v9, 2, s23
	v_lshl_add_u32 v202, v10, 2, s23
	v_lshl_add_u32 v203, v11, 2, s23
	ds_read_b32 v136, v200
	ds_read_b32 v137, v201
	ds_read_b32 v138, v202
	ds_read_b32 v139, v203
	s_waitcnt lgkmcnt(0)
	v_lshl_add_u32 v136, v136, 8, v24
	v_lshl_add_u32 v137, v137, 8, v25
	v_lshl_add_u32 v138, v138, 8, v26
	v_lshl_add_u32 v139, v139, 8, v27
	v_lshl_add_u32 v136, v136, 11, v4
	v_lshl_add_u32 v137, v137, 11, v4
	v_lshl_add_u32 v138, v138, 11, v4
	v_lshl_add_u32 v139, v139, 11, v4
	global_load_dword v72, v136, s[6:7]
	global_load_dword v73, v136, s[6:7] offset:256
	global_load_dword v74, v136, s[6:7] offset:512
	global_load_dword v75, v136, s[6:7] offset:768
	global_load_dword v76, v137, s[6:7]
	global_load_dword v77, v137, s[6:7] offset:256
	global_load_dword v78, v137, s[6:7] offset:512
	global_load_dword v79, v137, s[6:7] offset:768
	global_load_dword v80, v138, s[6:7]
	global_load_dword v81, v138, s[6:7] offset:256
	global_load_dword v82, v138, s[6:7] offset:512
	global_load_dword v83, v138, s[6:7] offset:768
	global_load_dword v84, v139, s[6:7]
	global_load_dword v85, v139, s[6:7] offset:256
	global_load_dword v86, v139, s[6:7] offset:512
	global_load_dword v87, v139, s[6:7] offset:768
	s_waitcnt vmcnt(63)
; __device__ __forceinline__ float bf_lo(unsigned w) { return __uint_as_float(w << 16); }
; __device__ __forceinline__ float bf_hi(unsigned w) { return __uint_as_float(w & 0xffff0000u); }
; __global__ void __launch_bounds__(512, 2) fwd_kernel(Params p) {
;     ...
;             for (int u = 0; u < UN; ++u) { const int it = it0 + u * NGT < NI ? it0 + u * NGT : it0; mm[u] = it >> 7; cc[u] = (it & 127) * 16;
;                 const i32x4 e4 = *(const i32x4*)(tok_e + mm[u] * 4), r4 = *(const i32x4*)(tok_rank + mm[u] * 4);
; #pragma unroll
;                 for (int k = 0; k < 4; ++k) { ee[u][k] = e4[k]; rk[u][k] = r4[k]; }
;                 const bf16_t* xp = X1 + (size_t)mm[u] * DM + cc[u]; xa[u] = *(const u32x4*)xp; xb[u] = *(const u32x4*)(xp + 8); }
; #pragma unroll
;             for (int u = 0; u < UN; ++u)
; #pragma unroll
;                 for (int k = 0; k < 4; ++k) { const int pos = ts[ee[u][k]] * 256 + rk[u][k]; y[u][k] = *(const u32x4*)(Yb + (size_t)pos * DM + cc[u]); }
;     ...
;             for (int u = 0; u < UN; ++u) {
;                 f32x4 a[4];
;                 a[0] = (f32x4){bf_lo(xa[u].x), bf_hi(xa[u].x), bf_lo(xa[u].y), bf_hi(xa[u].y)}; a[1] = (f32x4){bf_lo(xa[u].z), bf_hi(xa[u].z), bf_lo(xa[u].w), bf_hi(xa[u].w)};
;                 a[2] = (f32x4){bf_lo(xb[u].x), bf_hi(xb[u].x), bf_lo(xb[u].y), bf_hi(xb[u].y)}; a[3] = (f32x4){bf_lo(xb[u].z), bf_hi(xb[u].z), bf_lo(xb[u].w), bf_hi(xb[u].w)};
; #pragma unroll
;                 for (int k = 0; k < 4; ++k)
; #pragma unroll
;                     for (int q = 0; q < 4; ++q) { const f32x2 lo = __builtin_amdgcn_cvt_pk_f32_fp8((int)y[u][k][q], false), hi = __builtin_amdgcn_cvt_pk_f32_fp8((int)y[u][k][q], true);
;                         a[q].x += lo.x * (1.0f / Y8_SCALE); a[q].y += lo.y * (1.0f / Y8_SCALE); a[q].z += hi.x * (1.0f / Y8_SCALE); a[q].w += hi.y * (1.0f / Y8_SCALE); }
;                 if (it0 + u * NGT < NI) { float* op = p.out + (size_t)mm[u] * DM + cc[u];
; #pragma unroll
;                     for (int q = 0; q < 4; ++q) *(f32x4*)(op + 4 * q) = a[q]; }
	v_lshlrev_b32_e32 v176, 16, v48
	v_and_b32_e32 v177, 0xffff0000, v48
	v_lshlrev_b32_e32 v178, 16, v49
	v_and_b32_e32 v179, 0xffff0000, v49
	v_cvt_pk_f32_fp8_e32 v[160:161], v88
	v_cvt_pk_f32_fp8_sdwa v[162:163], v88 src0_sel:WORD_1
	v_pk_fma_f32 v[176:177], v[160:161], s[10:11], v[176:177] op_sel_hi:[1,0,1]
	v_pk_fma_f32 v[178:179], v[162:163], s[10:11], v[178:179] op_sel_hi:[1,0,1]
	v_cvt_pk_f32_fp8_e32 v[164:165], v92
	v_cvt_pk_f32_fp8_sdwa v[166:167], v92 src0_sel:WORD_1
	v_pk_fma_f32 v[176:177], v[164:165], s[10:11], v[176:177] op_sel_hi:[1,0,1]
	v_pk_fma_f32 v[178:179], v[166:167], s[10:11], v[178:179] op_sel_hi:[1,0,1]
	v_cvt_pk_f32_fp8_e32 v[168:169], v96
	v_cvt_pk_f32_fp8_sdwa v[170:171], v96 src0_sel:WORD_1
	v_pk_fma_f32 v[176:177], v[168:169], s[10:11], v[176:177] op_sel_hi:[1,0,1]
	v_pk_fma_f32 v[178:179], v[170:171], s[10:11], v[178:179] op_sel_hi:[1,0,1]
	v_cvt_pk_f32_fp8_e32 v[172:173], v100
	v_cvt_pk_f32_fp8_sdwa v[174:175], v100 src0_sel:WORD_1
	v_pk_fma_f32 v[176:177], v[172:173], s[10:11], v[176:177] op_sel_hi:[1,0,1]
	v_pk_fma_f32 v[178:179], v[174:175], s[10:11], v[178:179] op_sel_hi:[1,0,1]
	global_store_dwordx4 v157, v[176:179], s[4:5]
	v_lshlrev_b32_e32 v180, 16, v50
	v_and_b32_e32 v181, 0xffff0000, v50
	v_lshlrev_b32_e32 v182, 16, v51
	v_and_b32_e32 v183, 0xffff0000, v51
	v_cvt_pk_f32_fp8_e32 v[160:161], v89
	v_cvt_pk_f32_fp8_sdwa v[162:163], v89 src0_sel:WORD_1
	v_pk_fma_f32 v[180:181], v[160:161], s[10:11], v[180:181] op_sel_hi:[1,0,1]
	v_pk_fma_f32 v[182:183], v[162:163], s[10:11], v[182:183] op_sel_hi:[1,0,1]
	v_cvt_pk_f32_fp8_e32 v[164:165], v93
	v_cvt_pk_f32_fp8_sdwa v[166:167], v93 src0_sel:WORD_1
	v_pk_fma_f32 v[180:181], v[164:165], s[10:11], v[180:181] op_sel_hi:[1,0,1]
	v_pk_fma_f32 v[182:183], v[166:167], s[10:11], v[182:183] op_sel_hi:[1,0,1]
	v_cvt_pk_f32_fp8_e32 v[168:169], v97
	v_cvt_pk_f32_fp8_sdwa v[170:171], v97 src0_sel:WORD_1
	v_pk_fma_f32 v[180:181], v[168:169], s[10:11], v[180:181] op_sel_hi:[1,0,1]
	v_pk_fma_f32 v[182:183], v[170:171], s[10:11], v[182:183] op_sel_hi:[1,0,1]
	v_cvt_pk_f32_fp8_e32 v[172:173], v101
	v_cvt_pk_f32_fp8_sdwa v[174:175], v101 src0_sel:WORD_1
	v_pk_fma_f32 v[180:181], v[172:173], s[10:11], v[180:181] op_sel_hi:[1,0,1]
	v_pk_fma_f32 v[182:183], v[174:175], s[10:11], v[182:183] op_sel_hi:[1,0,1]
	global_store_dwordx4 v157, v[180:183], s[4:5] offset:1024
	v_lshlrev_b32_e32 v184, 16, v52
	v_and_b32_e32 v185, 0xffff0000, v52
	v_lshlrev_b32_e32 v186, 16, v53
	v_and_b32_e32 v187, 0xffff0000, v53
	v_cvt_pk_f32_fp8_e32 v[160:161], v90
	v_cvt_pk_f32_fp8_sdwa v[162:163], v90 src0_sel:WORD_1
	v_pk_fma_f32 v[184:185], v[160:161], s[10:11], v[184:185] op_sel_hi:[1,0,1]
	v_pk_fma_f32 v[186:187], v[162:163], s[10:11], v[186:187] op_sel_hi:[1,0,1]
	v_cvt_pk_f32_fp8_e32 v[164:165], v94
	v_cvt_pk_f32_fp8_sdwa v[166:167], v94 src0_sel:WORD_1
	v_pk_fma_f32 v[184:185], v[164:165], s[10:11], v[184:185] op_sel_hi:[1,0,1]
	v_pk_fma_f32 v[186:187], v[166:167], s[10:11], v[186:187] op_sel_hi:[1,0,1]
	v_cvt_pk_f32_fp8_e32 v[168:169], v98
	v_cvt_pk_f32_fp8_sdwa v[170:171], v98 src0_sel:WORD_1
	v_pk_fma_f32 v[184:185], v[168:169], s[10:11], v[184:185] op_sel_hi:[1,0,1]
	v_pk_fma_f32 v[186:187], v[170:171], s[10:11], v[186:187] op_sel_hi:[1,0,1]
	v_cvt_pk_f32_fp8_e32 v[172:173], v102
	v_cvt_pk_f32_fp8_sdwa v[174:175], v102 src0_sel:WORD_1
	v_pk_fma_f32 v[184:185], v[172:173], s[10:11], v[184:185] op_sel_hi:[1,0,1]
	v_pk_fma_f32 v[186:187], v[174:175], s[10:11], v[186:187] op_sel_hi:[1,0,1]
	global_store_dwordx4 v157, v[184:187], s[4:5] offset:2048
	v_lshlrev_b32_e32 v188, 16, v54
	v_and_b32_e32 v189, 0xffff0000, v54
	v_lshlrev_b32_e32 v190, 16, v55
	v_and_b32_e32 v191, 0xffff0000, v55
	v_cvt_pk_f32_fp8_e32 v[160:161], v91
	v_cvt_pk_f32_fp8_sdwa v[162:163], v91 src0_sel:WORD_1
	v_pk_fma_f32 v[188:189], v[160:161], s[10:11], v[188:189] op_sel_hi:[1,0,1]
	v_pk_fma_f32 v[190:191], v[162:163], s[10:11], v[190:191] op_sel_hi:[1,0,1]
	v_cvt_pk_f32_fp8_e32 v[164:165], v95
	v_cvt_pk_f32_fp8_sdwa v[166:167], v95 src0_sel:WORD_1
	v_pk_fma_f32 v[188:189], v[164:165], s[10:11], v[188:189] op_sel_hi:[1,0,1]
	v_pk_fma_f32 v[190:191], v[166:167], s[10:11], v[190:191] op_sel_hi:[1,0,1]
	v_cvt_pk_f32_fp8_e32 v[168:169], v99
	v_cvt_pk_f32_fp8_sdwa v[170:171], v99 src0_sel:WORD_1
	v_pk_fma_f32 v[188:189], v[168:169], s[10:11], v[188:189] op_sel_hi:[1,0,1]
	v_pk_fma_f32 v[190:191], v[170:171], s[10:11], v[190:191] op_sel_hi:[1,0,1]
	v_cvt_pk_f32_fp8_e32 v[172:173], v103
	v_cvt_pk_f32_fp8_sdwa v[174:175], v103 src0_sel:WORD_1
	v_pk_fma_f32 v[188:189], v[172:173], s[10:11], v[188:189] op_sel_hi:[1,0,1]
	v_pk_fma_f32 v[190:191], v[174:175], s[10:11], v[190:191] op_sel_hi:[1,0,1]
	global_store_dwordx4 v157, v[188:191], s[4:5] offset:3072
	v_lshl_add_u32 v200, v12, 2, s23
	v_lshl_add_u32 v201, v13, 2, s23
	v_lshl_add_u32 v202, v14, 2, s23
	v_lshl_add_u32 v203, v15, 2, s23
	ds_read_b32 v140, v200
	ds_read_b32 v141, v201
	ds_read_b32 v142, v202
	ds_read_b32 v143, v203
	s_waitcnt lgkmcnt(0)
	v_lshl_add_u32 v140, v140, 8, v28
	v_lshl_add_u32 v141, v141, 8, v29
	v_lshl_add_u32 v142, v142, 8, v30
	v_lshl_add_u32 v143, v143, 8, v31
	v_lshl_add_u32 v140, v140, 11, v4
	v_lshl_add_u32 v141, v141, 11, v4
	v_lshl_add_u32 v142, v142, 11, v4
	v_lshl_add_u32 v143, v143, 11, v4
	global_load_dword v88, v140, s[6:7]
	global_load_dword v89, v140, s[6:7] offset:256
	global_load_dword v90, v140, s[6:7] offset:512
	global_load_dword v91, v140, s[6:7] offset:768
	global_load_dword v92, v141, s[6:7]
	global_load_dword v93, v141, s[6:7] offset:256
	global_load_dword v94, v141, s[6:7] offset:512
	global_load_dword v95, v141, s[6:7] offset:768
	global_load_dword v96, v142, s[6:7]
	global_load_dword v97, v142, s[6:7] offset:256
	global_load_dword v98, v142, s[6:7] offset:512
	global_load_dword v99, v142, s[6:7] offset:768
	global_load_dword v100, v143, s[6:7]
	global_load_dword v101, v143, s[6:7] offset:256
	global_load_dword v102, v143, s[6:7] offset:512
	global_load_dword v103, v143, s[6:7] offset:768
	s_waitcnt vmcnt(63)
; __device__ __forceinline__ float bf_lo(unsigned w) { return __uint_as_float(w << 16); }
; __device__ __forceinline__ float bf_hi(unsigned w) { return __uint_as_float(w & 0xffff0000u); }
; __global__ void __launch_bounds__(512, 2) fwd_kernel(Params p) {
;     ...
;             for (int u = 0; u < UN; ++u) { const int it = it0 + u * NGT < NI ? it0 + u * NGT : it0; mm[u] = it >> 7; cc[u] = (it & 127) * 16;
;                 const i32x4 e4 = *(const i32x4*)(tok_e + mm[u] * 4), r4 = *(const i32x4*)(tok_rank + mm[u] * 4);
; #pragma unroll
;                 for (int k = 0; k < 4; ++k) { ee[u][k] = e4[k]; rk[u][k] = r4[k]; }
;                 const bf16_t* xp = X1 + (size_t)mm[u] * DM + cc[u]; xa[u] = *(const u32x4*)xp; xb[u] = *(const u32x4*)(xp + 8); }
; #pragma unroll
;             for (int u = 0; u < UN; ++u)
; #pragma unroll
;                 for (int k = 0; k < 4; ++k) { const int pos = ts[ee[u][k]] * 256 + rk[u][k]; y[u][k] = *(const u32x4*)(Yb + (size_t)pos * DM + cc[u]); }
;     ...
;             for (int u = 0; u < UN; ++u) {
;                 f32x4 a[4];
;                 a[0] = (f32x4){bf_lo(xa[u].x), bf_hi(xa[u].x), bf_lo(xa[u].y), bf_hi(xa[u].y)}; a[1] = (f32x4){bf_lo(xa[u].z), bf_hi(xa[u].z), bf_lo(xa[u].w), bf_hi(xa[u].w)};
;                 a[2] = (f32x4){bf_lo(xb[u].x), bf_hi(xb[u].x), bf_lo(xb[u].y), bf_hi(xb[u].y)}; a[3] = (f32x4){bf_lo(xb[u].z), bf_hi(xb[u].z), bf_lo(xb[u].w), bf_hi(xb[u].w)};
; #pragma unroll
;                 for (int k = 0; k < 4; ++k)
; #pragma unroll
;                     for (int q = 0; q < 4; ++q) { const f32x2 lo = __builtin_amdgcn_cvt_pk_f32_fp8((int)y[u][k][q], false), hi = __builtin_amdgcn_cvt_pk_f32_fp8((int)y[u][k][q], true);
;                         a[q].x += lo.x * (1.0f / Y8_SCALE); a[q].y += lo.y * (1.0f / Y8_SCALE); a[q].z += hi.x * (1.0f / Y8_SCALE); a[q].w += hi.y * (1.0f / Y8_SCALE); }
;                 if (it0 + u * NGT < NI) { float* op = p.out + (size_t)mm[u] * DM + cc[u];
; #pragma unroll
;                     for (int q = 0; q < 4; ++q) *(f32x4*)(op + 4 * q) = a[q]; }
	v_lshlrev_b32_e32 v176, 16, v56
	v_and_b32_e32 v177, 0xffff0000, v56
	v_lshlrev_b32_e32 v178, 16, v57
	v_and_b32_e32 v179, 0xffff0000, v57
	v_cvt_pk_f32_fp8_e32 v[160:161], v104
	v_cvt_pk_f32_fp8_sdwa v[162:163], v104 src0_sel:WORD_1
	v_pk_fma_f32 v[176:177], v[160:161], s[10:11], v[176:177] op_sel_hi:[1,0,1]
	v_pk_fma_f32 v[178:179], v[162:163], s[10:11], v[178:179] op_sel_hi:[1,0,1]
	v_cvt_pk_f32_fp8_e32 v[164:165], v108
	v_cvt_pk_f32_fp8_sdwa v[166:167], v108 src0_sel:WORD_1
	v_pk_fma_f32 v[176:177], v[164:165], s[10:11], v[176:177] op_sel_hi:[1,0,1]
	v_pk_fma_f32 v[178:179], v[166:167], s[10:11], v[178:179] op_sel_hi:[1,0,1]
	v_cvt_pk_f32_fp8_e32 v[168:169], v112
	v_cvt_pk_f32_fp8_sdwa v[170:171], v112 src0_sel:WORD_1
	v_pk_fma_f32 v[176:177], v[168:169], s[10:11], v[176:177] op_sel_hi:[1,0,1]
	v_pk_fma_f32 v[178:179], v[170:171], s[10:11], v[178:179] op_sel_hi:[1,0,1]
	v_cvt_pk_f32_fp8_e32 v[172:173], v116
	v_cvt_pk_f32_fp8_sdwa v[174:175], v116 src0_sel:WORD_1
	v_pk_fma_f32 v[176:177], v[172:173], s[10:11], v[176:177] op_sel_hi:[1,0,1]
	v_pk_fma_f32 v[178:179], v[174:175], s[10:11], v[178:179] op_sel_hi:[1,0,1]
	global_store_dwordx4 v158, v[176:179], s[4:5]
	v_lshlrev_b32_e32 v180, 16, v58
	v_and_b32_e32 v181, 0xffff0000, v58
	v_lshlrev_b32_e32 v182, 16, v59
	v_and_b32_e32 v183, 0xffff0000, v59
	v_cvt_pk_f32_fp8_e32 v[160:161], v105
	v_cvt_pk_f32_fp8_sdwa v[162:163], v105 src0_sel:WORD_1
	v_pk_fma_f32 v[180:181], v[160:161], s[10:11], v[180:181] op_sel_hi:[1,0,1]
	v_pk_fma_f32 v[182:183], v[162:163], s[10:11], v[182:183] op_sel_hi:[1,0,1]
	v_cvt_pk_f32_fp8_e32 v[164:165], v109
	v_cvt_pk_f32_fp8_sdwa v[166:167], v109 src0_sel:WORD_1
	v_pk_fma_f32 v[180:181], v[164:165], s[10:11], v[180:181] op_sel_hi:[1,0,1]
	v_pk_fma_f32 v[182:183], v[166:167], s[10:11], v[182:183] op_sel_hi:[1,0,1]
	v_cvt_pk_f32_fp8_e32 v[168:169], v113
	v_cvt_pk_f32_fp8_sdwa v[170:171], v113 src0_sel:WORD_1
	v_pk_fma_f32 v[180:181], v[168:169], s[10:11], v[180:181] op_sel_hi:[1,0,1]
	v_pk_fma_f32 v[182:183], v[170:171], s[10:11], v[182:183] op_sel_hi:[1,0,1]
	v_cvt_pk_f32_fp8_e32 v[172:173], v117
	v_cvt_pk_f32_fp8_sdwa v[174:175], v117 src0_sel:WORD_1
	v_pk_fma_f32 v[180:181], v[172:173], s[10:11], v[180:181] op_sel_hi:[1,0,1]
	v_pk_fma_f32 v[182:183], v[174:175], s[10:11], v[182:183] op_sel_hi:[1,0,1]
	global_store_dwordx4 v158, v[180:183], s[4:5] offset:1024
	v_lshlrev_b32_e32 v184, 16, v60
	v_and_b32_e32 v185, 0xffff0000, v60
	v_lshlrev_b32_e32 v186, 16, v61
	v_and_b32_e32 v187, 0xffff0000, v61
	v_cvt_pk_f32_fp8_e32 v[160:161], v106
	v_cvt_pk_f32_fp8_sdwa v[162:163], v106 src0_sel:WORD_1
	v_pk_fma_f32 v[184:185], v[160:161], s[10:11], v[184:185] op_sel_hi:[1,0,1]
	v_pk_fma_f32 v[186:187], v[162:163], s[10:11], v[186:187] op_sel_hi:[1,0,1]
	v_cvt_pk_f32_fp8_e32 v[164:165], v110
	v_cvt_pk_f32_fp8_sdwa v[166:167], v110 src0_sel:WORD_1
	v_pk_fma_f32 v[184:185], v[164:165], s[10:11], v[184:185] op_sel_hi:[1,0,1]
	v_pk_fma_f32 v[186:187], v[166:167], s[10:11], v[186:187] op_sel_hi:[1,0,1]
	v_cvt_pk_f32_fp8_e32 v[168:169], v114
	v_cvt_pk_f32_fp8_sdwa v[170:171], v114 src0_sel:WORD_1
	v_pk_fma_f32 v[184:185], v[168:169], s[10:11], v[184:185] op_sel_hi:[1,0,1]
	v_pk_fma_f32 v[186:187], v[170:171], s[10:11], v[186:187] op_sel_hi:[1,0,1]
	v_cvt_pk_f32_fp8_e32 v[172:173], v118
	v_cvt_pk_f32_fp8_sdwa v[174:175], v118 src0_sel:WORD_1
	v_pk_fma_f32 v[184:185], v[172:173], s[10:11], v[184:185] op_sel_hi:[1,0,1]
	v_pk_fma_f32 v[186:187], v[174:175], s[10:11], v[186:187] op_sel_hi:[1,0,1]
	global_store_dwordx4 v158, v[184:187], s[4:5] offset:2048
	v_lshlrev_b32_e32 v188, 16, v62
	v_and_b32_e32 v189, 0xffff0000, v62
	v_lshlrev_b32_e32 v190, 16, v63
	v_and_b32_e32 v191, 0xffff0000, v63
	v_cvt_pk_f32_fp8_e32 v[160:161], v107
	v_cvt_pk_f32_fp8_sdwa v[162:163], v107 src0_sel:WORD_1
	v_pk_fma_f32 v[188:189], v[160:161], s[10:11], v[188:189] op_sel_hi:[1,0,1]
	v_pk_fma_f32 v[190:191], v[162:163], s[10:11], v[190:191] op_sel_hi:[1,0,1]
	v_cvt_pk_f32_fp8_e32 v[164:165], v111
	v_cvt_pk_f32_fp8_sdwa v[166:167], v111 src0_sel:WORD_1
	v_pk_fma_f32 v[188:189], v[164:165], s[10:11], v[188:189] op_sel_hi:[1,0,1]
	v_pk_fma_f32 v[190:191], v[166:167], s[10:11], v[190:191] op_sel_hi:[1,0,1]
	v_cvt_pk_f32_fp8_e32 v[168:169], v115
	v_cvt_pk_f32_fp8_sdwa v[170:171], v115 src0_sel:WORD_1
	v_pk_fma_f32 v[188:189], v[168:169], s[10:11], v[188:189] op_sel_hi:[1,0,1]
	v_pk_fma_f32 v[190:191], v[170:171], s[10:11], v[190:191] op_sel_hi:[1,0,1]
	v_cvt_pk_f32_fp8_e32 v[172:173], v119
	v_cvt_pk_f32_fp8_sdwa v[174:175], v119 src0_sel:WORD_1
	v_pk_fma_f32 v[188:189], v[172:173], s[10:11], v[188:189] op_sel_hi:[1,0,1]
	v_pk_fma_f32 v[190:191], v[174:175], s[10:11], v[190:191] op_sel_hi:[1,0,1]
	global_store_dwordx4 v158, v[188:191], s[4:5] offset:3072
	v_lshl_add_u32 v200, v16, 2, s23
	v_lshl_add_u32 v201, v17, 2, s23
	v_lshl_add_u32 v202, v18, 2, s23
	v_lshl_add_u32 v203, v19, 2, s23
	ds_read_b32 v144, v200
	ds_read_b32 v145, v201
	ds_read_b32 v146, v202
	ds_read_b32 v147, v203
	s_waitcnt lgkmcnt(0)
	v_lshl_add_u32 v144, v144, 8, v32
	v_lshl_add_u32 v145, v145, 8, v33
	v_lshl_add_u32 v146, v146, 8, v34
	v_lshl_add_u32 v147, v147, 8, v35
	v_lshl_add_u32 v144, v144, 11, v4
	v_lshl_add_u32 v145, v145, 11, v4
	v_lshl_add_u32 v146, v146, 11, v4
	v_lshl_add_u32 v147, v147, 11, v4
	global_load_dword v104, v144, s[6:7]
	global_load_dword v105, v144, s[6:7] offset:256
	global_load_dword v106, v144, s[6:7] offset:512
	global_load_dword v107, v144, s[6:7] offset:768
	global_load_dword v108, v145, s[6:7]
	global_load_dword v109, v145, s[6:7] offset:256
	global_load_dword v110, v145, s[6:7] offset:512
	global_load_dword v111, v145, s[6:7] offset:768
	global_load_dword v112, v146, s[6:7]
	global_load_dword v113, v146, s[6:7] offset:256
	global_load_dword v114, v146, s[6:7] offset:512
	global_load_dword v115, v146, s[6:7] offset:768
	global_load_dword v116, v147, s[6:7]
	global_load_dword v117, v147, s[6:7] offset:256
	global_load_dword v118, v147, s[6:7] offset:512
	global_load_dword v119, v147, s[6:7] offset:768
	s_waitcnt vmcnt(63)
; __device__ __forceinline__ float bf_lo(unsigned w) { return __uint_as_float(w << 16); }
; __device__ __forceinline__ float bf_hi(unsigned w) { return __uint_as_float(w & 0xffff0000u); }
; __global__ void __launch_bounds__(512, 2) fwd_kernel(Params p) {
;     ...
;             for (int u = 0; u < UN; ++u) { const int it = it0 + u * NGT < NI ? it0 + u * NGT : it0; mm[u] = it >> 7; cc[u] = (it & 127) * 16;
;                 const i32x4 e4 = *(const i32x4*)(tok_e + mm[u] * 4), r4 = *(const i32x4*)(tok_rank + mm[u] * 4);
; #pragma unroll
;                 for (int k = 0; k < 4; ++k) { ee[u][k] = e4[k]; rk[u][k] = r4[k]; }
;                 const bf16_t* xp = X1 + (size_t)mm[u] * DM + cc[u]; xa[u] = *(const u32x4*)xp; xb[u] = *(const u32x4*)(xp + 8); }
; #pragma unroll
;             for (int u = 0; u < UN; ++u)
; #pragma unroll
;                 for (int k = 0; k < 4; ++k) { const int pos = ts[ee[u][k]] * 256 + rk[u][k]; y[u][k] = *(const u32x4*)(Yb + (size_t)pos * DM + cc[u]); }
; #pragma unroll
;             for (int u = 0; u < UN; ++u) {
;                 f32x4 a[4];
;                 a[0] = (f32x4){bf_lo(xa[u].x), bf_hi(xa[u].x), bf_lo(xa[u].y), bf_hi(xa[u].y)}; a[1] = (f32x4){bf_lo(xa[u].z), bf_hi(xa[u].z), bf_lo(xa[u].w), bf_hi(xa[u].w)};
;                 a[2] = (f32x4){bf_lo(xb[u].x), bf_hi(xb[u].x), bf_lo(xb[u].y), bf_hi(xb[u].y)}; a[3] = (f32x4){bf_lo(xb[u].z), bf_hi(xb[u].z), bf_lo(xb[u].w), bf_hi(xb[u].w)};
; #pragma unroll
;                 for (int k = 0; k < 4; ++k)
; #pragma unroll
;                     for (int q = 0; q < 4; ++q) { const f32x2 lo = __builtin_amdgcn_cvt_pk_f32_fp8((int)y[u][k][q], false), hi = __builtin_amdgcn_cvt_pk_f32_fp8((int)y[u][k][q], true);
;                         a[q].x += lo.x * (1.0f / Y8_SCALE); a[q].y += lo.y * (1.0f / Y8_SCALE); a[q].z += hi.x * (1.0f / Y8_SCALE); a[q].w += hi.y * (1.0f / Y8_SCALE); }
;                 if (it0 + u * NGT < NI) { float* op = p.out + (size_t)mm[u] * DM + cc[u];
; #pragma unroll
;                     for (int q = 0; q < 4; ++q) *(f32x4*)(op + 4 * q) = a[q]; }
	v_lshlrev_b32_e32 v176, 16, v64
	v_and_b32_e32 v177, 0xffff0000, v64
	v_lshlrev_b32_e32 v178, 16, v65
	v_and_b32_e32 v179, 0xffff0000, v65
	v_cvt_pk_f32_fp8_e32 v[160:161], v120
	v_cvt_pk_f32_fp8_sdwa v[162:163], v120 src0_sel:WORD_1
	v_pk_fma_f32 v[176:177], v[160:161], s[10:11], v[176:177] op_sel_hi:[1,0,1]
	v_pk_fma_f32 v[178:179], v[162:163], s[10:11], v[178:179] op_sel_hi:[1,0,1]
	v_cvt_pk_f32_fp8_e32 v[164:165], v124
	v_cvt_pk_f32_fp8_sdwa v[166:167], v124 src0_sel:WORD_1
	v_pk_fma_f32 v[176:177], v[164:165], s[10:11], v[176:177] op_sel_hi:[1,0,1]
	v_pk_fma_f32 v[178:179], v[166:167], s[10:11], v[178:179] op_sel_hi:[1,0,1]
	v_cvt_pk_f32_fp8_e32 v[168:169], v128
	v_cvt_pk_f32_fp8_sdwa v[170:171], v128 src0_sel:WORD_1
	v_pk_fma_f32 v[176:177], v[168:169], s[10:11], v[176:177] op_sel_hi:[1,0,1]
	v_pk_fma_f32 v[178:179], v[170:171], s[10:11], v[178:179] op_sel_hi:[1,0,1]
	v_cvt_pk_f32_fp8_e32 v[172:173], v132
	v_cvt_pk_f32_fp8_sdwa v[174:175], v132 src0_sel:WORD_1
	v_pk_fma_f32 v[176:177], v[172:173], s[10:11], v[176:177] op_sel_hi:[1,0,1]
	v_pk_fma_f32 v[178:179], v[174:175], s[10:11], v[178:179] op_sel_hi:[1,0,1]
	global_store_dwordx4 v159, v[176:179], s[4:5]
	v_lshlrev_b32_e32 v180, 16, v66
	v_and_b32_e32 v181, 0xffff0000, v66
	v_lshlrev_b32_e32 v182, 16, v67
	v_and_b32_e32 v183, 0xffff0000, v67
	v_cvt_pk_f32_fp8_e32 v[160:161], v121
	v_cvt_pk_f32_fp8_sdwa v[162:163], v121 src0_sel:WORD_1
	v_pk_fma_f32 v[180:181], v[160:161], s[10:11], v[180:181] op_sel_hi:[1,0,1]
	v_pk_fma_f32 v[182:183], v[162:163], s[10:11], v[182:183] op_sel_hi:[1,0,1]
	v_cvt_pk_f32_fp8_e32 v[164:165], v125
	v_cvt_pk_f32_fp8_sdwa v[166:167], v125 src0_sel:WORD_1
	v_pk_fma_f32 v[180:181], v[164:165], s[10:11], v[180:181] op_sel_hi:[1,0,1]
	v_pk_fma_f32 v[182:183], v[166:167], s[10:11], v[182:183] op_sel_hi:[1,0,1]
	v_cvt_pk_f32_fp8_e32 v[168:169], v129
	v_cvt_pk_f32_fp8_sdwa v[170:171], v129 src0_sel:WORD_1
	v_pk_fma_f32 v[180:181], v[168:169], s[10:11], v[180:181] op_sel_hi:[1,0,1]
	v_pk_fma_f32 v[182:183], v[170:171], s[10:11], v[182:183] op_sel_hi:[1,0,1]
	v_cvt_pk_f32_fp8_e32 v[172:173], v133
	v_cvt_pk_f32_fp8_sdwa v[174:175], v133 src0_sel:WORD_1
	v_pk_fma_f32 v[180:181], v[172:173], s[10:11], v[180:181] op_sel_hi:[1,0,1]
	v_pk_fma_f32 v[182:183], v[174:175], s[10:11], v[182:183] op_sel_hi:[1,0,1]
	global_store_dwordx4 v159, v[180:183], s[4:5] offset:1024
	v_lshlrev_b32_e32 v184, 16, v68
	v_and_b32_e32 v185, 0xffff0000, v68
	v_lshlrev_b32_e32 v186, 16, v69
	v_and_b32_e32 v187, 0xffff0000, v69
	v_cvt_pk_f32_fp8_e32 v[160:161], v122
	v_cvt_pk_f32_fp8_sdwa v[162:163], v122 src0_sel:WORD_1
	v_pk_fma_f32 v[184:185], v[160:161], s[10:11], v[184:185] op_sel_hi:[1,0,1]
	v_pk_fma_f32 v[186:187], v[162:163], s[10:11], v[186:187] op_sel_hi:[1,0,1]
	v_cvt_pk_f32_fp8_e32 v[164:165], v126
	v_cvt_pk_f32_fp8_sdwa v[166:167], v126 src0_sel:WORD_1
	v_pk_fma_f32 v[184:185], v[164:165], s[10:11], v[184:185] op_sel_hi:[1,0,1]
	v_pk_fma_f32 v[186:187], v[166:167], s[10:11], v[186:187] op_sel_hi:[1,0,1]
	v_cvt_pk_f32_fp8_e32 v[168:169], v130
	v_cvt_pk_f32_fp8_sdwa v[170:171], v130 src0_sel:WORD_1
	v_pk_fma_f32 v[184:185], v[168:169], s[10:11], v[184:185] op_sel_hi:[1,0,1]
	v_pk_fma_f32 v[186:187], v[170:171], s[10:11], v[186:187] op_sel_hi:[1,0,1]
	v_cvt_pk_f32_fp8_e32 v[172:173], v134
	v_cvt_pk_f32_fp8_sdwa v[174:175], v134 src0_sel:WORD_1
	v_pk_fma_f32 v[184:185], v[172:173], s[10:11], v[184:185] op_sel_hi:[1,0,1]
	v_pk_fma_f32 v[186:187], v[174:175], s[10:11], v[186:187] op_sel_hi:[1,0,1]
	global_store_dwordx4 v159, v[184:187], s[4:5] offset:2048
	v_lshlrev_b32_e32 v188, 16, v70
	v_and_b32_e32 v189, 0xffff0000, v70
	v_lshlrev_b32_e32 v190, 16, v71
	v_and_b32_e32 v191, 0xffff0000, v71
	v_cvt_pk_f32_fp8_e32 v[160:161], v123
	v_cvt_pk_f32_fp8_sdwa v[162:163], v123 src0_sel:WORD_1
	v_pk_fma_f32 v[188:189], v[160:161], s[10:11], v[188:189] op_sel_hi:[1,0,1]
	v_pk_fma_f32 v[190:191], v[162:163], s[10:11], v[190:191] op_sel_hi:[1,0,1]
	v_cvt_pk_f32_fp8_e32 v[164:165], v127
	v_cvt_pk_f32_fp8_sdwa v[166:167], v127 src0_sel:WORD_1
	v_pk_fma_f32 v[188:189], v[164:165], s[10:11], v[188:189] op_sel_hi:[1,0,1]
	v_pk_fma_f32 v[190:191], v[166:167], s[10:11], v[190:191] op_sel_hi:[1,0,1]
	v_cvt_pk_f32_fp8_e32 v[168:169], v131
	v_cvt_pk_f32_fp8_sdwa v[170:171], v131 src0_sel:WORD_1
	v_pk_fma_f32 v[188:189], v[168:169], s[10:11], v[188:189] op_sel_hi:[1,0,1]
	v_pk_fma_f32 v[190:191], v[170:171], s[10:11], v[190:191] op_sel_hi:[1,0,1]
	v_cvt_pk_f32_fp8_e32 v[172:173], v135
	v_cvt_pk_f32_fp8_sdwa v[174:175], v135 src0_sel:WORD_1
	v_pk_fma_f32 v[188:189], v[172:173], s[10:11], v[188:189] op_sel_hi:[1,0,1]
	v_pk_fma_f32 v[190:191], v[174:175], s[10:11], v[190:191] op_sel_hi:[1,0,1]
	global_store_dwordx4 v159, v[188:191], s[4:5] offset:3072
	v_lshl_add_u32 v200, v20, 2, s23
	v_lshl_add_u32 v201, v21, 2, s23
	v_lshl_add_u32 v202, v22, 2, s23
	v_lshl_add_u32 v203, v23, 2, s23
	ds_read_b32 v148, v200
	ds_read_b32 v149, v201
	ds_read_b32 v150, v202
	ds_read_b32 v151, v203
	s_waitcnt lgkmcnt(0)
	v_lshl_add_u32 v148, v148, 8, v36
	v_lshl_add_u32 v149, v149, 8, v37
	v_lshl_add_u32 v150, v150, 8, v38
	v_lshl_add_u32 v151, v151, 8, v39
	v_lshl_add_u32 v148, v148, 11, v4
	v_lshl_add_u32 v149, v149, 11, v4
	v_lshl_add_u32 v150, v150, 11, v4
	v_lshl_add_u32 v151, v151, 11, v4
	global_load_dword v120, v148, s[6:7]
	global_load_dword v121, v148, s[6:7] offset:256
	global_load_dword v122, v148, s[6:7] offset:512
	global_load_dword v123, v148, s[6:7] offset:768
	global_load_dword v124, v149, s[6:7]
	global_load_dword v125, v149, s[6:7] offset:256
	global_load_dword v126, v149, s[6:7] offset:512
	global_load_dword v127, v149, s[6:7] offset:768
	global_load_dword v128, v150, s[6:7]
	global_load_dword v129, v150, s[6:7] offset:256
	global_load_dword v130, v150, s[6:7] offset:512
	global_load_dword v131, v150, s[6:7] offset:768
	global_load_dword v132, v151, s[6:7]
	global_load_dword v133, v151, s[6:7] offset:256
	global_load_dword v134, v151, s[6:7] offset:512
	global_load_dword v135, v151, s[6:7] offset:768
	s_waitcnt vmcnt(60)
; __device__ __forceinline__ float bf_lo(unsigned w) { return __uint_as_float(w << 16); }
; __device__ __forceinline__ float bf_hi(unsigned w) { return __uint_as_float(w & 0xffff0000u); }
; __global__ void __launch_bounds__(512, 2) fwd_kernel(Params p) {
;     ...
;             for (int u = 0; u < UN; ++u) { const int it = it0 + u * NGT < NI ? it0 + u * NGT : it0; mm[u] = it >> 7; cc[u] = (it & 127) * 16;
;                 const i32x4 e4 = *(const i32x4*)(tok_e + mm[u] * 4), r4 = *(const i32x4*)(tok_rank + mm[u] * 4);
; #pragma unroll
;                 for (int k = 0; k < 4; ++k) { ee[u][k] = e4[k]; rk[u][k] = r4[k]; }
;                 const bf16_t* xp = X1 + (size_t)mm[u] * DM + cc[u]; xa[u] = *(const u32x4*)xp; xb[u] = *(const u32x4*)(xp + 8); }
; #pragma unroll
;             for (int u = 0; u < UN; ++u)
; #pragma unroll
;                 for (int k = 0; k < 4; ++k) { const int pos = ts[ee[u][k]] * 256 + rk[u][k]; y[u][k] = *(const u32x4*)(Yb + (size_t)pos * DM + cc[u]); }
; #pragma unroll
;             for (int u = 0; u < UN; ++u) {
;                 f32x4 a[4];
;                 a[0] = (f32x4){bf_lo(xa[u].x), bf_hi(xa[u].x), bf_lo(xa[u].y), bf_hi(xa[u].y)}; a[1] = (f32x4){bf_lo(xa[u].z), bf_hi(xa[u].z), bf_lo(xa[u].w), bf_hi(xa[u].w)};
;                 a[2] = (f32x4){bf_lo(xb[u].x), bf_hi(xb[u].x), bf_lo(xb[u].y), bf_hi(xb[u].y)}; a[3] = (f32x4){bf_lo(xb[u].z), bf_hi(xb[u].z), bf_lo(xb[u].w), bf_hi(xb[u].w)};
; #pragma unroll
;                 for (int k = 0; k < 4; ++k)
; #pragma unroll
;                     for (int q = 0; q < 4; ++q) { const f32x2 lo = __builtin_amdgcn_cvt_pk_f32_fp8((int)y[u][k][q], false), hi = __builtin_amdgcn_cvt_pk_f32_fp8((int)y[u][k][q], true);
;                         a[q].x += lo.x * (1.0f / Y8_SCALE); a[q].y += lo.y * (1.0f / Y8_SCALE); a[q].z += hi.x * (1.0f / Y8_SCALE); a[q].w += hi.y * (1.0f / Y8_SCALE); }
;                 if (it0 + u * NGT < NI) { float* op = p.out + (size_t)mm[u] * DM + cc[u];
; #pragma unroll
;                     for (int q = 0; q < 4; ++q) *(f32x4*)(op + 4 * q) = a[q]; }
	v_lshlrev_b32_e32 v176, 16, v216
	v_and_b32_e32 v177, 0xffff0000, v216
	v_lshlrev_b32_e32 v178, 16, v217
	v_and_b32_e32 v179, 0xffff0000, v217
	v_cvt_pk_f32_fp8_e32 v[160:161], v72
	v_cvt_pk_f32_fp8_sdwa v[162:163], v72 src0_sel:WORD_1
	v_pk_fma_f32 v[176:177], v[160:161], s[10:11], v[176:177] op_sel_hi:[1,0,1]
	v_pk_fma_f32 v[178:179], v[162:163], s[10:11], v[178:179] op_sel_hi:[1,0,1]
	v_cvt_pk_f32_fp8_e32 v[164:165], v76
	v_cvt_pk_f32_fp8_sdwa v[166:167], v76 src0_sel:WORD_1
	v_pk_fma_f32 v[176:177], v[164:165], s[10:11], v[176:177] op_sel_hi:[1,0,1]
	v_pk_fma_f32 v[178:179], v[166:167], s[10:11], v[178:179] op_sel_hi:[1,0,1]
	v_cvt_pk_f32_fp8_e32 v[168:169], v80
	v_cvt_pk_f32_fp8_sdwa v[170:171], v80 src0_sel:WORD_1
	v_pk_fma_f32 v[176:177], v[168:169], s[10:11], v[176:177] op_sel_hi:[1,0,1]
	v_pk_fma_f32 v[178:179], v[170:171], s[10:11], v[178:179] op_sel_hi:[1,0,1]
	v_cvt_pk_f32_fp8_e32 v[172:173], v84
	v_cvt_pk_f32_fp8_sdwa v[174:175], v84 src0_sel:WORD_1
	v_pk_fma_f32 v[176:177], v[172:173], s[10:11], v[176:177] op_sel_hi:[1,0,1]
	v_pk_fma_f32 v[178:179], v[174:175], s[10:11], v[178:179] op_sel_hi:[1,0,1]
	global_store_dwordx4 v248, v[176:179], s[4:5]
	v_lshlrev_b32_e32 v180, 16, v218
	v_and_b32_e32 v181, 0xffff0000, v218
	v_lshlrev_b32_e32 v182, 16, v219
	v_and_b32_e32 v183, 0xffff0000, v219
	v_cvt_pk_f32_fp8_e32 v[160:161], v73
	v_cvt_pk_f32_fp8_sdwa v[162:163], v73 src0_sel:WORD_1
	v_pk_fma_f32 v[180:181], v[160:161], s[10:11], v[180:181] op_sel_hi:[1,0,1]
	v_pk_fma_f32 v[182:183], v[162:163], s[10:11], v[182:183] op_sel_hi:[1,0,1]
	v_cvt_pk_f32_fp8_e32 v[164:165], v77
	v_cvt_pk_f32_fp8_sdwa v[166:167], v77 src0_sel:WORD_1
	v_pk_fma_f32 v[180:181], v[164:165], s[10:11], v[180:181] op_sel_hi:[1,0,1]
	v_pk_fma_f32 v[182:183], v[166:167], s[10:11], v[182:183] op_sel_hi:[1,0,1]
	v_cvt_pk_f32_fp8_e32 v[168:169], v81
	v_cvt_pk_f32_fp8_sdwa v[170:171], v81 src0_sel:WORD_1
	v_pk_fma_f32 v[180:181], v[168:169], s[10:11], v[180:181] op_sel_hi:[1,0,1]
	v_pk_fma_f32 v[182:183], v[170:171], s[10:11], v[182:183] op_sel_hi:[1,0,1]
	v_cvt_pk_f32_fp8_e32 v[172:173], v85
	v_cvt_pk_f32_fp8_sdwa v[174:175], v85 src0_sel:WORD_1
	v_pk_fma_f32 v[180:181], v[172:173], s[10:11], v[180:181] op_sel_hi:[1,0,1]
	v_pk_fma_f32 v[182:183], v[174:175], s[10:11], v[182:183] op_sel_hi:[1,0,1]
	global_store_dwordx4 v248, v[180:183], s[4:5] offset:1024
	v_lshlrev_b32_e32 v184, 16, v220
	v_and_b32_e32 v185, 0xffff0000, v220
	v_lshlrev_b32_e32 v186, 16, v221
	v_and_b32_e32 v187, 0xffff0000, v221
	v_cvt_pk_f32_fp8_e32 v[160:161], v74
	v_cvt_pk_f32_fp8_sdwa v[162:163], v74 src0_sel:WORD_1
	v_pk_fma_f32 v[184:185], v[160:161], s[10:11], v[184:185] op_sel_hi:[1,0,1]
	v_pk_fma_f32 v[186:187], v[162:163], s[10:11], v[186:187] op_sel_hi:[1,0,1]
	v_cvt_pk_f32_fp8_e32 v[164:165], v78
	v_cvt_pk_f32_fp8_sdwa v[166:167], v78 src0_sel:WORD_1
	v_pk_fma_f32 v[184:185], v[164:165], s[10:11], v[184:185] op_sel_hi:[1,0,1]
	v_pk_fma_f32 v[186:187], v[166:167], s[10:11], v[186:187] op_sel_hi:[1,0,1]
	v_cvt_pk_f32_fp8_e32 v[168:169], v82
	v_cvt_pk_f32_fp8_sdwa v[170:171], v82 src0_sel:WORD_1
	v_pk_fma_f32 v[184:185], v[168:169], s[10:11], v[184:185] op_sel_hi:[1,0,1]
	v_pk_fma_f32 v[186:187], v[170:171], s[10:11], v[186:187] op_sel_hi:[1,0,1]
	v_cvt_pk_f32_fp8_e32 v[172:173], v86
	v_cvt_pk_f32_fp8_sdwa v[174:175], v86 src0_sel:WORD_1
	v_pk_fma_f32 v[184:185], v[172:173], s[10:11], v[184:185] op_sel_hi:[1,0,1]
	v_pk_fma_f32 v[186:187], v[174:175], s[10:11], v[186:187] op_sel_hi:[1,0,1]
	global_store_dwordx4 v248, v[184:187], s[4:5] offset:2048
	v_lshlrev_b32_e32 v188, 16, v222
	v_and_b32_e32 v189, 0xffff0000, v222
	v_lshlrev_b32_e32 v190, 16, v223
	v_and_b32_e32 v191, 0xffff0000, v223
	v_cvt_pk_f32_fp8_e32 v[160:161], v75
	v_cvt_pk_f32_fp8_sdwa v[162:163], v75 src0_sel:WORD_1
	v_pk_fma_f32 v[188:189], v[160:161], s[10:11], v[188:189] op_sel_hi:[1,0,1]
	v_pk_fma_f32 v[190:191], v[162:163], s[10:11], v[190:191] op_sel_hi:[1,0,1]
	v_cvt_pk_f32_fp8_e32 v[164:165], v79
	v_cvt_pk_f32_fp8_sdwa v[166:167], v79 src0_sel:WORD_1
	v_pk_fma_f32 v[188:189], v[164:165], s[10:11], v[188:189] op_sel_hi:[1,0,1]
	v_pk_fma_f32 v[190:191], v[166:167], s[10:11], v[190:191] op_sel_hi:[1,0,1]
	v_cvt_pk_f32_fp8_e32 v[168:169], v83
	v_cvt_pk_f32_fp8_sdwa v[170:171], v83 src0_sel:WORD_1
	v_pk_fma_f32 v[188:189], v[168:169], s[10:11], v[188:189] op_sel_hi:[1,0,1]
	v_pk_fma_f32 v[190:191], v[170:171], s[10:11], v[190:191] op_sel_hi:[1,0,1]
	v_cvt_pk_f32_fp8_e32 v[172:173], v87
	v_cvt_pk_f32_fp8_sdwa v[174:175], v87 src0_sel:WORD_1
	v_pk_fma_f32 v[188:189], v[172:173], s[10:11], v[188:189] op_sel_hi:[1,0,1]
	v_pk_fma_f32 v[190:191], v[174:175], s[10:11], v[190:191] op_sel_hi:[1,0,1]
	global_store_dwordx4 v248, v[188:191], s[4:5] offset:3072
	s_waitcnt vmcnt(44)
; __device__ __forceinline__ float bf_lo(unsigned w) { return __uint_as_float(w << 16); }
; __device__ __forceinline__ float bf_hi(unsigned w) { return __uint_as_float(w & 0xffff0000u); }
; __global__ void __launch_bounds__(512, 2) fwd_kernel(Params p) {
;     ...
;             for (int u = 0; u < UN; ++u) { const int it = it0 + u * NGT < NI ? it0 + u * NGT : it0; mm[u] = it >> 7; cc[u] = (it & 127) * 16;
;                 const i32x4 e4 = *(const i32x4*)(tok_e + mm[u] * 4), r4 = *(const i32x4*)(tok_rank + mm[u] * 4);
; #pragma unroll
;                 for (int k = 0; k < 4; ++k) { ee[u][k] = e4[k]; rk[u][k] = r4[k]; }
;                 const bf16_t* xp = X1 + (size_t)mm[u] * DM + cc[u]; xa[u] = *(const u32x4*)xp; xb[u] = *(const u32x4*)(xp + 8); }
; #pragma unroll
;             for (int u = 0; u < UN; ++u)
; #pragma unroll
;                 for (int k = 0; k < 4; ++k) { const int pos = ts[ee[u][k]] * 256 + rk[u][k]; y[u][k] = *(const u32x4*)(Yb + (size_t)pos * DM + cc[u]); }
; #pragma unroll
;             for (int u = 0; u < UN; ++u) {
;                 f32x4 a[4];
;                 a[0] = (f32x4){bf_lo(xa[u].x), bf_hi(xa[u].x), bf_lo(xa[u].y), bf_hi(xa[u].y)}; a[1] = (f32x4){bf_lo(xa[u].z), bf_hi(xa[u].z), bf_lo(xa[u].w), bf_hi(xa[u].w)};
;                 a[2] = (f32x4){bf_lo(xb[u].x), bf_hi(xb[u].x), bf_lo(xb[u].y), bf_hi(xb[u].y)}; a[3] = (f32x4){bf_lo(xb[u].z), bf_hi(xb[u].z), bf_lo(xb[u].w), bf_hi(xb[u].w)};
; #pragma unroll
;                 for (int k = 0; k < 4; ++k)
; #pragma unroll
;                     for (int q = 0; q < 4; ++q) { const f32x2 lo = __builtin_amdgcn_cvt_pk_f32_fp8((int)y[u][k][q], false), hi = __builtin_amdgcn_cvt_pk_f32_fp8((int)y[u][k][q], true);
;                         a[q].x += lo.x * (1.0f / Y8_SCALE); a[q].y += lo.y * (1.0f / Y8_SCALE); a[q].z += hi.x * (1.0f / Y8_SCALE); a[q].w += hi.y * (1.0f / Y8_SCALE); }
;                 if (it0 + u * NGT < NI) { float* op = p.out + (size_t)mm[u] * DM + cc[u];
; #pragma unroll
;                     for (int q = 0; q < 4; ++q) *(f32x4*)(op + 4 * q) = a[q]; }
	v_lshlrev_b32_e32 v176, 16, v224
	v_and_b32_e32 v177, 0xffff0000, v224
	v_lshlrev_b32_e32 v178, 16, v225
	v_and_b32_e32 v179, 0xffff0000, v225
	v_cvt_pk_f32_fp8_e32 v[160:161], v88
	v_cvt_pk_f32_fp8_sdwa v[162:163], v88 src0_sel:WORD_1
	v_pk_fma_f32 v[176:177], v[160:161], s[10:11], v[176:177] op_sel_hi:[1,0,1]
	v_pk_fma_f32 v[178:179], v[162:163], s[10:11], v[178:179] op_sel_hi:[1,0,1]
	v_cvt_pk_f32_fp8_e32 v[164:165], v92
	v_cvt_pk_f32_fp8_sdwa v[166:167], v92 src0_sel:WORD_1
	v_pk_fma_f32 v[176:177], v[164:165], s[10:11], v[176:177] op_sel_hi:[1,0,1]
	v_pk_fma_f32 v[178:179], v[166:167], s[10:11], v[178:179] op_sel_hi:[1,0,1]
	v_cvt_pk_f32_fp8_e32 v[168:169], v96
	v_cvt_pk_f32_fp8_sdwa v[170:171], v96 src0_sel:WORD_1
	v_pk_fma_f32 v[176:177], v[168:169], s[10:11], v[176:177] op_sel_hi:[1,0,1]
	v_pk_fma_f32 v[178:179], v[170:171], s[10:11], v[178:179] op_sel_hi:[1,0,1]
	v_cvt_pk_f32_fp8_e32 v[172:173], v100
	v_cvt_pk_f32_fp8_sdwa v[174:175], v100 src0_sel:WORD_1
	v_pk_fma_f32 v[176:177], v[172:173], s[10:11], v[176:177] op_sel_hi:[1,0,1]
	v_pk_fma_f32 v[178:179], v[174:175], s[10:11], v[178:179] op_sel_hi:[1,0,1]
	global_store_dwordx4 v249, v[176:179], s[4:5]
	v_lshlrev_b32_e32 v180, 16, v226
	v_and_b32_e32 v181, 0xffff0000, v226
	v_lshlrev_b32_e32 v182, 16, v227
	v_and_b32_e32 v183, 0xffff0000, v227
	v_cvt_pk_f32_fp8_e32 v[160:161], v89
	v_cvt_pk_f32_fp8_sdwa v[162:163], v89 src0_sel:WORD_1
	v_pk_fma_f32 v[180:181], v[160:161], s[10:11], v[180:181] op_sel_hi:[1,0,1]
	v_pk_fma_f32 v[182:183], v[162:163], s[10:11], v[182:183] op_sel_hi:[1,0,1]
	v_cvt_pk_f32_fp8_e32 v[164:165], v93
	v_cvt_pk_f32_fp8_sdwa v[166:167], v93 src0_sel:WORD_1
	v_pk_fma_f32 v[180:181], v[164:165], s[10:11], v[180:181] op_sel_hi:[1,0,1]
	v_pk_fma_f32 v[182:183], v[166:167], s[10:11], v[182:183] op_sel_hi:[1,0,1]
	v_cvt_pk_f32_fp8_e32 v[168:169], v97
	v_cvt_pk_f32_fp8_sdwa v[170:171], v97 src0_sel:WORD_1
	v_pk_fma_f32 v[180:181], v[168:169], s[10:11], v[180:181] op_sel_hi:[1,0,1]
	v_pk_fma_f32 v[182:183], v[170:171], s[10:11], v[182:183] op_sel_hi:[1,0,1]
	v_cvt_pk_f32_fp8_e32 v[172:173], v101
	v_cvt_pk_f32_fp8_sdwa v[174:175], v101 src0_sel:WORD_1
	v_pk_fma_f32 v[180:181], v[172:173], s[10:11], v[180:181] op_sel_hi:[1,0,1]
	v_pk_fma_f32 v[182:183], v[174:175], s[10:11], v[182:183] op_sel_hi:[1,0,1]
	global_store_dwordx4 v249, v[180:183], s[4:5] offset:1024
	v_lshlrev_b32_e32 v184, 16, v228
	v_and_b32_e32 v185, 0xffff0000, v228
	v_lshlrev_b32_e32 v186, 16, v229
	v_and_b32_e32 v187, 0xffff0000, v229
	v_cvt_pk_f32_fp8_e32 v[160:161], v90
	v_cvt_pk_f32_fp8_sdwa v[162:163], v90 src0_sel:WORD_1
	v_pk_fma_f32 v[184:185], v[160:161], s[10:11], v[184:185] op_sel_hi:[1,0,1]
	v_pk_fma_f32 v[186:187], v[162:163], s[10:11], v[186:187] op_sel_hi:[1,0,1]
	v_cvt_pk_f32_fp8_e32 v[164:165], v94
	v_cvt_pk_f32_fp8_sdwa v[166:167], v94 src0_sel:WORD_1
	v_pk_fma_f32 v[184:185], v[164:165], s[10:11], v[184:185] op_sel_hi:[1,0,1]
	v_pk_fma_f32 v[186:187], v[166:167], s[10:11], v[186:187] op_sel_hi:[1,0,1]
	v_cvt_pk_f32_fp8_e32 v[168:169], v98
	v_cvt_pk_f32_fp8_sdwa v[170:171], v98 src0_sel:WORD_1
	v_pk_fma_f32 v[184:185], v[168:169], s[10:11], v[184:185] op_sel_hi:[1,0,1]
	v_pk_fma_f32 v[186:187], v[170:171], s[10:11], v[186:187] op_sel_hi:[1,0,1]
	v_cvt_pk_f32_fp8_e32 v[172:173], v102
	v_cvt_pk_f32_fp8_sdwa v[174:175], v102 src0_sel:WORD_1
	v_pk_fma_f32 v[184:185], v[172:173], s[10:11], v[184:185] op_sel_hi:[1,0,1]
	v_pk_fma_f32 v[186:187], v[174:175], s[10:11], v[186:187] op_sel_hi:[1,0,1]
	global_store_dwordx4 v249, v[184:187], s[4:5] offset:2048
	v_lshlrev_b32_e32 v188, 16, v230
	v_and_b32_e32 v189, 0xffff0000, v230
	v_lshlrev_b32_e32 v190, 16, v231
	v_and_b32_e32 v191, 0xffff0000, v231
	v_cvt_pk_f32_fp8_e32 v[160:161], v91
	v_cvt_pk_f32_fp8_sdwa v[162:163], v91 src0_sel:WORD_1
	v_pk_fma_f32 v[188:189], v[160:161], s[10:11], v[188:189] op_sel_hi:[1,0,1]
	v_pk_fma_f32 v[190:191], v[162:163], s[10:11], v[190:191] op_sel_hi:[1,0,1]
	v_cvt_pk_f32_fp8_e32 v[164:165], v95
	v_cvt_pk_f32_fp8_sdwa v[166:167], v95 src0_sel:WORD_1
	v_pk_fma_f32 v[188:189], v[164:165], s[10:11], v[188:189] op_sel_hi:[1,0,1]
	v_pk_fma_f32 v[190:191], v[166:167], s[10:11], v[190:191] op_sel_hi:[1,0,1]
	v_cvt_pk_f32_fp8_e32 v[168:169], v99
	v_cvt_pk_f32_fp8_sdwa v[170:171], v99 src0_sel:WORD_1
	v_pk_fma_f32 v[188:189], v[168:169], s[10:11], v[188:189] op_sel_hi:[1,0,1]
	v_pk_fma_f32 v[190:191], v[170:171], s[10:11], v[190:191] op_sel_hi:[1,0,1]
	v_cvt_pk_f32_fp8_e32 v[172:173], v103
	v_cvt_pk_f32_fp8_sdwa v[174:175], v103 src0_sel:WORD_1
	v_pk_fma_f32 v[188:189], v[172:173], s[10:11], v[188:189] op_sel_hi:[1,0,1]
	v_pk_fma_f32 v[190:191], v[174:175], s[10:11], v[190:191] op_sel_hi:[1,0,1]
	global_store_dwordx4 v249, v[188:191], s[4:5] offset:3072
	s_waitcnt vmcnt(28)
; __device__ __forceinline__ float bf_lo(unsigned w) { return __uint_as_float(w << 16); }
; __device__ __forceinline__ float bf_hi(unsigned w) { return __uint_as_float(w & 0xffff0000u); }
; __global__ void __launch_bounds__(512, 2) fwd_kernel(Params p) {
;     ...
;             for (int u = 0; u < UN; ++u) { const int it = it0 + u * NGT < NI ? it0 + u * NGT : it0; mm[u] = it >> 7; cc[u] = (it & 127) * 16;
;                 const i32x4 e4 = *(const i32x4*)(tok_e + mm[u] * 4), r4 = *(const i32x4*)(tok_rank + mm[u] * 4);
; #pragma unroll
;                 for (int k = 0; k < 4; ++k) { ee[u][k] = e4[k]; rk[u][k] = r4[k]; }
;                 const bf16_t* xp = X1 + (size_t)mm[u] * DM + cc[u]; xa[u] = *(const u32x4*)xp; xb[u] = *(const u32x4*)(xp + 8); }
; #pragma unroll
;             for (int u = 0; u < UN; ++u)
; #pragma unroll
;                 for (int k = 0; k < 4; ++k) { const int pos = ts[ee[u][k]] * 256 + rk[u][k]; y[u][k] = *(const u32x4*)(Yb + (size_t)pos * DM + cc[u]); }
; #pragma unroll
;             for (int u = 0; u < UN; ++u) {
;                 f32x4 a[4];
;                 a[0] = (f32x4){bf_lo(xa[u].x), bf_hi(xa[u].x), bf_lo(xa[u].y), bf_hi(xa[u].y)}; a[1] = (f32x4){bf_lo(xa[u].z), bf_hi(xa[u].z), bf_lo(xa[u].w), bf_hi(xa[u].w)};
;                 a[2] = (f32x4){bf_lo(xb[u].x), bf_hi(xb[u].x), bf_lo(xb[u].y), bf_hi(xb[u].y)}; a[3] = (f32x4){bf_lo(xb[u].z), bf_hi(xb[u].z), bf_lo(xb[u].w), bf_hi(xb[u].w)};
; #pragma unroll
;                 for (int k = 0; k < 4; ++k)
; #pragma unroll
;                     for (int q = 0; q < 4; ++q) { const f32x2 lo = __builtin_amdgcn_cvt_pk_f32_fp8((int)y[u][k][q], false), hi = __builtin_amdgcn_cvt_pk_f32_fp8((int)y[u][k][q], true);
;                         a[q].x += lo.x * (1.0f / Y8_SCALE); a[q].y += lo.y * (1.0f / Y8_SCALE); a[q].z += hi.x * (1.0f / Y8_SCALE); a[q].w += hi.y * (1.0f / Y8_SCALE); }
;                 if (it0 + u * NGT < NI) { float* op = p.out + (size_t)mm[u] * DM + cc[u];
; #pragma unroll
;                     for (int q = 0; q < 4; ++q) *(f32x4*)(op + 4 * q) = a[q]; }
	v_lshlrev_b32_e32 v176, 16, v232
	v_and_b32_e32 v177, 0xffff0000, v232
	v_lshlrev_b32_e32 v178, 16, v233
	v_and_b32_e32 v179, 0xffff0000, v233
	v_cvt_pk_f32_fp8_e32 v[160:161], v104
	v_cvt_pk_f32_fp8_sdwa v[162:163], v104 src0_sel:WORD_1
	v_pk_fma_f32 v[176:177], v[160:161], s[10:11], v[176:177] op_sel_hi:[1,0,1]
	v_pk_fma_f32 v[178:179], v[162:163], s[10:11], v[178:179] op_sel_hi:[1,0,1]
	v_cvt_pk_f32_fp8_e32 v[164:165], v108
	v_cvt_pk_f32_fp8_sdwa v[166:167], v108 src0_sel:WORD_1
	v_pk_fma_f32 v[176:177], v[164:165], s[10:11], v[176:177] op_sel_hi:[1,0,1]
	v_pk_fma_f32 v[178:179], v[166:167], s[10:11], v[178:179] op_sel_hi:[1,0,1]
	v_cvt_pk_f32_fp8_e32 v[168:169], v112
	v_cvt_pk_f32_fp8_sdwa v[170:171], v112 src0_sel:WORD_1
	v_pk_fma_f32 v[176:177], v[168:169], s[10:11], v[176:177] op_sel_hi:[1,0,1]
	v_pk_fma_f32 v[178:179], v[170:171], s[10:11], v[178:179] op_sel_hi:[1,0,1]
	v_cvt_pk_f32_fp8_e32 v[172:173], v116
	v_cvt_pk_f32_fp8_sdwa v[174:175], v116 src0_sel:WORD_1
	v_pk_fma_f32 v[176:177], v[172:173], s[10:11], v[176:177] op_sel_hi:[1,0,1]
	v_pk_fma_f32 v[178:179], v[174:175], s[10:11], v[178:179] op_sel_hi:[1,0,1]
	global_store_dwordx4 v250, v[176:179], s[4:5]
	v_lshlrev_b32_e32 v180, 16, v234
	v_and_b32_e32 v181, 0xffff0000, v234
	v_lshlrev_b32_e32 v182, 16, v235
	v_and_b32_e32 v183, 0xffff0000, v235
	v_cvt_pk_f32_fp8_e32 v[160:161], v105
	v_cvt_pk_f32_fp8_sdwa v[162:163], v105 src0_sel:WORD_1
	v_pk_fma_f32 v[180:181], v[160:161], s[10:11], v[180:181] op_sel_hi:[1,0,1]
	v_pk_fma_f32 v[182:183], v[162:163], s[10:11], v[182:183] op_sel_hi:[1,0,1]
	v_cvt_pk_f32_fp8_e32 v[164:165], v109
	v_cvt_pk_f32_fp8_sdwa v[166:167], v109 src0_sel:WORD_1
	v_pk_fma_f32 v[180:181], v[164:165], s[10:11], v[180:181] op_sel_hi:[1,0,1]
	v_pk_fma_f32 v[182:183], v[166:167], s[10:11], v[182:183] op_sel_hi:[1,0,1]
	v_cvt_pk_f32_fp8_e32 v[168:169], v113
	v_cvt_pk_f32_fp8_sdwa v[170:171], v113 src0_sel:WORD_1
	v_pk_fma_f32 v[180:181], v[168:169], s[10:11], v[180:181] op_sel_hi:[1,0,1]
	v_pk_fma_f32 v[182:183], v[170:171], s[10:11], v[182:183] op_sel_hi:[1,0,1]
	v_cvt_pk_f32_fp8_e32 v[172:173], v117
	v_cvt_pk_f32_fp8_sdwa v[174:175], v117 src0_sel:WORD_1
	v_pk_fma_f32 v[180:181], v[172:173], s[10:11], v[180:181] op_sel_hi:[1,0,1]
	v_pk_fma_f32 v[182:183], v[174:175], s[10:11], v[182:183] op_sel_hi:[1,0,1]
	global_store_dwordx4 v250, v[180:183], s[4:5] offset:1024
	v_lshlrev_b32_e32 v184, 16, v236
	v_and_b32_e32 v185, 0xffff0000, v236
	v_lshlrev_b32_e32 v186, 16, v237
	v_and_b32_e32 v187, 0xffff0000, v237
	v_cvt_pk_f32_fp8_e32 v[160:161], v106
	v_cvt_pk_f32_fp8_sdwa v[162:163], v106 src0_sel:WORD_1
	v_pk_fma_f32 v[184:185], v[160:161], s[10:11], v[184:185] op_sel_hi:[1,0,1]
	v_pk_fma_f32 v[186:187], v[162:163], s[10:11], v[186:187] op_sel_hi:[1,0,1]
	v_cvt_pk_f32_fp8_e32 v[164:165], v110
	v_cvt_pk_f32_fp8_sdwa v[166:167], v110 src0_sel:WORD_1
	v_pk_fma_f32 v[184:185], v[164:165], s[10:11], v[184:185] op_sel_hi:[1,0,1]
	v_pk_fma_f32 v[186:187], v[166:167], s[10:11], v[186:187] op_sel_hi:[1,0,1]
	v_cvt_pk_f32_fp8_e32 v[168:169], v114
	v_cvt_pk_f32_fp8_sdwa v[170:171], v114 src0_sel:WORD_1
	v_pk_fma_f32 v[184:185], v[168:169], s[10:11], v[184:185] op_sel_hi:[1,0,1]
	v_pk_fma_f32 v[186:187], v[170:171], s[10:11], v[186:187] op_sel_hi:[1,0,1]
	v_cvt_pk_f32_fp8_e32 v[172:173], v118
	v_cvt_pk_f32_fp8_sdwa v[174:175], v118 src0_sel:WORD_1
	v_pk_fma_f32 v[184:185], v[172:173], s[10:11], v[184:185] op_sel_hi:[1,0,1]
	v_pk_fma_f32 v[186:187], v[174:175], s[10:11], v[186:187] op_sel_hi:[1,0,1]
	global_store_dwordx4 v250, v[184:187], s[4:5] offset:2048
	v_lshlrev_b32_e32 v188, 16, v238
	v_and_b32_e32 v189, 0xffff0000, v238
	v_lshlrev_b32_e32 v190, 16, v239
	v_and_b32_e32 v191, 0xffff0000, v239
	v_cvt_pk_f32_fp8_e32 v[160:161], v107
	v_cvt_pk_f32_fp8_sdwa v[162:163], v107 src0_sel:WORD_1
	v_pk_fma_f32 v[188:189], v[160:161], s[10:11], v[188:189] op_sel_hi:[1,0,1]
	v_pk_fma_f32 v[190:191], v[162:163], s[10:11], v[190:191] op_sel_hi:[1,0,1]
	v_cvt_pk_f32_fp8_e32 v[164:165], v111
	v_cvt_pk_f32_fp8_sdwa v[166:167], v111 src0_sel:WORD_1
	v_pk_fma_f32 v[188:189], v[164:165], s[10:11], v[188:189] op_sel_hi:[1,0,1]
	v_pk_fma_f32 v[190:191], v[166:167], s[10:11], v[190:191] op_sel_hi:[1,0,1]
	v_cvt_pk_f32_fp8_e32 v[168:169], v115
	v_cvt_pk_f32_fp8_sdwa v[170:171], v115 src0_sel:WORD_1
	v_pk_fma_f32 v[188:189], v[168:169], s[10:11], v[188:189] op_sel_hi:[1,0,1]
	v_pk_fma_f32 v[190:191], v[170:171], s[10:11], v[190:191] op_sel_hi:[1,0,1]
	v_cvt_pk_f32_fp8_e32 v[172:173], v119
	v_cvt_pk_f32_fp8_sdwa v[174:175], v119 src0_sel:WORD_1
	v_pk_fma_f32 v[188:189], v[172:173], s[10:11], v[188:189] op_sel_hi:[1,0,1]
	v_pk_fma_f32 v[190:191], v[174:175], s[10:11], v[190:191] op_sel_hi:[1,0,1]
	global_store_dwordx4 v250, v[188:191], s[4:5] offset:3072
	s_waitcnt vmcnt(12)
; __device__ __forceinline__ float bf_lo(unsigned w) { return __uint_as_float(w << 16); }
; __device__ __forceinline__ float bf_hi(unsigned w) { return __uint_as_float(w & 0xffff0000u); }
; __global__ void __launch_bounds__(512, 2) fwd_kernel(Params p) {
;     ...
;             for (int u = 0; u < UN; ++u) { const int it = it0 + u * NGT < NI ? it0 + u * NGT : it0; mm[u] = it >> 7; cc[u] = (it & 127) * 16;
;                 const i32x4 e4 = *(const i32x4*)(tok_e + mm[u] * 4), r4 = *(const i32x4*)(tok_rank + mm[u] * 4);
; #pragma unroll
;                 for (int k = 0; k < 4; ++k) { ee[u][k] = e4[k]; rk[u][k] = r4[k]; }
;                 const bf16_t* xp = X1 + (size_t)mm[u] * DM + cc[u]; xa[u] = *(const u32x4*)xp; xb[u] = *(const u32x4*)(xp + 8); }
; #pragma unroll
;             for (int u = 0; u < UN; ++u)
; #pragma unroll
;                 for (int k = 0; k < 4; ++k) { const int pos = ts[ee[u][k]] * 256 + rk[u][k]; y[u][k] = *(const u32x4*)(Yb + (size_t)pos * DM + cc[u]); }
; #pragma unroll
;             for (int u = 0; u < UN; ++u) {
;                 f32x4 a[4];
;                 a[0] = (f32x4){bf_lo(xa[u].x), bf_hi(xa[u].x), bf_lo(xa[u].y), bf_hi(xa[u].y)}; a[1] = (f32x4){bf_lo(xa[u].z), bf_hi(xa[u].z), bf_lo(xa[u].w), bf_hi(xa[u].w)};
;                 a[2] = (f32x4){bf_lo(xb[u].x), bf_hi(xb[u].x), bf_lo(xb[u].y), bf_hi(xb[u].y)}; a[3] = (f32x4){bf_lo(xb[u].z), bf_hi(xb[u].z), bf_lo(xb[u].w), bf_hi(xb[u].w)};
; #pragma unroll
;                 for (int k = 0; k < 4; ++k)
; #pragma unroll
;                     for (int q = 0; q < 4; ++q) { const f32x2 lo = __builtin_amdgcn_cvt_pk_f32_fp8((int)y[u][k][q], false), hi = __builtin_amdgcn_cvt_pk_f32_fp8((int)y[u][k][q], true);
;                         a[q].x += lo.x * (1.0f / Y8_SCALE); a[q].y += lo.y * (1.0f / Y8_SCALE); a[q].z += hi.x * (1.0f / Y8_SCALE); a[q].w += hi.y * (1.0f / Y8_SCALE); }
;                 if (it0 + u * NGT < NI) { float* op = p.out + (size_t)mm[u] * DM + cc[u];
; #pragma unroll
;                     for (int q = 0; q < 4; ++q) *(f32x4*)(op + 4 * q) = a[q]; }
	v_lshlrev_b32_e32 v176, 16, v240
	v_and_b32_e32 v177, 0xffff0000, v240
	v_lshlrev_b32_e32 v178, 16, v241
	v_and_b32_e32 v179, 0xffff0000, v241
	v_cvt_pk_f32_fp8_e32 v[160:161], v120
	v_cvt_pk_f32_fp8_sdwa v[162:163], v120 src0_sel:WORD_1
	v_pk_fma_f32 v[176:177], v[160:161], s[10:11], v[176:177] op_sel_hi:[1,0,1]
	v_pk_fma_f32 v[178:179], v[162:163], s[10:11], v[178:179] op_sel_hi:[1,0,1]
	v_cvt_pk_f32_fp8_e32 v[164:165], v124
	v_cvt_pk_f32_fp8_sdwa v[166:167], v124 src0_sel:WORD_1
	v_pk_fma_f32 v[176:177], v[164:165], s[10:11], v[176:177] op_sel_hi:[1,0,1]
	v_pk_fma_f32 v[178:179], v[166:167], s[10:11], v[178:179] op_sel_hi:[1,0,1]
	v_cvt_pk_f32_fp8_e32 v[168:169], v128
	v_cvt_pk_f32_fp8_sdwa v[170:171], v128 src0_sel:WORD_1
	v_pk_fma_f32 v[176:177], v[168:169], s[10:11], v[176:177] op_sel_hi:[1,0,1]
	v_pk_fma_f32 v[178:179], v[170:171], s[10:11], v[178:179] op_sel_hi:[1,0,1]
	v_cvt_pk_f32_fp8_e32 v[172:173], v132
	v_cvt_pk_f32_fp8_sdwa v[174:175], v132 src0_sel:WORD_1
	v_pk_fma_f32 v[176:177], v[172:173], s[10:11], v[176:177] op_sel_hi:[1,0,1]
	v_pk_fma_f32 v[178:179], v[174:175], s[10:11], v[178:179] op_sel_hi:[1,0,1]
	global_store_dwordx4 v251, v[176:179], s[4:5]
	v_lshlrev_b32_e32 v180, 16, v242
	v_and_b32_e32 v181, 0xffff0000, v242
	v_lshlrev_b32_e32 v182, 16, v243
	v_and_b32_e32 v183, 0xffff0000, v243
	v_cvt_pk_f32_fp8_e32 v[160:161], v121
	v_cvt_pk_f32_fp8_sdwa v[162:163], v121 src0_sel:WORD_1
	v_pk_fma_f32 v[180:181], v[160:161], s[10:11], v[180:181] op_sel_hi:[1,0,1]
	v_pk_fma_f32 v[182:183], v[162:163], s[10:11], v[182:183] op_sel_hi:[1,0,1]
	v_cvt_pk_f32_fp8_e32 v[164:165], v125
	v_cvt_pk_f32_fp8_sdwa v[166:167], v125 src0_sel:WORD_1
	v_pk_fma_f32 v[180:181], v[164:165], s[10:11], v[180:181] op_sel_hi:[1,0,1]
	v_pk_fma_f32 v[182:183], v[166:167], s[10:11], v[182:183] op_sel_hi:[1,0,1]
	v_cvt_pk_f32_fp8_e32 v[168:169], v129
	v_cvt_pk_f32_fp8_sdwa v[170:171], v129 src0_sel:WORD_1
	v_pk_fma_f32 v[180:181], v[168:169], s[10:11], v[180:181] op_sel_hi:[1,0,1]
	v_pk_fma_f32 v[182:183], v[170:171], s[10:11], v[182:183] op_sel_hi:[1,0,1]
	v_cvt_pk_f32_fp8_e32 v[172:173], v133
	v_cvt_pk_f32_fp8_sdwa v[174:175], v133 src0_sel:WORD_1
	v_pk_fma_f32 v[180:181], v[172:173], s[10:11], v[180:181] op_sel_hi:[1,0,1]
	v_pk_fma_f32 v[182:183], v[174:175], s[10:11], v[182:183] op_sel_hi:[1,0,1]
	global_store_dwordx4 v251, v[180:183], s[4:5] offset:1024
	v_lshlrev_b32_e32 v184, 16, v244
	v_and_b32_e32 v185, 0xffff0000, v244
	v_lshlrev_b32_e32 v186, 16, v245
	v_and_b32_e32 v187, 0xffff0000, v245
	v_cvt_pk_f32_fp8_e32 v[160:161], v122
	v_cvt_pk_f32_fp8_sdwa v[162:163], v122 src0_sel:WORD_1
	v_pk_fma_f32 v[184:185], v[160:161], s[10:11], v[184:185] op_sel_hi:[1,0,1]
	v_pk_fma_f32 v[186:187], v[162:163], s[10:11], v[186:187] op_sel_hi:[1,0,1]
	v_cvt_pk_f32_fp8_e32 v[164:165], v126
	v_cvt_pk_f32_fp8_sdwa v[166:167], v126 src0_sel:WORD_1
	v_pk_fma_f32 v[184:185], v[164:165], s[10:11], v[184:185] op_sel_hi:[1,0,1]
	v_pk_fma_f32 v[186:187], v[166:167], s[10:11], v[186:187] op_sel_hi:[1,0,1]
	v_cvt_pk_f32_fp8_e32 v[168:169], v130
	v_cvt_pk_f32_fp8_sdwa v[170:171], v130 src0_sel:WORD_1
	v_pk_fma_f32 v[184:185], v[168:169], s[10:11], v[184:185] op_sel_hi:[1,0,1]
	v_pk_fma_f32 v[186:187], v[170:171], s[10:11], v[186:187] op_sel_hi:[1,0,1]
	v_cvt_pk_f32_fp8_e32 v[172:173], v134
	v_cvt_pk_f32_fp8_sdwa v[174:175], v134 src0_sel:WORD_1
	v_pk_fma_f32 v[184:185], v[172:173], s[10:11], v[184:185] op_sel_hi:[1,0,1]
	v_pk_fma_f32 v[186:187], v[174:175], s[10:11], v[186:187] op_sel_hi:[1,0,1]
	global_store_dwordx4 v251, v[184:187], s[4:5] offset:2048
	v_lshlrev_b32_e32 v188, 16, v246
	v_and_b32_e32 v189, 0xffff0000, v246
	v_lshlrev_b32_e32 v190, 16, v247
	v_and_b32_e32 v191, 0xffff0000, v247
	v_cvt_pk_f32_fp8_e32 v[160:161], v123
	v_cvt_pk_f32_fp8_sdwa v[162:163], v123 src0_sel:WORD_1
	v_pk_fma_f32 v[188:189], v[160:161], s[10:11], v[188:189] op_sel_hi:[1,0,1]
	v_pk_fma_f32 v[190:191], v[162:163], s[10:11], v[190:191] op_sel_hi:[1,0,1]
	v_cvt_pk_f32_fp8_e32 v[164:165], v127
	v_cvt_pk_f32_fp8_sdwa v[166:167], v127 src0_sel:WORD_1
	v_pk_fma_f32 v[188:189], v[164:165], s[10:11], v[188:189] op_sel_hi:[1,0,1]
	v_pk_fma_f32 v[190:191], v[166:167], s[10:11], v[190:191] op_sel_hi:[1,0,1]
	v_cvt_pk_f32_fp8_e32 v[168:169], v131
	v_cvt_pk_f32_fp8_sdwa v[170:171], v131 src0_sel:WORD_1
	v_pk_fma_f32 v[188:189], v[168:169], s[10:11], v[188:189] op_sel_hi:[1,0,1]
	v_pk_fma_f32 v[190:191], v[170:171], s[10:11], v[190:191] op_sel_hi:[1,0,1]
	v_cvt_pk_f32_fp8_e32 v[172:173], v135
	v_cvt_pk_f32_fp8_sdwa v[174:175], v135 src0_sel:WORD_1
	v_pk_fma_f32 v[188:189], v[172:173], s[10:11], v[188:189] op_sel_hi:[1,0,1]
	v_pk_fma_f32 v[190:191], v[174:175], s[10:11], v[190:191] op_sel_hi:[1,0,1]
	global_store_dwordx4 v251, v[188:191], s[4:5] offset:3072
	s_branch .LBB0_1207
